# speedup vs baseline: 1.1035x; 1.0020x over previous
.LBB0_2:
	s_or_b64 exec, exec, s[14:15]
	s_load_dwordx2 s[0:1], s[0:1], 0x18
	v_lshrrev_b32_e32 v67, 5, v206
	v_or_b32_e32 v132, s11, v67
	s_lshl_b64 s[14:15], s[18:19], 14
	v_ashrrev_i32_e32 v133, 31, v132
	v_and_b32_e32 v124, 31, v0
	s_waitcnt lgkmcnt(0)
	s_add_u32 s14, s0, s14
	v_lshlrev_b64 v[2:3], 12, v[132:133]
	s_addc_u32 s15, s1, s15
	s_add_i32 s0, s7, 0x100
	v_lshl_add_u64 v[2:3], s[8:9], 0, v[2:3]
	v_lshlrev_b32_e32 v190, 4, v124
	v_mov_b32_e32 v191, 0
	s_and_b32 s26, s0, 0x300
	v_lshl_add_u64 v[130:131], v[2:3], 0, v[190:191]
	s_mov_b64 s[0:1], 0x30000
	v_lshl_add_u64 v[126:127], v[130:131], 0, s[0:1]
	s_mov_b64 s[0:1], 0x32000
	v_lshl_add_u64 v[128:129], v[130:131], 0, s[0:1]
	s_mov_b64 s[0:1], 0x34000
	v_lshl_add_u64 v[134:135], v[130:131], 0, s[0:1]
	s_mov_b64 s[0:1], 0x36000
	v_lshl_add_u64 v[136:137], v[130:131], 0, s[0:1]
	s_mov_b64 s[0:1], 0x38000
	v_lshl_add_u64 v[138:139], v[130:131], 0, s[0:1]
	s_mov_b64 s[0:1], 0x3a000
	v_lshl_add_u64 v[140:141], v[130:131], 0, s[0:1]
	s_mov_b64 s[0:1], 0x3c000
	s_or_b32 s24, s7, 0x80
	v_lshl_add_u64 v[142:143], v[130:131], 0, s[0:1]
	s_mov_b64 s[0:1], 0x3e000
	s_lshl_b32 s20, s7, 2
	v_lshl_add_u64 v[144:145], v[130:131], 0, s[0:1]
	s_lshl_b32 s8, s24, 2
	s_mov_b32 s9, s21
	v_lshl_add_u64 v[2:3], v[126:127], 0, s[20:21]
	v_lshl_add_u64 v[4:5], v[128:129], 0, s[20:21]
	v_lshl_add_u64 v[6:7], v[134:135], 0, s[20:21]
	v_lshl_add_u64 v[8:9], v[136:137], 0, s[20:21]
	v_lshl_add_u64 v[10:11], v[138:139], 0, s[20:21]
	v_lshl_add_u64 v[12:13], v[140:141], 0, s[20:21]
	v_lshl_add_u64 v[14:15], v[142:143], 0, s[20:21]
	v_lshl_add_u64 v[16:17], v[144:145], 0, s[20:21]
	v_lshl_add_u64 v[18:19], v[126:127], 0, s[8:9]
	v_lshl_add_u64 v[20:21], v[128:129], 0, s[8:9]
	v_lshl_add_u64 v[22:23], v[134:135], 0, s[8:9]
	v_lshl_add_u64 v[24:25], v[136:137], 0, s[8:9]
	s_lshl_b32 s0, s26, 2
	s_mov_b32 s1, s21
	v_lshl_add_u64 v[72:73], v[138:139], 0, s[8:9]
	v_lshl_add_u64 v[102:103], v[140:141], 0, s[8:9]
	v_lshl_add_u64 v[104:105], v[142:143], 0, s[8:9]
	v_lshl_add_u64 v[106:107], v[144:145], 0, s[8:9]
	v_lshl_add_u64 v[108:109], v[126:127], 0, s[0:1]
	v_lshl_add_u64 v[110:111], v[128:129], 0, s[0:1]
	v_lshl_add_u64 v[112:113], v[134:135], 0, s[0:1]
	v_lshl_add_u64 v[114:115], v[136:137], 0, s[0:1]
	v_lshl_add_u64 v[116:117], v[138:139], 0, s[0:1]
	v_lshl_add_u64 v[118:119], v[140:141], 0, s[0:1]
	v_lshl_add_u64 v[120:121], v[142:143], 0, s[0:1]
	v_lshl_add_u64 v[122:123], v[144:145], 0, s[0:1]
	global_load_dwordx4 v[68:71], v[2:3], off nt
	global_load_dwordx4 v[78:81], v[4:5], off nt
	global_load_dwordx4 v[82:85], v[6:7], off nt
	global_load_dwordx4 v[90:93], v[8:9], off nt
	global_load_dwordx4 v[98:101], v[10:11], off nt
	global_load_dwordx4 v[62:65], v[12:13], off nt
	global_load_dwordx4 v[54:57], v[14:15], off nt
	global_load_dwordx4 v[46:49], v[16:17], off nt
	global_load_dwordx4 v[94:97], v[18:19], off nt
	global_load_dwordx4 v[86:89], v[20:21], off nt
	global_load_dwordx4 v[74:77], v[22:23], off nt
	global_load_dwordx4 v[58:61], v[24:25], off nt
	global_load_dwordx4 v[50:53], v[72:73], off nt
	global_load_dwordx4 v[42:45], v[102:103], off nt
	global_load_dwordx4 v[38:41], v[104:105], off nt
	global_load_dwordx4 v[34:37], v[106:107], off nt
	global_load_dwordx4 v[30:33], v[108:109], off nt
	global_load_dwordx4 v[26:29], v[110:111], off nt
	s_nop 0
	global_load_dwordx4 v[22:25], v[112:113], off nt
	global_load_dwordx4 v[18:21], v[114:115], off nt
	global_load_dwordx4 v[14:17], v[116:117], off nt
	global_load_dwordx4 v[10:13], v[118:119], off nt
	global_load_dwordx4 v[6:9], v[120:121], off nt
	global_load_dwordx4 v[2:5], v[122:123], off nt
	s_waitcnt vmcnt(25)
	v_div_scale_f32 v72, s[22:23], v207, v207, 1.0
	v_rcp_f32_e32 v73, v72
	s_lshl_b32 s11, s10, 2
	s_mul_i32 s19, s35, 0x1100
	s_add_i32 s22, s11, 0x26600
	v_fma_f32 v103, -v72, v73, 1.0
	v_fmac_f32_e32 v73, v103, v73
	v_div_scale_f32 v103, vcc, 1.0, v207, 1.0
	v_mul_f32_e32 v104, v103, v73
	v_fma_f32 v105, -v72, v104, v103
	v_fmac_f32_e32 v104, v105, v73
	v_fma_f32 v72, -v72, v104, v103
	v_div_fmas_f32 v72, v72, v73, v104
	v_div_fixup_f32 v72, v72, v207, 1.0
	s_waitcnt vmcnt(24)
	v_fma_f32 v208, v72, v1, -v66
	v_lshl_add_u32 v1, v206, 2, s22
	s_add_i32 s19, s19, 0x22200
	ds_write_b32 v1, v72
	v_lshl_or_b32 v1, v124, 3, s19
	v_lshl_add_u32 v187, v67, 2, s22
	s_movk_i32 s22, 0x110
	v_mad_u32_u24 v186, v67, s22, v1
	s_add_i32 s22, s7, 0x180
	v_and_b32_e32 v102, 15, v0
	s_lshl_b32 s27, s34, 8
	s_and_b32 s25, s22, 0x380
	s_add_i32 s22, s7, 0x280
	v_lshlrev_b32_e32 v66, 2, v124
	v_mul_u32_u24_e32 v1, 0x110, v102
	v_and_b32_e32 v209, 48, v0
	s_and_b32 s23, s22, 0x380
	s_add_i32 s22, s7, 0x300
	v_mov_b32_e32 v67, 0x200
	s_addk_i32 s27, 0x380
	v_or_b32_e32 v133, s7, v66
	v_add3_u32 v1, s19, v1, v209
	s_lshl_b32 s19, s35, 15
	v_lshlrev_b32_e32 v210, 4, v206
	v_or_b32_e32 v189, s24, v66
	s_xor_b32 s24, s7, 0x200
	s_and_b32 s22, s22, 0x300
	v_bitop3_b32 v197, s7, v66, v67 bitop3:0xde
	s_and_b32 s7, s27, 0x380
	v_lshrrev_b32_e32 v185, 4, v206
	s_ashr_i32 s11, s10, 31
	v_or_b32_e32 v184, s19, v210
	v_or_b32_e32 v188, s26, v66
	v_or_b32_e32 v198, s25, v66
	v_or_b32_e32 v196, s23, v66
	v_or_b32_e32 v195, s22, v66
	v_or_b32_e32 v194, s7, v66
	v_mov_b32_e32 v102, v133
	v_and_b32_e32 v248, 2, v206
	v_cmp_ne_u32_e32 vcc, 0, v248
	v_mov_b32_e32 v249, 0x44444444
	v_mov_b32_e32 v250, 0xeeeeeeee
	s_nop 1
	v_cndmask_b32_e32 v223, v249, v250, vcc
	v_lshrrev_b32_e32 v248, 4, v206
	v_lshl_add_u32 v248, v248, 4, 1
	v_add_u32_e32 v249, 0, v248
	v_cvt_f32_u32_e32 v249, v249
	v_add_u32_e32 v250, 1, v248
	v_cvt_f32_u32_e32 v250, v250
	v_cvt_pk_bf16_f32 v232, v249, v250
	v_add_u32_e32 v249, 2, v248
	v_cvt_f32_u32_e32 v249, v249
	v_add_u32_e32 v250, 3, v248
	v_cvt_f32_u32_e32 v250, v250
	v_cvt_pk_bf16_f32 v233, v249, v250
	v_add_u32_e32 v249, 4, v248
	v_cvt_f32_u32_e32 v249, v249
	v_add_u32_e32 v250, 5, v248
	v_cvt_f32_u32_e32 v250, v250
	v_cvt_pk_bf16_f32 v234, v249, v250
	v_add_u32_e32 v249, 6, v248
	v_cvt_f32_u32_e32 v249, v249
	v_add_u32_e32 v250, 7, v248
	v_cvt_f32_u32_e32 v250, v250
	v_cvt_pk_bf16_f32 v235, v249, v250
	v_add_u32_e32 v249, 8, v248
	v_cvt_f32_u32_e32 v249, v249
	v_add_u32_e32 v250, 9, v248
	v_cvt_f32_u32_e32 v250, v250
	v_cvt_pk_bf16_f32 v236, v249, v250
	v_add_u32_e32 v249, 10, v248
	v_cvt_f32_u32_e32 v249, v249
	v_add_u32_e32 v250, 11, v248
	v_cvt_f32_u32_e32 v250, v250
	v_cvt_pk_bf16_f32 v237, v249, v250
	v_add_u32_e32 v249, 12, v248
	v_cvt_f32_u32_e32 v249, v249
	v_add_u32_e32 v250, 13, v248
	v_cvt_f32_u32_e32 v250, v250
	v_cvt_pk_bf16_f32 v238, v249, v250
	v_add_u32_e32 v249, 14, v248
	v_cvt_f32_u32_e32 v249, v249
	v_add_u32_e32 v250, 15, v248
	v_cvt_f32_u32_e32 v250, v250
	v_cvt_pk_bf16_f32 v239, v249, v250
	v_and_b32_e32 v248, 15, v206
	v_lshrrev_b32_e32 v249, 2, v248
	v_and_b32_e32 v250, 1, v248
	v_lshl_add_u32 v249, v249, 1, v250
	v_and_b32_e32 v250, 3, v249
	v_lshrrev_b32_e32 v251, 4, v206
	v_cmp_eq_u32_e32 vcc, v250, v251
	v_lshrrev_b32_e32 v249, 2, v249
	v_cmp_ne_u32_e64 s[78:79], 0, v249
	v_mov_b32_e32 v250, 0x3f80
	v_mov_b32_e32 v251, 0x3f800000
	s_nop 1
	v_cndmask_b32_e64 v250, v250, v251, s[78:79]
	v_cndmask_b32_e32 v252, 0, v250, vcc
	s_lshr_b32 s77, s19, 15
	s_mulk_i32 s77, 0x1100
	s_add_i32 s77, s77, 0x22200
	v_lshrrev_b32_e32 v248, 4, v206
	v_and_b32_e32 v249, 1, v248
	v_lshrrev_b32_e32 v250, 1, v248
	v_lshlrev_b32_e32 v249, 6, v249
	v_lshl_add_u32 v253, v250, 1, v249
	v_and_b32_e32 v248, 15, v206
	v_cmp_eq_u32_e64 s[78:79], 0, v248
	v_mov_b32_e32 v244, v252
	v_mov_b32_e32 v245, 0
	v_mov_b32_e32 v246, 0
	v_mov_b32_e32 v247, 0
	v_mov_b64_e32 v[240:241], 0
	v_mov_b64_e32 v[242:243], 0
	s_nop 1
	v_smfmac_f32_16x16x64_bf16 v[240:243], v[244:247], v[232:239], v223
	s_nop 15
	s_nop 3
	s_and_saveexec_b64 s[80:81], s[78:79]
	v_cvt_u32_f32_e32 v248, v240
	v_add_u32_e32 v248, -1, v248
	v_lshl_add_u32 v248, v248, 2, s77
	v_add_u32_e32 v249, 0, v253
	ds_write_b32 v248, v249
	v_cvt_u32_f32_e32 v248, v241
	v_add_u32_e32 v248, -1, v248
	v_lshl_add_u32 v248, v248, 2, s77
	v_add_u32_e32 v249, 32, v253
	ds_write_b32 v248, v249
	v_cvt_u32_f32_e32 v248, v242
	v_add_u32_e32 v248, -1, v248
	v_lshl_add_u32 v248, v248, 2, s77
	v_add_u32_e32 v249, 16, v253
	ds_write_b32 v248, v249
	v_cvt_u32_f32_e32 v248, v243
	v_add_u32_e32 v248, -1, v248
	v_lshl_add_u32 v248, v248, 2, s77
	v_add_u32_e32 v249, 48, v253
	ds_write_b32 v248, v249
	s_or_b64 exec, exec, s[80:81]
	v_mov_b32_e32 v244, 0
	v_mov_b32_e32 v245, v252
	v_mov_b32_e32 v246, 0
	v_mov_b32_e32 v247, 0
	v_mov_b64_e32 v[240:241], 0
	v_mov_b64_e32 v[242:243], 0
	s_nop 1
	v_smfmac_f32_16x16x64_bf16 v[240:243], v[244:247], v[232:239], v223
	s_nop 15
	s_nop 3
	s_and_saveexec_b64 s[80:81], s[78:79]
	v_cvt_u32_f32_e32 v248, v240
	v_add_u32_e32 v248, -1, v248
	v_lshl_add_u32 v248, v248, 2, s77
	v_add_u32_e32 v249, 4, v253
	ds_write_b32 v248, v249
	v_cvt_u32_f32_e32 v248, v241
	v_add_u32_e32 v248, -1, v248
	v_lshl_add_u32 v248, v248, 2, s77
	v_add_u32_e32 v249, 36, v253
	ds_write_b32 v248, v249
	v_cvt_u32_f32_e32 v248, v242
	v_add_u32_e32 v248, -1, v248
	v_lshl_add_u32 v248, v248, 2, s77
	v_add_u32_e32 v249, 20, v253
	ds_write_b32 v248, v249
	v_cvt_u32_f32_e32 v248, v243
	v_add_u32_e32 v248, -1, v248
	v_lshl_add_u32 v248, v248, 2, s77
	v_add_u32_e32 v249, 52, v253
	ds_write_b32 v248, v249
	s_or_b64 exec, exec, s[80:81]
	v_mov_b32_e32 v244, 0
	v_mov_b32_e32 v245, 0
	v_mov_b32_e32 v246, v252
	v_mov_b32_e32 v247, 0
	v_mov_b64_e32 v[240:241], 0
	v_mov_b64_e32 v[242:243], 0
	s_nop 1
	v_smfmac_f32_16x16x64_bf16 v[240:243], v[244:247], v[232:239], v223
	s_nop 15
	s_nop 3
	s_and_saveexec_b64 s[80:81], s[78:79]
	v_cvt_u32_f32_e32 v248, v240
	v_add_u32_e32 v248, -1, v248
	v_lshl_add_u32 v248, v248, 2, s77
	v_add_u32_e32 v249, 8, v253
	ds_write_b32 v248, v249
	v_cvt_u32_f32_e32 v248, v241
	v_add_u32_e32 v248, -1, v248
	v_lshl_add_u32 v248, v248, 2, s77
	v_add_u32_e32 v249, 40, v253
	ds_write_b32 v248, v249
	v_cvt_u32_f32_e32 v248, v242
	v_add_u32_e32 v248, -1, v248
	v_lshl_add_u32 v248, v248, 2, s77
	v_add_u32_e32 v249, 24, v253
	ds_write_b32 v248, v249
	v_cvt_u32_f32_e32 v248, v243
	v_add_u32_e32 v248, -1, v248
	v_lshl_add_u32 v248, v248, 2, s77
	v_add_u32_e32 v249, 56, v253
	ds_write_b32 v248, v249
	s_or_b64 exec, exec, s[80:81]
	v_mov_b32_e32 v244, 0
	v_mov_b32_e32 v245, 0
	v_mov_b32_e32 v246, 0
	v_mov_b32_e32 v247, v252
	v_mov_b64_e32 v[240:241], 0
	v_mov_b64_e32 v[242:243], 0
	s_nop 1
	v_smfmac_f32_16x16x64_bf16 v[240:243], v[244:247], v[232:239], v223
	s_nop 15
	s_nop 3
	s_and_saveexec_b64 s[80:81], s[78:79]
	v_cvt_u32_f32_e32 v248, v240
	v_add_u32_e32 v248, -1, v248
	v_lshl_add_u32 v248, v248, 2, s77
	v_add_u32_e32 v249, 12, v253
	ds_write_b32 v248, v249
	v_cvt_u32_f32_e32 v248, v241
	v_add_u32_e32 v248, -1, v248
	v_lshl_add_u32 v248, v248, 2, s77
	v_add_u32_e32 v249, 44, v253
	ds_write_b32 v248, v249
	v_cvt_u32_f32_e32 v248, v242
	v_add_u32_e32 v248, -1, v248
	v_lshl_add_u32 v248, v248, 2, s77
	v_add_u32_e32 v249, 28, v253
	ds_write_b32 v248, v249
	v_cvt_u32_f32_e32 v248, v243
	v_add_u32_e32 v248, -1, v248
	v_lshl_add_u32 v248, v248, 2, s77
	v_add_u32_e32 v249, 60, v253
	ds_write_b32 v248, v249
	s_or_b64 exec, exec, s[80:81]
	v_bfe_u32 v248, v206, 3, 2
	v_lshrrev_b32_e32 v249, 5, v206
	v_lshlrev_b32_e32 v248, 4, v248
	v_lshl_or_b32 v248, v249, 3, v248
	v_and_b32_e32 v249, 7, v206
	v_or_b32_e32 v248, v248, v249
	v_lshl_add_u32 v248, v248, 2, s77
	s_waitcnt lgkmcnt(0)
	ds_read_b32 v254, v248
	v_and_b32_e32 v248, 15, v206
	v_bfe_u32 v249, v248, 1, 2
	v_lshrrev_b32_e32 v250, 3, v248
	v_lshlrev_b32_e32 v249, 4, v249
	v_lshl_or_b32 v249, v250, 3, v249
	v_and_b32_e32 v250, 1, v248
	v_lshl_or_b32 v249, v250, 2, v249
	v_lshl_add_u32 v249, v249, 2, s77
	ds_read_b128 v[248:251], v249
	s_lshr_b32 s76, s19, 6
	s_add_i32 s76, s76, 0x20000
	v_lshrrev_b32_e32 v252, 4, v206
	v_lshl_add_u32 v252, v252, 7, s76
	s_waitcnt lgkmcnt(0)
	v_add_u32_e32 v248, v252, v248
	v_add_u32_e32 v249, v252, v249
	v_add_u32_e32 v250, v252, v250
	v_add_u32_e32 v251, v252, v251
	v_cvt_pk_bf16_f32 v236, v224, v225
	v_cvt_pk_bf16_f32 v237, v226, v227
	v_lshlrev_b32_e32 v238, 16, v236
	v_and_b32_e32 v239, 0xffff0000, v236
	v_lshlrev_b32_e32 v240, 16, v237
	v_and_b32_e32 v241, 0xffff0000, v237
	v_sub_f32_e32 v238, v224, v238
	v_sub_f32_e32 v239, v225, v239
	v_sub_f32_e32 v240, v226, v240
	v_sub_f32_e32 v241, v227, v241
	v_cvt_pk_bf16_f32 v238, v238, v239
	v_cvt_pk_bf16_f32 v239, v240, v241
	ds_write_b16 v248, v236
	ds_write_b16_d16_hi v249, v236
	ds_write_b16 v250, v237
	ds_write_b16_d16_hi v251, v237
	ds_write_b16 v248, v238 offset:2176
	ds_write_b16_d16_hi v249, v238 offset:2176
	ds_write_b16 v250, v239 offset:2176
	ds_write_b16_d16_hi v251, v239 offset:2176
	s_waitcnt vmcnt(23)
	s_waitcnt vmcnt(22)
	s_waitcnt vmcnt(21)
	s_waitcnt vmcnt(20)
	s_waitcnt vmcnt(19)
	s_waitcnt vmcnt(18)
	s_waitcnt vmcnt(17)
	s_waitcnt vmcnt(16)
	ds_read_b32 v66, v187 offset:192
	v_or_b32_e32 v103, 48, v132
	v_add_u32_e32 v104, 1, v102
	v_cmp_eq_u32_e32 vcc, v102, v103
	v_add_u32_e32 v105, 3, v102
	v_add_u32_e32 v106, 2, v102
	v_cndmask_b32_e64 v72, 0, 1.0, vcc
	v_cmp_eq_u32_e32 vcc, v104, v103
	v_or_b32_e32 v107, 50, v132
	v_or_b32_e32 v108, 52, v132
	v_cndmask_b32_e64 v73, 0, 1.0, vcc
	v_cmp_eq_u32_e32 vcc, v105, v103
	s_waitcnt lgkmcnt(0)
	v_pk_fma_f32 v[68:69], v[66:67], v[68:69], v[72:73] op_sel_hi:[0,1,1] neg_lo:[1,0,0] neg_hi:[1,0,0]
	v_cvt_pk_bf16_f32 v68, v68, v69
	v_cndmask_b32_e64 v73, 0, 1.0, vcc
	v_cmp_eq_u32_e32 vcc, v106, v103
	v_or_b32_e32 v109, 54, v132
	v_or_b32_e32 v110, 56, v132
	v_cndmask_b32_e64 v72, 0, 1.0, vcc
	v_pk_fma_f32 v[66:67], v[66:67], v[70:71], v[72:73] op_sel_hi:[0,1,1] neg_lo:[1,0,0] neg_hi:[1,0,0]
	v_cvt_pk_bf16_f32 v69, v66, v67
	ds_write_b64 v186, v[68:69]
	ds_read_b32 v66, v187 offset:200
	v_cmp_eq_u32_e32 vcc, v102, v107
	v_or_b32_e32 v111, 58, v132
	v_or_b32_e32 v112, 60, v132
	v_cndmask_b32_e64 v68, 0, 1.0, vcc
	v_cmp_eq_u32_e32 vcc, v104, v107
	v_or_b32_e32 v113, 62, v132
	v_or_b32_e32 v193, 2, v132
	v_cndmask_b32_e64 v69, 0, 1.0, vcc
	v_cmp_eq_u32_e32 vcc, v105, v107
	s_waitcnt lgkmcnt(0)
	v_pk_fma_f32 v[68:69], v[66:67], v[78:79], v[68:69] op_sel_hi:[0,1,1] neg_lo:[1,0,0] neg_hi:[1,0,0]
	v_cvt_pk_bf16_f32 v68, v68, v69
	v_cndmask_b32_e64 v71, 0, 1.0, vcc
	v_cmp_eq_u32_e32 vcc, v106, v107
	v_or_b32_e32 v192, 4, v132
	v_or_b32_e32 v190, 6, v132
	v_cndmask_b32_e64 v70, 0, 1.0, vcc
	v_pk_fma_f32 v[66:67], v[66:67], v[80:81], v[70:71] op_sel_hi:[0,1,1] neg_lo:[1,0,0] neg_hi:[1,0,0]
	v_cvt_pk_bf16_f32 v69, v66, v67
	ds_write_b64 v186, v[68:69] offset:544
	ds_read_b32 v66, v187 offset:208
	v_cmp_eq_u32_e32 vcc, v102, v108
	v_or_b32_e32 v149, 8, v132
	v_or_b32_e32 v148, 10, v132
	v_cndmask_b32_e64 v68, 0, 1.0, vcc
	v_cmp_eq_u32_e32 vcc, v104, v108
	v_or_b32_e32 v147, 12, v132
	v_or_b32_e32 v146, 14, v132
	v_cndmask_b32_e64 v69, 0, 1.0, vcc
	v_cmp_eq_u32_e32 vcc, v105, v108
	s_waitcnt lgkmcnt(0)
	v_pk_fma_f32 v[68:69], v[66:67], v[82:83], v[68:69] op_sel_hi:[0,1,1] neg_lo:[1,0,0] neg_hi:[1,0,0]
	v_cvt_pk_bf16_f32 v68, v68, v69
	v_cndmask_b32_e64 v71, 0, 1.0, vcc
	v_cmp_eq_u32_e32 vcc, v106, v108
	s_nop 1
	v_cndmask_b32_e64 v70, 0, 1.0, vcc
	v_pk_fma_f32 v[66:67], v[66:67], v[84:85], v[70:71] op_sel_hi:[0,1,1] neg_lo:[1,0,0] neg_hi:[1,0,0]
	v_cvt_pk_bf16_f32 v69, v66, v67
	ds_write_b64 v186, v[68:69] offset:1088
	ds_read_b32 v66, v187 offset:216
	v_cmp_eq_u32_e32 vcc, v102, v109
	s_nop 1
	v_cndmask_b32_e64 v68, 0, 1.0, vcc
	v_cmp_eq_u32_e32 vcc, v104, v109
	s_nop 1
	v_cndmask_b32_e64 v69, 0, 1.0, vcc
	v_cmp_eq_u32_e32 vcc, v105, v109
	s_waitcnt lgkmcnt(0)
	v_pk_fma_f32 v[68:69], v[66:67], v[90:91], v[68:69] op_sel_hi:[0,1,1] neg_lo:[1,0,0] neg_hi:[1,0,0]
	v_cvt_pk_bf16_f32 v68, v68, v69
	v_cndmask_b32_e64 v71, 0, 1.0, vcc
	v_cmp_eq_u32_e32 vcc, v106, v109
	s_nop 1
	v_cndmask_b32_e64 v70, 0, 1.0, vcc
	v_pk_fma_f32 v[66:67], v[66:67], v[92:93], v[70:71] op_sel_hi:[0,1,1] neg_lo:[1,0,0] neg_hi:[1,0,0]
	v_cvt_pk_bf16_f32 v69, v66, v67
	ds_write_b64 v186, v[68:69] offset:1632
	ds_read_b32 v66, v187 offset:224
	v_cmp_eq_u32_e32 vcc, v102, v110
	s_nop 1
	v_cndmask_b32_e64 v68, 0, 1.0, vcc
	v_cmp_eq_u32_e32 vcc, v104, v110
	s_nop 1
	v_cndmask_b32_e64 v69, 0, 1.0, vcc
	v_cmp_eq_u32_e32 vcc, v105, v110
	s_waitcnt lgkmcnt(0)
	v_pk_fma_f32 v[68:69], v[66:67], v[98:99], v[68:69] op_sel_hi:[0,1,1] neg_lo:[1,0,0] neg_hi:[1,0,0]
	v_cvt_pk_bf16_f32 v68, v68, v69
	v_cndmask_b32_e64 v71, 0, 1.0, vcc
	v_cmp_eq_u32_e32 vcc, v106, v110
	s_nop 1
	v_cndmask_b32_e64 v70, 0, 1.0, vcc
	v_pk_fma_f32 v[66:67], v[66:67], v[100:101], v[70:71] op_sel_hi:[0,1,1] neg_lo:[1,0,0] neg_hi:[1,0,0]
	v_cvt_pk_bf16_f32 v69, v66, v67
	ds_write_b64 v186, v[68:69] offset:2176
	ds_read_b32 v66, v187 offset:232
	v_cmp_eq_u32_e32 vcc, v102, v111
	s_nop 1
	v_cndmask_b32_e64 v68, 0, 1.0, vcc
	v_cmp_eq_u32_e32 vcc, v104, v111
	s_nop 1
	v_cndmask_b32_e64 v69, 0, 1.0, vcc
	v_cmp_eq_u32_e32 vcc, v105, v111
	s_waitcnt lgkmcnt(0)
	v_pk_fma_f32 v[62:63], v[66:67], v[62:63], v[68:69] op_sel_hi:[0,1,1] neg_lo:[1,0,0] neg_hi:[1,0,0]
	v_cvt_pk_bf16_f32 v62, v62, v63
	v_cndmask_b32_e64 v69, 0, 1.0, vcc
	v_cmp_eq_u32_e32 vcc, v106, v111
	s_nop 1
	v_cndmask_b32_e64 v68, 0, 1.0, vcc
	v_pk_fma_f32 v[64:65], v[66:67], v[64:65], v[68:69] op_sel_hi:[0,1,1] neg_lo:[1,0,0] neg_hi:[1,0,0]
	v_cvt_pk_bf16_f32 v63, v64, v65
	ds_write_b64 v186, v[62:63] offset:2720
	ds_read_b32 v62, v187 offset:240
	v_cmp_eq_u32_e32 vcc, v102, v112
	s_nop 1
	v_cndmask_b32_e64 v64, 0, 1.0, vcc
	v_cmp_eq_u32_e32 vcc, v104, v112
	s_nop 1
	v_cndmask_b32_e64 v65, 0, 1.0, vcc
	v_cmp_eq_u32_e32 vcc, v105, v112
	s_waitcnt lgkmcnt(0)
	v_pk_fma_f32 v[54:55], v[62:63], v[54:55], v[64:65] op_sel_hi:[0,1,1] neg_lo:[1,0,0] neg_hi:[1,0,0]
	v_cvt_pk_bf16_f32 v54, v54, v55
	v_cndmask_b32_e64 v65, 0, 1.0, vcc
	v_cmp_eq_u32_e32 vcc, v106, v112
	s_nop 1
	v_cndmask_b32_e64 v64, 0, 1.0, vcc
	v_pk_fma_f32 v[56:57], v[62:63], v[56:57], v[64:65] op_sel_hi:[0,1,1] neg_lo:[1,0,0] neg_hi:[1,0,0]
	v_cvt_pk_bf16_f32 v55, v56, v57
	ds_write_b64 v186, v[54:55] offset:3264
	ds_read_b32 v54, v187 offset:248
	v_cmp_eq_u32_e32 vcc, v102, v113
	s_nop 1
	v_cndmask_b32_e64 v56, 0, 1.0, vcc
	v_cmp_eq_u32_e32 vcc, v104, v113
	s_nop 1
	v_cndmask_b32_e64 v57, 0, 1.0, vcc
	v_cmp_eq_u32_e32 vcc, v105, v113
	s_waitcnt lgkmcnt(0)
	v_pk_fma_f32 v[46:47], v[54:55], v[46:47], v[56:57] op_sel_hi:[0,1,1] neg_lo:[1,0,0] neg_hi:[1,0,0]
	v_cvt_pk_bf16_f32 v46, v46, v47
	v_cndmask_b32_e64 v57, 0, 1.0, vcc
	v_cmp_eq_u32_e32 vcc, v106, v113
	s_nop 1
	v_cndmask_b32_e64 v56, 0, 1.0, vcc
	v_pk_fma_f32 v[48:49], v[54:55], v[48:49], v[56:57] op_sel_hi:[0,1,1] neg_lo:[1,0,0] neg_hi:[1,0,0]
	v_cvt_pk_bf16_f32 v47, v48, v49
	ds_write_b64 v186, v[46:47] offset:3808
	ds_read_b128 v[46:49], v1
	s_waitcnt lgkmcnt(0)
	ds_write_b128 v184, v[46:49]
	ds_read_b128 v[46:49], v1 offset:64
	s_waitcnt lgkmcnt(0)
	ds_write_b128 v184, v[46:49] offset:1024
	ds_read_b128 v[46:49], v1 offset:128
	s_waitcnt lgkmcnt(0)
	ds_write_b128 v184, v[46:49] offset:2048
	ds_read_b128 v[46:49], v1 offset:192
	s_waitcnt lgkmcnt(0)
	ds_write_b128 v184, v[46:49] offset:3072
	s_lshl_b32 s30, s25, 2
	s_mov_b32 s31, s21
	v_lshl_add_u64 v[46:47], v[126:127], 0, s[30:31]
	v_lshl_add_u64 v[48:49], v[128:129], 0, s[30:31]
	v_lshl_add_u64 v[54:55], v[134:135], 0, s[30:31]
	v_lshl_add_u64 v[56:57], v[136:137], 0, s[30:31]
	v_lshl_add_u64 v[62:63], v[138:139], 0, s[30:31]
	v_lshl_add_u64 v[64:65], v[140:141], 0, s[30:31]
	v_lshl_add_u64 v[98:99], v[142:143], 0, s[30:31]
	v_lshl_add_u64 v[100:101], v[144:145], 0, s[30:31]
	global_load_dwordx4 v[90:93], v[46:47], off nt
	global_load_dwordx4 v[82:85], v[48:49], off nt
	global_load_dwordx4 v[78:81], v[54:55], off nt
	global_load_dwordx4 v[70:73], v[56:57], off nt
	global_load_dwordx4 v[66:69], v[62:63], off nt
	s_nop 0
	global_load_dwordx4 v[62:65], v[64:65], off nt
	s_nop 0
	global_load_dwordx4 v[54:57], v[98:99], off nt
	global_load_dwordx4 v[46:49], v[100:101], off nt
	v_mov_b32_e32 v99, v189
	s_waitcnt vmcnt(23)
	s_waitcnt vmcnt(22)
	s_waitcnt vmcnt(21)
	s_waitcnt vmcnt(20)
	s_waitcnt vmcnt(19)
	s_waitcnt vmcnt(18)
	s_waitcnt vmcnt(17)
	s_waitcnt vmcnt(16)
	ds_read_b32 v98, v187 offset:192
	v_add_u32_e32 v102, 1, v99
	v_cmp_eq_u32_e32 vcc, v99, v103
	v_add_u32_e32 v104, 3, v99
	v_add_u32_e32 v105, 2, v99
	v_cndmask_b32_e64 v100, 0, 1.0, vcc
	v_cmp_eq_u32_e32 vcc, v102, v103
	s_nop 1
	v_cndmask_b32_e64 v101, 0, 1.0, vcc
	v_cmp_eq_u32_e32 vcc, v104, v103
	s_waitcnt lgkmcnt(0)
	v_pk_fma_f32 v[94:95], v[98:99], v[94:95], v[100:101] op_sel_hi:[0,1,1] neg_lo:[1,0,0] neg_hi:[1,0,0]
	v_cvt_pk_bf16_f32 v94, v94, v95
	v_cndmask_b32_e64 v101, 0, 1.0, vcc
	v_cmp_eq_u32_e32 vcc, v105, v103
	s_nop 1
	v_cndmask_b32_e64 v100, 0, 1.0, vcc
	v_pk_fma_f32 v[96:97], v[98:99], v[96:97], v[100:101] op_sel_hi:[0,1,1] neg_lo:[1,0,0] neg_hi:[1,0,0]
	v_cvt_pk_bf16_f32 v95, v96, v97
	ds_write_b64 v186, v[94:95]
	ds_read_b32 v94, v187 offset:200
	v_cmp_eq_u32_e32 vcc, v99, v107
	s_nop 1
	v_cndmask_b32_e64 v96, 0, 1.0, vcc
	v_cmp_eq_u32_e32 vcc, v102, v107
	s_nop 1
	v_cndmask_b32_e64 v97, 0, 1.0, vcc
	v_cmp_eq_u32_e32 vcc, v104, v107
	s_waitcnt lgkmcnt(0)
	v_pk_fma_f32 v[86:87], v[94:95], v[86:87], v[96:97] op_sel_hi:[0,1,1] neg_lo:[1,0,0] neg_hi:[1,0,0]
	v_cvt_pk_bf16_f32 v86, v86, v87
	v_cndmask_b32_e64 v97, 0, 1.0, vcc
	v_cmp_eq_u32_e32 vcc, v105, v107
	s_nop 1
	v_cndmask_b32_e64 v96, 0, 1.0, vcc
	v_pk_fma_f32 v[88:89], v[94:95], v[88:89], v[96:97] op_sel_hi:[0,1,1] neg_lo:[1,0,0] neg_hi:[1,0,0]
	v_cvt_pk_bf16_f32 v87, v88, v89
	ds_write_b64 v186, v[86:87] offset:544
	ds_read_b32 v86, v187 offset:208
	v_cmp_eq_u32_e32 vcc, v99, v108
	s_nop 1
	v_cndmask_b32_e64 v88, 0, 1.0, vcc
	v_cmp_eq_u32_e32 vcc, v102, v108
	s_nop 1
	v_cndmask_b32_e64 v89, 0, 1.0, vcc
	v_cmp_eq_u32_e32 vcc, v104, v108
	s_waitcnt lgkmcnt(0)
	v_pk_fma_f32 v[74:75], v[86:87], v[74:75], v[88:89] op_sel_hi:[0,1,1] neg_lo:[1,0,0] neg_hi:[1,0,0]
	v_cvt_pk_bf16_f32 v74, v74, v75
	v_cndmask_b32_e64 v89, 0, 1.0, vcc
	v_cmp_eq_u32_e32 vcc, v105, v108
	s_nop 1
	v_cndmask_b32_e64 v88, 0, 1.0, vcc
	v_pk_fma_f32 v[76:77], v[86:87], v[76:77], v[88:89] op_sel_hi:[0,1,1] neg_lo:[1,0,0] neg_hi:[1,0,0]
	v_cvt_pk_bf16_f32 v75, v76, v77
	ds_write_b64 v186, v[74:75] offset:1088
	ds_read_b32 v74, v187 offset:216
	v_cmp_eq_u32_e32 vcc, v99, v109
	s_nop 1
	v_cndmask_b32_e64 v76, 0, 1.0, vcc
	v_cmp_eq_u32_e32 vcc, v102, v109
	s_nop 1
	v_cndmask_b32_e64 v77, 0, 1.0, vcc
	v_cmp_eq_u32_e32 vcc, v104, v109
	s_waitcnt lgkmcnt(0)
	v_pk_fma_f32 v[58:59], v[74:75], v[58:59], v[76:77] op_sel_hi:[0,1,1] neg_lo:[1,0,0] neg_hi:[1,0,0]
	v_cvt_pk_bf16_f32 v58, v58, v59
	v_cndmask_b32_e64 v77, 0, 1.0, vcc
	v_cmp_eq_u32_e32 vcc, v105, v109
	s_nop 1
	v_cndmask_b32_e64 v76, 0, 1.0, vcc
	v_pk_fma_f32 v[60:61], v[74:75], v[60:61], v[76:77] op_sel_hi:[0,1,1] neg_lo:[1,0,0] neg_hi:[1,0,0]
	v_cvt_pk_bf16_f32 v59, v60, v61
	ds_write_b64 v186, v[58:59] offset:1632
	ds_read_b32 v58, v187 offset:224
	v_cmp_eq_u32_e32 vcc, v99, v110
	s_nop 1
	v_cndmask_b32_e64 v60, 0, 1.0, vcc
	v_cmp_eq_u32_e32 vcc, v102, v110
	s_nop 1
	v_cndmask_b32_e64 v61, 0, 1.0, vcc
	v_cmp_eq_u32_e32 vcc, v104, v110
	s_waitcnt lgkmcnt(0)
	v_pk_fma_f32 v[50:51], v[58:59], v[50:51], v[60:61] op_sel_hi:[0,1,1] neg_lo:[1,0,0] neg_hi:[1,0,0]
	v_cvt_pk_bf16_f32 v50, v50, v51
	v_cndmask_b32_e64 v61, 0, 1.0, vcc
	v_cmp_eq_u32_e32 vcc, v105, v110
	s_nop 1
	v_cndmask_b32_e64 v60, 0, 1.0, vcc
	v_pk_fma_f32 v[52:53], v[58:59], v[52:53], v[60:61] op_sel_hi:[0,1,1] neg_lo:[1,0,0] neg_hi:[1,0,0]
	v_cvt_pk_bf16_f32 v51, v52, v53
	ds_write_b64 v186, v[50:51] offset:2176
	ds_read_b32 v50, v187 offset:232
	v_cmp_eq_u32_e32 vcc, v99, v111
	s_nop 1
	v_cndmask_b32_e64 v52, 0, 1.0, vcc
	v_cmp_eq_u32_e32 vcc, v102, v111
	s_nop 1
	v_cndmask_b32_e64 v53, 0, 1.0, vcc
	v_cmp_eq_u32_e32 vcc, v104, v111
	s_waitcnt lgkmcnt(0)
	v_pk_fma_f32 v[42:43], v[50:51], v[42:43], v[52:53] op_sel_hi:[0,1,1] neg_lo:[1,0,0] neg_hi:[1,0,0]
	v_cvt_pk_bf16_f32 v42, v42, v43
	v_cndmask_b32_e64 v53, 0, 1.0, vcc
	v_cmp_eq_u32_e32 vcc, v105, v111
	s_nop 1
	v_cndmask_b32_e64 v52, 0, 1.0, vcc
	v_pk_fma_f32 v[44:45], v[50:51], v[44:45], v[52:53] op_sel_hi:[0,1,1] neg_lo:[1,0,0] neg_hi:[1,0,0]
	v_cvt_pk_bf16_f32 v43, v44, v45
	ds_write_b64 v186, v[42:43] offset:2720
	ds_read_b32 v42, v187 offset:240
	v_cmp_eq_u32_e32 vcc, v99, v112
	s_nop 1
	v_cndmask_b32_e64 v44, 0, 1.0, vcc
	v_cmp_eq_u32_e32 vcc, v102, v112
	s_nop 1
	v_cndmask_b32_e64 v45, 0, 1.0, vcc
	v_cmp_eq_u32_e32 vcc, v104, v112
	s_waitcnt lgkmcnt(0)
	v_pk_fma_f32 v[38:39], v[42:43], v[38:39], v[44:45] op_sel_hi:[0,1,1] neg_lo:[1,0,0] neg_hi:[1,0,0]
	v_cvt_pk_bf16_f32 v38, v38, v39
	v_cndmask_b32_e64 v45, 0, 1.0, vcc
	v_cmp_eq_u32_e32 vcc, v105, v112
	s_nop 1
	v_cndmask_b32_e64 v44, 0, 1.0, vcc
	v_pk_fma_f32 v[40:41], v[42:43], v[40:41], v[44:45] op_sel_hi:[0,1,1] neg_lo:[1,0,0] neg_hi:[1,0,0]
	v_cvt_pk_bf16_f32 v39, v40, v41
	ds_write_b64 v186, v[38:39] offset:3264
	ds_read_b32 v38, v187 offset:248
	v_cmp_eq_u32_e32 vcc, v99, v113
	s_nop 1
	v_cndmask_b32_e64 v40, 0, 1.0, vcc
	v_cmp_eq_u32_e32 vcc, v102, v113
	s_nop 1
	v_cndmask_b32_e64 v41, 0, 1.0, vcc
	v_cmp_eq_u32_e32 vcc, v104, v113
	s_waitcnt lgkmcnt(0)
	v_pk_fma_f32 v[34:35], v[38:39], v[34:35], v[40:41] op_sel_hi:[0,1,1] neg_lo:[1,0,0] neg_hi:[1,0,0]
	v_cvt_pk_bf16_f32 v34, v34, v35
	v_cndmask_b32_e64 v41, 0, 1.0, vcc
	v_cmp_eq_u32_e32 vcc, v105, v113
	s_nop 1
	v_cndmask_b32_e64 v40, 0, 1.0, vcc
	v_pk_fma_f32 v[36:37], v[38:39], v[36:37], v[40:41] op_sel_hi:[0,1,1] neg_lo:[1,0,0] neg_hi:[1,0,0]
	v_cvt_pk_bf16_f32 v35, v36, v37
	ds_write_b64 v186, v[34:35] offset:3808
	ds_read_b128 v[34:37], v1
	s_waitcnt lgkmcnt(0)
	ds_write_b128 v184, v[34:37] offset:4096
	ds_read_b128 v[34:37], v1 offset:64
	s_waitcnt lgkmcnt(0)
	ds_write_b128 v184, v[34:37] offset:5120
	ds_read_b128 v[34:37], v1 offset:128
	s_waitcnt lgkmcnt(0)
	ds_write_b128 v184, v[34:37] offset:6144
	ds_read_b128 v[34:37], v1 offset:192
	s_waitcnt lgkmcnt(0)
	ds_write_b128 v184, v[34:37] offset:7168
	s_lshl_b32 s28, s24, 2
	s_mov_b32 s29, s21
	v_lshl_add_u64 v[34:35], v[126:127], 0, s[28:29]
	v_lshl_add_u64 v[36:37], v[128:129], 0, s[28:29]
	v_lshl_add_u64 v[38:39], v[134:135], 0, s[28:29]
	v_lshl_add_u64 v[40:41], v[136:137], 0, s[28:29]
	v_lshl_add_u64 v[42:43], v[138:139], 0, s[28:29]
	v_lshl_add_u64 v[44:45], v[140:141], 0, s[28:29]
	v_lshl_add_u64 v[50:51], v[142:143], 0, s[28:29]
	v_lshl_add_u64 v[52:53], v[144:145], 0, s[28:29]
	global_load_dwordx4 v[122:125], v[34:35], off nt
	global_load_dwordx4 v[114:117], v[36:37], off nt
	global_load_dwordx4 v[106:109], v[38:39], off nt
	global_load_dwordx4 v[86:89], v[40:41], off nt
	global_load_dwordx4 v[74:77], v[42:43], off nt
	s_nop 0
	global_load_dwordx4 v[42:45], v[44:45], off nt
	s_nop 0
	global_load_dwordx4 v[38:41], v[50:51], off nt
	global_load_dwordx4 v[34:37], v[52:53], off nt
	v_mov_b32_e32 v50, v188
	s_waitcnt vmcnt(23)
	s_waitcnt vmcnt(22)
	s_waitcnt vmcnt(21)
	s_waitcnt vmcnt(20)
	s_waitcnt vmcnt(19)
	s_waitcnt vmcnt(18)
	s_waitcnt vmcnt(17)
	s_waitcnt vmcnt(16)
	ds_read_b32 v50, v187 offset:192
	s_waitcnt lgkmcnt(0)
	v_pk_fma_f32 v[30:31], v[50:51], v[30:31], 0 op_sel_hi:[0,1,0] neg_lo:[1,0,0] neg_hi:[1,0,0]
	v_pk_fma_f32 v[32:33], v[50:51], v[32:33], 0 op_sel_hi:[0,1,0] neg_lo:[1,0,0] neg_hi:[1,0,0]
	v_cvt_pk_bf16_f32 v30, v30, v31
	v_cvt_pk_bf16_f32 v31, v32, v33
	ds_write_b64 v186, v[30:31]
	ds_read_b32 v30, v187 offset:200
	s_waitcnt lgkmcnt(0)
	v_pk_fma_f32 v[26:27], v[30:31], v[26:27], 0 op_sel_hi:[0,1,0] neg_lo:[1,0,0] neg_hi:[1,0,0]
	v_pk_fma_f32 v[28:29], v[30:31], v[28:29], 0 op_sel_hi:[0,1,0] neg_lo:[1,0,0] neg_hi:[1,0,0]
	v_cvt_pk_bf16_f32 v26, v26, v27
	v_cvt_pk_bf16_f32 v27, v28, v29
	ds_write_b64 v186, v[26:27] offset:544
	ds_read_b32 v26, v187 offset:208
	s_waitcnt lgkmcnt(0)
	v_pk_fma_f32 v[22:23], v[26:27], v[22:23], 0 op_sel_hi:[0,1,0] neg_lo:[1,0,0] neg_hi:[1,0,0]
	v_pk_fma_f32 v[24:25], v[26:27], v[24:25], 0 op_sel_hi:[0,1,0] neg_lo:[1,0,0] neg_hi:[1,0,0]
	v_cvt_pk_bf16_f32 v22, v22, v23
	v_cvt_pk_bf16_f32 v23, v24, v25
	ds_write_b64 v186, v[22:23] offset:1088
	ds_read_b32 v22, v187 offset:216
	s_waitcnt lgkmcnt(0)
	v_pk_fma_f32 v[18:19], v[22:23], v[18:19], 0 op_sel_hi:[0,1,0] neg_lo:[1,0,0] neg_hi:[1,0,0]
	v_pk_fma_f32 v[20:21], v[22:23], v[20:21], 0 op_sel_hi:[0,1,0] neg_lo:[1,0,0] neg_hi:[1,0,0]
	v_cvt_pk_bf16_f32 v18, v18, v19
	v_cvt_pk_bf16_f32 v19, v20, v21
	ds_write_b64 v186, v[18:19] offset:1632
	ds_read_b32 v18, v187 offset:224
	s_waitcnt lgkmcnt(0)
	v_pk_fma_f32 v[14:15], v[18:19], v[14:15], 0 op_sel_hi:[0,1,0] neg_lo:[1,0,0] neg_hi:[1,0,0]
	v_pk_fma_f32 v[16:17], v[18:19], v[16:17], 0 op_sel_hi:[0,1,0] neg_lo:[1,0,0] neg_hi:[1,0,0]
	v_cvt_pk_bf16_f32 v14, v14, v15
	v_cvt_pk_bf16_f32 v15, v16, v17
	ds_write_b64 v186, v[14:15] offset:2176
	ds_read_b32 v14, v187 offset:232
	s_waitcnt lgkmcnt(0)
	v_pk_fma_f32 v[10:11], v[14:15], v[10:11], 0 op_sel_hi:[0,1,0] neg_lo:[1,0,0] neg_hi:[1,0,0]
	v_pk_fma_f32 v[12:13], v[14:15], v[12:13], 0 op_sel_hi:[0,1,0] neg_lo:[1,0,0] neg_hi:[1,0,0]
	v_cvt_pk_bf16_f32 v10, v10, v11
	v_cvt_pk_bf16_f32 v11, v12, v13
	ds_write_b64 v186, v[10:11] offset:2720
	ds_read_b32 v10, v187 offset:240
	s_waitcnt lgkmcnt(0)
	v_pk_fma_f32 v[6:7], v[10:11], v[6:7], 0 op_sel_hi:[0,1,0] neg_lo:[1,0,0] neg_hi:[1,0,0]
	v_pk_fma_f32 v[8:9], v[10:11], v[8:9], 0 op_sel_hi:[0,1,0] neg_lo:[1,0,0] neg_hi:[1,0,0]
	v_cvt_pk_bf16_f32 v6, v6, v7
	v_cvt_pk_bf16_f32 v7, v8, v9
	ds_write_b64 v186, v[6:7] offset:3264
	ds_read_b32 v6, v187 offset:248
	s_waitcnt lgkmcnt(0)
	v_pk_fma_f32 v[2:3], v[6:7], v[2:3], 0 op_sel_hi:[0,1,0] neg_lo:[1,0,0] neg_hi:[1,0,0]
	v_pk_fma_f32 v[4:5], v[6:7], v[4:5], 0 op_sel_hi:[0,1,0] neg_lo:[1,0,0] neg_hi:[1,0,0]
	v_cvt_pk_bf16_f32 v2, v2, v3
	v_cvt_pk_bf16_f32 v3, v4, v5
	ds_write_b64 v186, v[2:3] offset:3808
	ds_read_b128 v[2:5], v1
	s_waitcnt lgkmcnt(0)
	ds_write_b128 v184, v[2:5] offset:8192
	ds_read_b128 v[2:5], v1 offset:64
	s_waitcnt lgkmcnt(0)
	ds_write_b128 v184, v[2:5] offset:9216
	ds_read_b128 v[2:5], v1 offset:128
	s_waitcnt lgkmcnt(0)
	ds_write_b128 v184, v[2:5] offset:10240
	ds_read_b128 v[2:5], v1 offset:192
	s_waitcnt lgkmcnt(0)
	ds_write_b128 v184, v[2:5] offset:11264
	s_lshl_b32 s26, s23, 2
	s_mov_b32 s27, s21
	v_lshl_add_u64 v[2:3], v[126:127], 0, s[26:27]
	v_lshl_add_u64 v[4:5], v[128:129], 0, s[26:27]
	v_lshl_add_u64 v[6:7], v[134:135], 0, s[26:27]
	v_lshl_add_u64 v[8:9], v[136:137], 0, s[26:27]
	v_lshl_add_u64 v[10:11], v[138:139], 0, s[26:27]
	v_lshl_add_u64 v[12:13], v[140:141], 0, s[26:27]
	v_lshl_add_u64 v[14:15], v[142:143], 0, s[26:27]
	v_lshl_add_u64 v[16:17], v[144:145], 0, s[26:27]
	global_load_dwordx4 v[118:121], v[2:3], off nt
	global_load_dwordx4 v[110:113], v[4:5], off nt
	global_load_dwordx4 v[102:105], v[6:7], off nt
	global_load_dwordx4 v[98:101], v[8:9], off nt
	global_load_dwordx4 v[58:61], v[10:11], off nt
	global_load_dwordx4 v[50:53], v[12:13], off nt
	global_load_dwordx4 v[30:33], v[14:15], off nt
	global_load_dwordx4 v[22:25], v[16:17], off nt
	v_mov_b32_e32 v2, v198
	s_waitcnt vmcnt(23)
	s_waitcnt vmcnt(22)
	s_waitcnt vmcnt(21)
	s_waitcnt vmcnt(20)
	s_waitcnt vmcnt(19)
	s_waitcnt vmcnt(18)
	s_waitcnt vmcnt(17)
	s_waitcnt vmcnt(16)
	ds_read_b32 v2, v187 offset:192
	s_waitcnt lgkmcnt(0)
	v_pk_fma_f32 v[4:5], v[2:3], v[90:91], 0 op_sel_hi:[0,1,0] neg_lo:[1,0,0] neg_hi:[1,0,0]
	v_pk_fma_f32 v[2:3], v[2:3], v[92:93], 0 op_sel_hi:[0,1,0] neg_lo:[1,0,0] neg_hi:[1,0,0]
	v_cvt_pk_bf16_f32 v4, v4, v5
	v_cvt_pk_bf16_f32 v5, v2, v3
	ds_write_b64 v186, v[4:5]
	ds_read_b32 v2, v187 offset:200
	s_waitcnt lgkmcnt(0)
	v_pk_fma_f32 v[4:5], v[2:3], v[82:83], 0 op_sel_hi:[0,1,0] neg_lo:[1,0,0] neg_hi:[1,0,0]
	v_pk_fma_f32 v[2:3], v[2:3], v[84:85], 0 op_sel_hi:[0,1,0] neg_lo:[1,0,0] neg_hi:[1,0,0]
	v_cvt_pk_bf16_f32 v4, v4, v5
	v_cvt_pk_bf16_f32 v5, v2, v3
	ds_write_b64 v186, v[4:5] offset:544
	ds_read_b32 v2, v187 offset:208
	s_waitcnt lgkmcnt(0)
	v_pk_fma_f32 v[4:5], v[2:3], v[78:79], 0 op_sel_hi:[0,1,0] neg_lo:[1,0,0] neg_hi:[1,0,0]
	v_pk_fma_f32 v[2:3], v[2:3], v[80:81], 0 op_sel_hi:[0,1,0] neg_lo:[1,0,0] neg_hi:[1,0,0]
	v_cvt_pk_bf16_f32 v4, v4, v5
	v_cvt_pk_bf16_f32 v5, v2, v3
	ds_write_b64 v186, v[4:5] offset:1088
	ds_read_b32 v2, v187 offset:216
	s_waitcnt lgkmcnt(0)
	v_pk_fma_f32 v[4:5], v[2:3], v[70:71], 0 op_sel_hi:[0,1,0] neg_lo:[1,0,0] neg_hi:[1,0,0]
	v_pk_fma_f32 v[2:3], v[2:3], v[72:73], 0 op_sel_hi:[0,1,0] neg_lo:[1,0,0] neg_hi:[1,0,0]
	v_cvt_pk_bf16_f32 v4, v4, v5
	v_cvt_pk_bf16_f32 v5, v2, v3
	ds_write_b64 v186, v[4:5] offset:1632
	ds_read_b32 v2, v187 offset:224
	s_waitcnt lgkmcnt(0)
	v_pk_fma_f32 v[4:5], v[2:3], v[66:67], 0 op_sel_hi:[0,1,0] neg_lo:[1,0,0] neg_hi:[1,0,0]
	v_pk_fma_f32 v[2:3], v[2:3], v[68:69], 0 op_sel_hi:[0,1,0] neg_lo:[1,0,0] neg_hi:[1,0,0]
	v_cvt_pk_bf16_f32 v4, v4, v5
	v_cvt_pk_bf16_f32 v5, v2, v3
	ds_write_b64 v186, v[4:5] offset:2176
	ds_read_b32 v2, v187 offset:232
	s_waitcnt lgkmcnt(0)
	v_pk_fma_f32 v[4:5], v[2:3], v[62:63], 0 op_sel_hi:[0,1,0] neg_lo:[1,0,0] neg_hi:[1,0,0]
	v_pk_fma_f32 v[2:3], v[2:3], v[64:65], 0 op_sel_hi:[0,1,0] neg_lo:[1,0,0] neg_hi:[1,0,0]
	v_cvt_pk_bf16_f32 v4, v4, v5
	v_cvt_pk_bf16_f32 v5, v2, v3
	ds_write_b64 v186, v[4:5] offset:2720
	ds_read_b32 v2, v187 offset:240
	s_waitcnt lgkmcnt(0)
	v_pk_fma_f32 v[4:5], v[2:3], v[54:55], 0 op_sel_hi:[0,1,0] neg_lo:[1,0,0] neg_hi:[1,0,0]
	v_pk_fma_f32 v[2:3], v[2:3], v[56:57], 0 op_sel_hi:[0,1,0] neg_lo:[1,0,0] neg_hi:[1,0,0]
	v_cvt_pk_bf16_f32 v4, v4, v5
	v_cvt_pk_bf16_f32 v5, v2, v3
	ds_write_b64 v186, v[4:5] offset:3264
	ds_read_b32 v2, v187 offset:248
	s_waitcnt lgkmcnt(0)
	v_pk_fma_f32 v[4:5], v[2:3], v[46:47], 0 op_sel_hi:[0,1,0] neg_lo:[1,0,0] neg_hi:[1,0,0]
	v_pk_fma_f32 v[2:3], v[2:3], v[48:49], 0 op_sel_hi:[0,1,0] neg_lo:[1,0,0] neg_hi:[1,0,0]
	v_cvt_pk_bf16_f32 v4, v4, v5
	v_cvt_pk_bf16_f32 v5, v2, v3
	ds_write_b64 v186, v[4:5] offset:3808
	ds_read_b128 v[2:5], v1
	s_waitcnt lgkmcnt(0)
	ds_write_b128 v184, v[2:5] offset:12288
	ds_read_b128 v[2:5], v1 offset:64
	s_waitcnt lgkmcnt(0)
	ds_write_b128 v184, v[2:5] offset:13312
	ds_read_b128 v[2:5], v1 offset:128
	s_waitcnt lgkmcnt(0)
	ds_write_b128 v184, v[2:5] offset:14336
	ds_read_b128 v[2:5], v1 offset:192
	s_waitcnt lgkmcnt(0)
	ds_write_b128 v184, v[2:5] offset:15360
	s_lshl_b32 s24, s22, 2
	s_mov_b32 s25, s21
	v_lshl_add_u64 v[2:3], v[126:127], 0, s[24:25]
	v_lshl_add_u64 v[6:7], v[134:135], 0, s[24:25]
	v_lshl_add_u64 v[8:9], v[136:137], 0, s[24:25]
	v_lshl_add_u64 v[14:15], v[142:143], 0, s[24:25]
	v_lshl_add_u64 v[4:5], v[128:129], 0, s[24:25]
	v_lshl_add_u64 v[10:11], v[138:139], 0, s[24:25]
	v_lshl_add_u64 v[12:13], v[140:141], 0, s[24:25]
	v_lshl_add_u64 v[18:19], v[144:145], 0, s[24:25]
	global_load_dwordx4 v[94:97], v[2:3], off nt
	global_load_dwordx4 v[90:93], v[4:5], off nt
	global_load_dwordx4 v[82:85], v[6:7], off nt
	global_load_dwordx4 v[70:73], v[8:9], off nt
	global_load_dwordx4 v[54:57], v[10:11], off nt
	global_load_dwordx4 v[26:29], v[12:13], off nt
	s_nop 0
	global_load_dwordx4 v[14:17], v[14:15], off nt
	s_nop 0
	global_load_dwordx4 v[6:9], v[18:19], off nt
	v_mov_b32_e32 v2, v197
	s_waitcnt vmcnt(23)
	s_waitcnt vmcnt(22)
	s_waitcnt vmcnt(21)
	s_waitcnt vmcnt(20)
	s_waitcnt vmcnt(19)
	s_waitcnt vmcnt(18)
	s_waitcnt vmcnt(17)
	s_waitcnt vmcnt(16)
	ds_read_b32 v2, v187 offset:192
	s_waitcnt lgkmcnt(0)
	v_pk_fma_f32 v[4:5], v[2:3], v[122:123], 0 op_sel_hi:[0,1,0] neg_lo:[1,0,0] neg_hi:[1,0,0]
	v_pk_fma_f32 v[2:3], v[2:3], v[124:125], 0 op_sel_hi:[0,1,0] neg_lo:[1,0,0] neg_hi:[1,0,0]
	v_cvt_pk_bf16_f32 v4, v4, v5
	v_cvt_pk_bf16_f32 v5, v2, v3
	ds_write_b64 v186, v[4:5]
	ds_read_b32 v2, v187 offset:200
	s_waitcnt lgkmcnt(0)
	v_pk_fma_f32 v[4:5], v[2:3], v[114:115], 0 op_sel_hi:[0,1,0] neg_lo:[1,0,0] neg_hi:[1,0,0]
	v_pk_fma_f32 v[2:3], v[2:3], v[116:117], 0 op_sel_hi:[0,1,0] neg_lo:[1,0,0] neg_hi:[1,0,0]
	v_cvt_pk_bf16_f32 v4, v4, v5
	v_cvt_pk_bf16_f32 v5, v2, v3
	ds_write_b64 v186, v[4:5] offset:544
	ds_read_b32 v2, v187 offset:208
	s_waitcnt lgkmcnt(0)
	v_pk_fma_f32 v[4:5], v[2:3], v[106:107], 0 op_sel_hi:[0,1,0] neg_lo:[1,0,0] neg_hi:[1,0,0]
	v_pk_fma_f32 v[2:3], v[2:3], v[108:109], 0 op_sel_hi:[0,1,0] neg_lo:[1,0,0] neg_hi:[1,0,0]
	v_cvt_pk_bf16_f32 v4, v4, v5
	v_cvt_pk_bf16_f32 v5, v2, v3
	ds_write_b64 v186, v[4:5] offset:1088
	ds_read_b32 v2, v187 offset:216
	s_waitcnt lgkmcnt(0)
	v_pk_fma_f32 v[4:5], v[2:3], v[86:87], 0 op_sel_hi:[0,1,0] neg_lo:[1,0,0] neg_hi:[1,0,0]
	v_pk_fma_f32 v[2:3], v[2:3], v[88:89], 0 op_sel_hi:[0,1,0] neg_lo:[1,0,0] neg_hi:[1,0,0]
	v_cvt_pk_bf16_f32 v4, v4, v5
	v_cvt_pk_bf16_f32 v5, v2, v3
	ds_write_b64 v186, v[4:5] offset:1632
	ds_read_b32 v2, v187 offset:224
	s_waitcnt lgkmcnt(0)
	v_pk_fma_f32 v[4:5], v[2:3], v[74:75], 0 op_sel_hi:[0,1,0] neg_lo:[1,0,0] neg_hi:[1,0,0]
	v_pk_fma_f32 v[2:3], v[2:3], v[76:77], 0 op_sel_hi:[0,1,0] neg_lo:[1,0,0] neg_hi:[1,0,0]
	v_cvt_pk_bf16_f32 v4, v4, v5
	v_cvt_pk_bf16_f32 v5, v2, v3
	ds_write_b64 v186, v[4:5] offset:2176
	ds_read_b32 v2, v187 offset:232
	s_waitcnt lgkmcnt(0)
	v_pk_fma_f32 v[4:5], v[2:3], v[42:43], 0 op_sel_hi:[0,1,0] neg_lo:[1,0,0] neg_hi:[1,0,0]
	v_pk_fma_f32 v[2:3], v[2:3], v[44:45], 0 op_sel_hi:[0,1,0] neg_lo:[1,0,0] neg_hi:[1,0,0]
	v_cvt_pk_bf16_f32 v4, v4, v5
	v_cvt_pk_bf16_f32 v5, v2, v3
	ds_write_b64 v186, v[4:5] offset:2720
	ds_read_b32 v2, v187 offset:240
	s_waitcnt lgkmcnt(0)
	v_pk_fma_f32 v[4:5], v[2:3], v[38:39], 0 op_sel_hi:[0,1,0] neg_lo:[1,0,0] neg_hi:[1,0,0]
	v_pk_fma_f32 v[2:3], v[2:3], v[40:41], 0 op_sel_hi:[0,1,0] neg_lo:[1,0,0] neg_hi:[1,0,0]
	v_cvt_pk_bf16_f32 v4, v4, v5
	v_cvt_pk_bf16_f32 v5, v2, v3
	ds_write_b64 v186, v[4:5] offset:3264
	ds_read_b32 v2, v187 offset:248
	s_waitcnt lgkmcnt(0)
	v_pk_fma_f32 v[4:5], v[2:3], v[34:35], 0 op_sel_hi:[0,1,0] neg_lo:[1,0,0] neg_hi:[1,0,0]
	v_pk_fma_f32 v[2:3], v[2:3], v[36:37], 0 op_sel_hi:[0,1,0] neg_lo:[1,0,0] neg_hi:[1,0,0]
	v_cvt_pk_bf16_f32 v4, v4, v5
	v_cvt_pk_bf16_f32 v5, v2, v3
	ds_write_b64 v186, v[4:5] offset:3808
	ds_read_b128 v[2:5], v1
	s_waitcnt lgkmcnt(0)
	ds_write_b128 v184, v[2:5] offset:16384
	ds_read_b128 v[2:5], v1 offset:64
	s_waitcnt lgkmcnt(0)
	ds_write_b128 v184, v[2:5] offset:17408
	ds_read_b128 v[2:5], v1 offset:128
	s_waitcnt lgkmcnt(0)
	ds_write_b128 v184, v[2:5] offset:18432
	ds_read_b128 v[2:5], v1 offset:192
	s_waitcnt lgkmcnt(0)
	ds_write_b128 v184, v[2:5] offset:19456
	s_lshl_b32 s22, s7, 2
	s_mov_b32 s23, s21
	v_lshl_add_u64 v[2:3], v[126:127], 0, s[22:23]
	v_lshl_add_u64 v[4:5], v[128:129], 0, s[22:23]
	v_lshl_add_u64 v[10:11], v[134:135], 0, s[22:23]
	v_lshl_add_u64 v[12:13], v[136:137], 0, s[22:23]
	v_lshl_add_u64 v[34:35], v[138:139], 0, s[22:23]
	v_lshl_add_u64 v[36:37], v[140:141], 0, s[22:23]
	v_lshl_add_u64 v[46:47], v[142:143], 0, s[22:23]
	v_lshl_add_u64 v[48:49], v[144:145], 0, s[22:23]
	global_load_dwordx4 v[86:89], v[2:3], off nt
	global_load_dwordx4 v[78:81], v[4:5], off nt
	global_load_dwordx4 v[66:69], v[10:11], off nt
	global_load_dwordx4 v[42:45], v[12:13], off nt
	global_load_dwordx4 v[38:41], v[34:35], off nt
	global_load_dwordx4 v[18:21], v[36:37], off nt
	s_nop 0
	global_load_dwordx4 v[10:13], v[46:47], off nt
	global_load_dwordx4 v[2:5], v[48:49], off nt
	v_mov_b32_e32 v34, v196
	s_waitcnt vmcnt(23)
	s_waitcnt vmcnt(22)
	s_waitcnt vmcnt(21)
	s_waitcnt vmcnt(20)
	s_waitcnt vmcnt(19)
	s_waitcnt vmcnt(18)
	s_waitcnt vmcnt(17)
	s_waitcnt vmcnt(16)
	ds_read_b32 v34, v187 offset:192
	s_waitcnt lgkmcnt(0)
	v_pk_fma_f32 v[36:37], v[34:35], v[118:119], 0 op_sel_hi:[0,1,0] neg_lo:[1,0,0] neg_hi:[1,0,0]
	v_pk_fma_f32 v[34:35], v[34:35], v[120:121], 0 op_sel_hi:[0,1,0] neg_lo:[1,0,0] neg_hi:[1,0,0]
	v_cvt_pk_bf16_f32 v36, v36, v37
	v_cvt_pk_bf16_f32 v37, v34, v35
	ds_write_b64 v186, v[36:37]
	ds_read_b32 v34, v187 offset:200
	s_waitcnt lgkmcnt(0)
	v_pk_fma_f32 v[36:37], v[34:35], v[110:111], 0 op_sel_hi:[0,1,0] neg_lo:[1,0,0] neg_hi:[1,0,0]
	v_pk_fma_f32 v[34:35], v[34:35], v[112:113], 0 op_sel_hi:[0,1,0] neg_lo:[1,0,0] neg_hi:[1,0,0]
	v_cvt_pk_bf16_f32 v36, v36, v37
	v_cvt_pk_bf16_f32 v37, v34, v35
	ds_write_b64 v186, v[36:37] offset:544
	ds_read_b32 v34, v187 offset:208
	s_waitcnt lgkmcnt(0)
	v_pk_fma_f32 v[36:37], v[34:35], v[102:103], 0 op_sel_hi:[0,1,0] neg_lo:[1,0,0] neg_hi:[1,0,0]
	v_pk_fma_f32 v[34:35], v[34:35], v[104:105], 0 op_sel_hi:[0,1,0] neg_lo:[1,0,0] neg_hi:[1,0,0]
	v_cvt_pk_bf16_f32 v36, v36, v37
	v_cvt_pk_bf16_f32 v37, v34, v35
	ds_write_b64 v186, v[36:37] offset:1088
	ds_read_b32 v34, v187 offset:216
	s_waitcnt lgkmcnt(0)
	v_pk_fma_f32 v[36:37], v[34:35], v[98:99], 0 op_sel_hi:[0,1,0] neg_lo:[1,0,0] neg_hi:[1,0,0]
	v_pk_fma_f32 v[34:35], v[34:35], v[100:101], 0 op_sel_hi:[0,1,0] neg_lo:[1,0,0] neg_hi:[1,0,0]
	v_cvt_pk_bf16_f32 v36, v36, v37
	v_cvt_pk_bf16_f32 v37, v34, v35
	ds_write_b64 v186, v[36:37] offset:1632
	ds_read_b32 v34, v187 offset:224
	s_waitcnt lgkmcnt(0)
	v_pk_fma_f32 v[36:37], v[34:35], v[58:59], 0 op_sel_hi:[0,1,0] neg_lo:[1,0,0] neg_hi:[1,0,0]
	v_pk_fma_f32 v[34:35], v[34:35], v[60:61], 0 op_sel_hi:[0,1,0] neg_lo:[1,0,0] neg_hi:[1,0,0]
	v_cvt_pk_bf16_f32 v36, v36, v37
	v_cvt_pk_bf16_f32 v37, v34, v35
	ds_write_b64 v186, v[36:37] offset:2176
	ds_read_b32 v34, v187 offset:232
	s_waitcnt lgkmcnt(0)
	v_pk_fma_f32 v[36:37], v[34:35], v[50:51], 0 op_sel_hi:[0,1,0] neg_lo:[1,0,0] neg_hi:[1,0,0]
	v_pk_fma_f32 v[34:35], v[34:35], v[52:53], 0 op_sel_hi:[0,1,0] neg_lo:[1,0,0] neg_hi:[1,0,0]
	v_cvt_pk_bf16_f32 v36, v36, v37
	v_cvt_pk_bf16_f32 v37, v34, v35
	ds_write_b64 v186, v[36:37] offset:2720
	ds_read_b32 v34, v187 offset:240
	s_waitcnt lgkmcnt(0)
	v_pk_fma_f32 v[30:31], v[34:35], v[30:31], 0 op_sel_hi:[0,1,0] neg_lo:[1,0,0] neg_hi:[1,0,0]
	v_pk_fma_f32 v[32:33], v[34:35], v[32:33], 0 op_sel_hi:[0,1,0] neg_lo:[1,0,0] neg_hi:[1,0,0]
	v_cvt_pk_bf16_f32 v30, v30, v31
	v_cvt_pk_bf16_f32 v31, v32, v33
	ds_write_b64 v186, v[30:31] offset:3264
	ds_read_b32 v30, v187 offset:248
	s_waitcnt lgkmcnt(0)
	v_pk_fma_f32 v[22:23], v[30:31], v[22:23], 0 op_sel_hi:[0,1,0] neg_lo:[1,0,0] neg_hi:[1,0,0]
	v_pk_fma_f32 v[24:25], v[30:31], v[24:25], 0 op_sel_hi:[0,1,0] neg_lo:[1,0,0] neg_hi:[1,0,0]
	v_cvt_pk_bf16_f32 v22, v22, v23
	v_cvt_pk_bf16_f32 v23, v24, v25
	ds_write_b64 v186, v[22:23] offset:3808
	ds_read_b128 v[22:25], v1
	s_waitcnt lgkmcnt(0)
	ds_write_b128 v184, v[22:25] offset:20480
	ds_read_b128 v[22:25], v1 offset:64
	s_waitcnt lgkmcnt(0)
	ds_write_b128 v184, v[22:25] offset:21504
	ds_read_b128 v[22:25], v1 offset:128
	s_waitcnt lgkmcnt(0)
	ds_write_b128 v184, v[22:25] offset:22528
	ds_read_b128 v[22:25], v1 offset:192
	s_waitcnt lgkmcnt(0)
	ds_write_b128 v184, v[22:25] offset:23552
	v_lshl_add_u64 v[22:23], v[130:131], 0, s[30:31]
	s_movk_i32 s7, 0x2000
	v_add_co_u32_e32 v24, vcc, s7, v22
	s_movk_i32 s36, 0x4000
	s_nop 0
	v_addc_co_u32_e32 v25, vcc, 0, v23, vcc
	global_load_dwordx4 v[74:77], v[22:23], off nt
	global_load_dwordx4 v[62:65], v[24:25], off nt
	v_add_co_u32_e32 v24, vcc, s36, v22
	s_movk_i32 s37, 0x6000
	s_nop 0
	v_addc_co_u32_e32 v25, vcc, 0, v23, vcc
	v_add_co_u32_e32 v30, vcc, s37, v22
	s_mov_b32 s38, 0x8000
	s_nop 0
	v_addc_co_u32_e32 v31, vcc, 0, v23, vcc
	global_load_dwordx4 v[58:61], v[24:25], off nt
	global_load_dwordx4 v[46:49], v[30:31], off nt
	v_add_co_u32_e32 v24, vcc, s38, v22
	s_mov_b32 s39, 0xa000
	s_nop 0
	v_addc_co_u32_e32 v25, vcc, 0, v23, vcc
	v_add_co_u32_e32 v34, vcc, s39, v22
	s_mov_b32 s41, 0xc000
	s_nop 0
	v_addc_co_u32_e32 v35, vcc, 0, v23, vcc
	global_load_dwordx4 v[50:53], v[24:25], off nt
	global_load_dwordx4 v[30:33], v[34:35], off nt
	v_add_co_u32_e32 v24, vcc, s41, v22
	s_mov_b32 s42, 0xe000
	s_nop 0
	v_addc_co_u32_e32 v25, vcc, 0, v23, vcc
	v_add_co_u32_e32 v22, vcc, s42, v22
	s_nop 1
	v_addc_co_u32_e32 v23, vcc, 0, v23, vcc
	global_load_dwordx4 v[34:37], v[24:25], off nt
	s_nop 0
	global_load_dwordx4 v[22:25], v[22:23], off nt
	v_mov_b32_e32 v98, v195
	s_waitcnt vmcnt(23)
	s_waitcnt vmcnt(22)
	s_waitcnt vmcnt(21)
	s_waitcnt vmcnt(20)
	s_waitcnt vmcnt(19)
	s_waitcnt vmcnt(18)
	s_waitcnt vmcnt(17)
	s_waitcnt vmcnt(16)
	ds_read_b32 v98, v187 offset:192
	s_waitcnt lgkmcnt(0)
	v_pk_fma_f32 v[94:95], v[98:99], v[94:95], 0 op_sel_hi:[0,1,0] neg_lo:[1,0,0] neg_hi:[1,0,0]
	v_pk_fma_f32 v[96:97], v[98:99], v[96:97], 0 op_sel_hi:[0,1,0] neg_lo:[1,0,0] neg_hi:[1,0,0]
	v_cvt_pk_bf16_f32 v94, v94, v95
	v_cvt_pk_bf16_f32 v95, v96, v97
	ds_write_b64 v186, v[94:95]
	ds_read_b32 v94, v187 offset:200
	s_waitcnt lgkmcnt(0)
	v_pk_fma_f32 v[90:91], v[94:95], v[90:91], 0 op_sel_hi:[0,1,0] neg_lo:[1,0,0] neg_hi:[1,0,0]
	v_pk_fma_f32 v[92:93], v[94:95], v[92:93], 0 op_sel_hi:[0,1,0] neg_lo:[1,0,0] neg_hi:[1,0,0]
	v_cvt_pk_bf16_f32 v90, v90, v91
	v_cvt_pk_bf16_f32 v91, v92, v93
	ds_write_b64 v186, v[90:91] offset:544
	ds_read_b32 v90, v187 offset:208
	s_waitcnt lgkmcnt(0)
	v_pk_fma_f32 v[82:83], v[90:91], v[82:83], 0 op_sel_hi:[0,1,0] neg_lo:[1,0,0] neg_hi:[1,0,0]
	v_pk_fma_f32 v[84:85], v[90:91], v[84:85], 0 op_sel_hi:[0,1,0] neg_lo:[1,0,0] neg_hi:[1,0,0]
	v_cvt_pk_bf16_f32 v82, v82, v83
	v_cvt_pk_bf16_f32 v83, v84, v85
	ds_write_b64 v186, v[82:83] offset:1088
	ds_read_b32 v82, v187 offset:216
	s_waitcnt lgkmcnt(0)
	v_pk_fma_f32 v[70:71], v[82:83], v[70:71], 0 op_sel_hi:[0,1,0] neg_lo:[1,0,0] neg_hi:[1,0,0]
	v_pk_fma_f32 v[72:73], v[82:83], v[72:73], 0 op_sel_hi:[0,1,0] neg_lo:[1,0,0] neg_hi:[1,0,0]
	v_cvt_pk_bf16_f32 v70, v70, v71
	v_cvt_pk_bf16_f32 v71, v72, v73
	ds_write_b64 v186, v[70:71] offset:1632
	ds_read_b32 v70, v187 offset:224
	s_waitcnt lgkmcnt(0)
	v_pk_fma_f32 v[54:55], v[70:71], v[54:55], 0 op_sel_hi:[0,1,0] neg_lo:[1,0,0] neg_hi:[1,0,0]
	v_pk_fma_f32 v[56:57], v[70:71], v[56:57], 0 op_sel_hi:[0,1,0] neg_lo:[1,0,0] neg_hi:[1,0,0]
	v_cvt_pk_bf16_f32 v54, v54, v55
	v_cvt_pk_bf16_f32 v55, v56, v57
	ds_write_b64 v186, v[54:55] offset:2176
	ds_read_b32 v54, v187 offset:232
	s_waitcnt lgkmcnt(0)
	v_pk_fma_f32 v[26:27], v[54:55], v[26:27], 0 op_sel_hi:[0,1,0] neg_lo:[1,0,0] neg_hi:[1,0,0]
	v_pk_fma_f32 v[28:29], v[54:55], v[28:29], 0 op_sel_hi:[0,1,0] neg_lo:[1,0,0] neg_hi:[1,0,0]
	v_cvt_pk_bf16_f32 v26, v26, v27
	v_cvt_pk_bf16_f32 v27, v28, v29
	ds_write_b64 v186, v[26:27] offset:2720
	ds_read_b32 v26, v187 offset:240
	s_waitcnt lgkmcnt(0)
	v_pk_fma_f32 v[14:15], v[26:27], v[14:15], 0 op_sel_hi:[0,1,0] neg_lo:[1,0,0] neg_hi:[1,0,0]
	v_pk_fma_f32 v[16:17], v[26:27], v[16:17], 0 op_sel_hi:[0,1,0] neg_lo:[1,0,0] neg_hi:[1,0,0]
	v_cvt_pk_bf16_f32 v14, v14, v15
	v_cvt_pk_bf16_f32 v15, v16, v17
	ds_write_b64 v186, v[14:15] offset:3264
	ds_read_b32 v14, v187 offset:248
	s_waitcnt lgkmcnt(0)
	v_pk_fma_f32 v[6:7], v[14:15], v[6:7], 0 op_sel_hi:[0,1,0] neg_lo:[1,0,0] neg_hi:[1,0,0]
	v_pk_fma_f32 v[8:9], v[14:15], v[8:9], 0 op_sel_hi:[0,1,0] neg_lo:[1,0,0] neg_hi:[1,0,0]
	v_cvt_pk_bf16_f32 v6, v6, v7
	v_cvt_pk_bf16_f32 v7, v8, v9
	ds_write_b64 v186, v[6:7] offset:3808
	ds_read_b128 v[6:9], v1
	s_waitcnt lgkmcnt(0)
	ds_write_b128 v184, v[6:9] offset:24576
	ds_read_b128 v[6:9], v1 offset:64
	s_waitcnt lgkmcnt(0)
	ds_write_b128 v184, v[6:9] offset:25600
	ds_read_b128 v[6:9], v1 offset:128
	s_waitcnt lgkmcnt(0)
	ds_write_b128 v184, v[6:9] offset:26624
	ds_read_b128 v[6:9], v1 offset:192
	s_waitcnt lgkmcnt(0)
	ds_write_b128 v184, v[6:9] offset:27648
	s_mov_b64 s[44:45], 0x10000
	v_lshl_add_u64 v[150:151], v[130:131], 0, s[44:45]
	s_mov_b64 s[44:45], 0x12000
	v_lshl_add_u64 v[152:153], v[130:131], 0, s[44:45]
	s_mov_b64 s[44:45], 0x14000
	v_lshl_add_u64 v[156:157], v[130:131], 0, s[44:45]
	s_mov_b64 s[44:45], 0x16000
	v_lshl_add_u64 v[158:159], v[130:131], 0, s[44:45]
	s_mov_b64 s[44:45], 0x18000
	v_lshl_add_u64 v[160:161], v[130:131], 0, s[44:45]
	s_mov_b64 s[44:45], 0x1a000
	v_lshl_add_u64 v[162:163], v[130:131], 0, s[44:45]
	s_mov_b64 s[44:45], 0x1c000
	v_lshl_add_u64 v[164:165], v[130:131], 0, s[44:45]
	s_mov_b64 s[44:45], 0x1e000
	v_lshl_add_u64 v[6:7], v[150:151], 0, s[30:31]
	v_lshl_add_u64 v[8:9], v[152:153], 0, s[30:31]
	v_lshl_add_u64 v[14:15], v[156:157], 0, s[30:31]
	v_lshl_add_u64 v[16:17], v[158:159], 0, s[30:31]
	v_lshl_add_u64 v[26:27], v[160:161], 0, s[30:31]
	v_lshl_add_u64 v[28:29], v[162:163], 0, s[30:31]
	v_lshl_add_u64 v[166:167], v[130:131], 0, s[44:45]
	v_lshl_add_u64 v[98:99], v[164:165], 0, s[30:31]
	v_lshl_add_u64 v[100:101], v[166:167], 0, s[30:31]
	global_load_dwordx4 v[94:97], v[6:7], off nt
	global_load_dwordx4 v[90:93], v[8:9], off nt
	global_load_dwordx4 v[82:85], v[14:15], off nt
	global_load_dwordx4 v[70:73], v[16:17], off nt
	global_load_dwordx4 v[54:57], v[26:27], off nt
	s_nop 0
	global_load_dwordx4 v[26:29], v[28:29], off nt
	s_nop 0
	global_load_dwordx4 v[14:17], v[98:99], off nt
	global_load_dwordx4 v[6:9], v[100:101], off nt
	v_mov_b32_e32 v98, v194
	s_waitcnt vmcnt(23)
	s_waitcnt vmcnt(22)
	s_waitcnt vmcnt(21)
	s_waitcnt vmcnt(20)
	s_waitcnt vmcnt(19)
	s_waitcnt vmcnt(18)
	s_waitcnt vmcnt(17)
	s_waitcnt vmcnt(16)
	ds_read_b32 v98, v187 offset:192
	s_waitcnt lgkmcnt(0)
	v_pk_fma_f32 v[86:87], v[98:99], v[86:87], 0 op_sel_hi:[0,1,0] neg_lo:[1,0,0] neg_hi:[1,0,0]
	v_pk_fma_f32 v[88:89], v[98:99], v[88:89], 0 op_sel_hi:[0,1,0] neg_lo:[1,0,0] neg_hi:[1,0,0]
	v_cvt_pk_bf16_f32 v86, v86, v87
	v_cvt_pk_bf16_f32 v87, v88, v89
	ds_write_b64 v186, v[86:87]
	ds_read_b32 v86, v187 offset:200
	s_waitcnt lgkmcnt(0)
	v_pk_fma_f32 v[78:79], v[86:87], v[78:79], 0 op_sel_hi:[0,1,0] neg_lo:[1,0,0] neg_hi:[1,0,0]
	v_pk_fma_f32 v[80:81], v[86:87], v[80:81], 0 op_sel_hi:[0,1,0] neg_lo:[1,0,0] neg_hi:[1,0,0]
	v_cvt_pk_bf16_f32 v78, v78, v79
	v_cvt_pk_bf16_f32 v79, v80, v81
	ds_write_b64 v186, v[78:79] offset:544
	ds_read_b32 v78, v187 offset:208
	s_waitcnt lgkmcnt(0)
	v_pk_fma_f32 v[66:67], v[78:79], v[66:67], 0 op_sel_hi:[0,1,0] neg_lo:[1,0,0] neg_hi:[1,0,0]
	v_pk_fma_f32 v[68:69], v[78:79], v[68:69], 0 op_sel_hi:[0,1,0] neg_lo:[1,0,0] neg_hi:[1,0,0]
	v_cvt_pk_bf16_f32 v66, v66, v67
	v_cvt_pk_bf16_f32 v67, v68, v69
	ds_write_b64 v186, v[66:67] offset:1088
	ds_read_b32 v66, v187 offset:216
	s_waitcnt lgkmcnt(0)
	v_pk_fma_f32 v[42:43], v[66:67], v[42:43], 0 op_sel_hi:[0,1,0] neg_lo:[1,0,0] neg_hi:[1,0,0]
	v_pk_fma_f32 v[44:45], v[66:67], v[44:45], 0 op_sel_hi:[0,1,0] neg_lo:[1,0,0] neg_hi:[1,0,0]
	v_cvt_pk_bf16_f32 v42, v42, v43
	v_cvt_pk_bf16_f32 v43, v44, v45
	ds_write_b64 v186, v[42:43] offset:1632
	ds_read_b32 v42, v187 offset:224
	s_waitcnt lgkmcnt(0)
	v_pk_fma_f32 v[38:39], v[42:43], v[38:39], 0 op_sel_hi:[0,1,0] neg_lo:[1,0,0] neg_hi:[1,0,0]
	v_pk_fma_f32 v[40:41], v[42:43], v[40:41], 0 op_sel_hi:[0,1,0] neg_lo:[1,0,0] neg_hi:[1,0,0]
	v_cvt_pk_bf16_f32 v38, v38, v39
	v_cvt_pk_bf16_f32 v39, v40, v41
	ds_write_b64 v186, v[38:39] offset:2176
	ds_read_b32 v38, v187 offset:232
	s_waitcnt lgkmcnt(0)
	v_pk_fma_f32 v[18:19], v[38:39], v[18:19], 0 op_sel_hi:[0,1,0] neg_lo:[1,0,0] neg_hi:[1,0,0]
	v_pk_fma_f32 v[20:21], v[38:39], v[20:21], 0 op_sel_hi:[0,1,0] neg_lo:[1,0,0] neg_hi:[1,0,0]
	v_cvt_pk_bf16_f32 v18, v18, v19
	v_cvt_pk_bf16_f32 v19, v20, v21
	ds_write_b64 v186, v[18:19] offset:2720
	ds_read_b32 v18, v187 offset:240
	s_waitcnt lgkmcnt(0)
	v_pk_fma_f32 v[10:11], v[18:19], v[10:11], 0 op_sel_hi:[0,1,0] neg_lo:[1,0,0] neg_hi:[1,0,0]
	v_pk_fma_f32 v[12:13], v[18:19], v[12:13], 0 op_sel_hi:[0,1,0] neg_lo:[1,0,0] neg_hi:[1,0,0]
	v_cvt_pk_bf16_f32 v10, v10, v11
	v_cvt_pk_bf16_f32 v11, v12, v13
	ds_write_b64 v186, v[10:11] offset:3264
	ds_read_b32 v10, v187 offset:248
	s_waitcnt lgkmcnt(0)
	v_pk_fma_f32 v[2:3], v[10:11], v[2:3], 0 op_sel_hi:[0,1,0] neg_lo:[1,0,0] neg_hi:[1,0,0]
	v_pk_fma_f32 v[4:5], v[10:11], v[4:5], 0 op_sel_hi:[0,1,0] neg_lo:[1,0,0] neg_hi:[1,0,0]
	v_cvt_pk_bf16_f32 v2, v2, v3
	v_cvt_pk_bf16_f32 v3, v4, v5
	ds_write_b64 v186, v[2:3] offset:3808
	ds_read_b128 v[2:5], v1
	s_waitcnt lgkmcnt(0)
	ds_write_b128 v184, v[2:5] offset:28672
	ds_read_b128 v[2:5], v1 offset:64
	s_waitcnt lgkmcnt(0)
	ds_write_b128 v184, v[2:5] offset:29696
	ds_read_b128 v[2:5], v1 offset:128
	s_waitcnt lgkmcnt(0)
	ds_write_b128 v184, v[2:5] offset:30720
	ds_read_b128 v[2:5], v1 offset:192
	s_waitcnt lgkmcnt(0)
	ds_write_b128 v184, v[2:5] offset:31744
	s_mov_b64 s[44:45], 0x20000
	v_lshl_add_u64 v[168:169], v[130:131], 0, s[44:45]
	s_mov_b64 s[44:45], 0x22000
	v_lshl_add_u64 v[170:171], v[130:131], 0, s[44:45]
	s_mov_b64 s[44:45], 0x24000
	v_lshl_add_u64 v[172:173], v[130:131], 0, s[44:45]
	s_mov_b64 s[44:45], 0x26000
	v_lshl_add_u64 v[174:175], v[130:131], 0, s[44:45]
	s_mov_b64 s[44:45], 0x28000
	v_lshl_add_u64 v[176:177], v[130:131], 0, s[44:45]
	s_mov_b64 s[44:45], 0x2a000
	v_lshl_add_u64 v[178:179], v[130:131], 0, s[44:45]
	s_mov_b64 s[44:45], 0x2c000
	v_lshl_add_u64 v[180:181], v[130:131], 0, s[44:45]
	s_mov_b64 s[44:45], 0x2e000
	v_lshl_add_u64 v[2:3], v[168:169], 0, s[30:31]
	v_lshl_add_u64 v[4:5], v[170:171], 0, s[30:31]
	v_lshl_add_u64 v[10:11], v[172:173], 0, s[30:31]
	v_lshl_add_u64 v[12:13], v[174:175], 0, s[30:31]
	v_lshl_add_u64 v[18:19], v[176:177], 0, s[30:31]
	v_lshl_add_u64 v[20:21], v[178:179], 0, s[30:31]
	v_lshl_add_u64 v[182:183], v[130:131], 0, s[44:45]
	v_lshl_add_u64 v[42:43], v[180:181], 0, s[30:31]
	v_lshl_add_u64 v[44:45], v[182:183], 0, s[30:31]
	global_load_dwordx4 v[106:109], v[2:3], off nt
	global_load_dwordx4 v[98:101], v[4:5], off nt
	global_load_dwordx4 v[78:81], v[10:11], off nt
	global_load_dwordx4 v[66:69], v[12:13], off nt
	global_load_dwordx4 v[38:41], v[18:19], off nt
	s_nop 0
	global_load_dwordx4 v[18:21], v[20:21], off nt
	s_nop 0
	global_load_dwordx4 v[10:13], v[42:43], off nt
	global_load_dwordx4 v[2:5], v[44:45], off nt
	v_mov_b32_e32 v42, v198
	s_waitcnt vmcnt(23)
	s_waitcnt vmcnt(22)
	s_waitcnt vmcnt(21)
	s_waitcnt vmcnt(20)
	s_waitcnt vmcnt(19)
	s_waitcnt vmcnt(18)
	s_waitcnt vmcnt(17)
	s_waitcnt vmcnt(16)
	ds_read_b32 v42, v187
	s_waitcnt lgkmcnt(0)
	v_pk_fma_f32 v[44:45], v[42:43], v[74:75], 0 op_sel_hi:[0,1,0] neg_lo:[1,0,0] neg_hi:[1,0,0]
	v_pk_fma_f32 v[42:43], v[42:43], v[76:77], 0 op_sel_hi:[0,1,0] neg_lo:[1,0,0] neg_hi:[1,0,0]
	v_cvt_pk_bf16_f32 v44, v44, v45
	v_cvt_pk_bf16_f32 v45, v42, v43
	ds_write_b64 v186, v[44:45]
	ds_read_b32 v42, v187 offset:8
	s_waitcnt lgkmcnt(0)
	v_pk_fma_f32 v[44:45], v[42:43], v[62:63], 0 op_sel_hi:[0,1,0] neg_lo:[1,0,0] neg_hi:[1,0,0]
	v_pk_fma_f32 v[42:43], v[42:43], v[64:65], 0 op_sel_hi:[0,1,0] neg_lo:[1,0,0] neg_hi:[1,0,0]
	v_cvt_pk_bf16_f32 v44, v44, v45
	v_cvt_pk_bf16_f32 v45, v42, v43
	ds_write_b64 v186, v[44:45] offset:544
	ds_read_b32 v42, v187 offset:16
	s_waitcnt lgkmcnt(0)
	v_pk_fma_f32 v[44:45], v[42:43], v[58:59], 0 op_sel_hi:[0,1,0] neg_lo:[1,0,0] neg_hi:[1,0,0]
	v_pk_fma_f32 v[42:43], v[42:43], v[60:61], 0 op_sel_hi:[0,1,0] neg_lo:[1,0,0] neg_hi:[1,0,0]
	v_cvt_pk_bf16_f32 v44, v44, v45
	v_cvt_pk_bf16_f32 v45, v42, v43
	ds_write_b64 v186, v[44:45] offset:1088
	ds_read_b32 v42, v187 offset:24
	s_waitcnt lgkmcnt(0)
	v_pk_fma_f32 v[44:45], v[42:43], v[46:47], 0 op_sel_hi:[0,1,0] neg_lo:[1,0,0] neg_hi:[1,0,0]
	v_pk_fma_f32 v[42:43], v[42:43], v[48:49], 0 op_sel_hi:[0,1,0] neg_lo:[1,0,0] neg_hi:[1,0,0]
	v_cvt_pk_bf16_f32 v44, v44, v45
	v_cvt_pk_bf16_f32 v45, v42, v43
	ds_write_b64 v186, v[44:45] offset:1632
	ds_read_b32 v42, v187 offset:32
	s_waitcnt lgkmcnt(0)
	v_pk_fma_f32 v[44:45], v[42:43], v[50:51], 0 op_sel_hi:[0,1,0] neg_lo:[1,0,0] neg_hi:[1,0,0]
	v_pk_fma_f32 v[42:43], v[42:43], v[52:53], 0 op_sel_hi:[0,1,0] neg_lo:[1,0,0] neg_hi:[1,0,0]
	v_cvt_pk_bf16_f32 v44, v44, v45
	v_cvt_pk_bf16_f32 v45, v42, v43
	ds_write_b64 v186, v[44:45] offset:2176
	ds_read_b32 v42, v187 offset:40
	s_waitcnt lgkmcnt(0)
	v_pk_fma_f32 v[30:31], v[42:43], v[30:31], 0 op_sel_hi:[0,1,0] neg_lo:[1,0,0] neg_hi:[1,0,0]
	v_pk_fma_f32 v[32:33], v[42:43], v[32:33], 0 op_sel_hi:[0,1,0] neg_lo:[1,0,0] neg_hi:[1,0,0]
	v_cvt_pk_bf16_f32 v30, v30, v31
	v_cvt_pk_bf16_f32 v31, v32, v33
	ds_write_b64 v186, v[30:31] offset:2720
	ds_read_b32 v30, v187 offset:48
	s_waitcnt lgkmcnt(0)
	v_pk_fma_f32 v[32:33], v[30:31], v[34:35], 0 op_sel_hi:[0,1,0] neg_lo:[1,0,0] neg_hi:[1,0,0]
	v_pk_fma_f32 v[30:31], v[30:31], v[36:37], 0 op_sel_hi:[0,1,0] neg_lo:[1,0,0] neg_hi:[1,0,0]
	v_cvt_pk_bf16_f32 v32, v32, v33
	v_cvt_pk_bf16_f32 v33, v30, v31
	ds_write_b64 v186, v[32:33] offset:3264
	ds_read_b32 v30, v187 offset:56
	s_waitcnt lgkmcnt(0)
	v_pk_fma_f32 v[22:23], v[30:31], v[22:23], 0 op_sel_hi:[0,1,0] neg_lo:[1,0,0] neg_hi:[1,0,0]
	v_pk_fma_f32 v[24:25], v[30:31], v[24:25], 0 op_sel_hi:[0,1,0] neg_lo:[1,0,0] neg_hi:[1,0,0]
	v_cvt_pk_bf16_f32 v22, v22, v23
	v_cvt_pk_bf16_f32 v23, v24, v25
	ds_write_b64 v186, v[22:23] offset:3808
	ds_read_b128 a[0:3], v1
	ds_read_b128 a[4:7], v1 offset:64
	ds_read_b128 a[8:11], v1 offset:128
	ds_read_b128 a[12:15], v1 offset:192
	v_lshl_add_u64 v[22:23], v[130:131], 0, s[28:29]
	v_add_co_u32_e32 v24, vcc, s7, v22
	s_nop 1
	v_addc_co_u32_e32 v25, vcc, 0, v23, vcc
	global_load_dwordx4 v[102:105], v[22:23], off nt
	global_load_dwordx4 v[86:89], v[24:25], off nt
	v_add_co_u32_e32 v24, vcc, s36, v22
	s_nop 1
	v_addc_co_u32_e32 v25, vcc, 0, v23, vcc
	v_add_co_u32_e32 v30, vcc, s37, v22
	s_nop 1
	v_addc_co_u32_e32 v31, vcc, 0, v23, vcc
	global_load_dwordx4 v[74:77], v[24:25], off nt
	global_load_dwordx4 v[62:65], v[30:31], off nt
	v_add_co_u32_e32 v24, vcc, s38, v22
	s_nop 1
	v_addc_co_u32_e32 v25, vcc, 0, v23, vcc
	v_add_co_u32_e32 v30, vcc, s39, v22
	s_nop 1
	v_addc_co_u32_e32 v31, vcc, 0, v23, vcc
	global_load_dwordx4 v[58:61], v[24:25], off nt
	global_load_dwordx4 v[46:49], v[30:31], off nt
	v_add_co_u32_e32 v24, vcc, s41, v22
	s_nop 1
	v_addc_co_u32_e32 v25, vcc, 0, v23, vcc
	v_add_co_u32_e32 v22, vcc, s42, v22
	s_nop 1
	v_addc_co_u32_e32 v23, vcc, 0, v23, vcc
	global_load_dwordx4 v[42:45], v[24:25], off nt
	global_load_dwordx4 v[30:33], v[22:23], off nt
	v_mov_b32_e32 v22, v198
	s_waitcnt vmcnt(23)
	s_waitcnt vmcnt(22)
	s_waitcnt vmcnt(21)
	s_waitcnt vmcnt(20)
	s_waitcnt vmcnt(19)
	s_waitcnt vmcnt(18)
	s_waitcnt vmcnt(17)
	s_waitcnt vmcnt(16)
	ds_read_b32 v22, v187 offset:64
	s_waitcnt lgkmcnt(0)
	v_pk_fma_f32 v[24:25], v[22:23], v[94:95], 0 op_sel_hi:[0,1,0] neg_lo:[1,0,0] neg_hi:[1,0,0]
	v_pk_fma_f32 v[22:23], v[22:23], v[96:97], 0 op_sel_hi:[0,1,0] neg_lo:[1,0,0] neg_hi:[1,0,0]
	v_cvt_pk_bf16_f32 v24, v24, v25
	v_cvt_pk_bf16_f32 v25, v22, v23
	ds_write_b64 v186, v[24:25]
	ds_read_b32 v22, v187 offset:72
	s_waitcnt lgkmcnt(0)
	v_pk_fma_f32 v[24:25], v[22:23], v[90:91], 0 op_sel_hi:[0,1,0] neg_lo:[1,0,0] neg_hi:[1,0,0]
	v_pk_fma_f32 v[22:23], v[22:23], v[92:93], 0 op_sel_hi:[0,1,0] neg_lo:[1,0,0] neg_hi:[1,0,0]
	v_cvt_pk_bf16_f32 v24, v24, v25
	v_cvt_pk_bf16_f32 v25, v22, v23
	ds_write_b64 v186, v[24:25] offset:544
	ds_read_b32 v22, v187 offset:80
	s_waitcnt lgkmcnt(0)
	v_pk_fma_f32 v[24:25], v[22:23], v[82:83], 0 op_sel_hi:[0,1,0] neg_lo:[1,0,0] neg_hi:[1,0,0]
	v_pk_fma_f32 v[22:23], v[22:23], v[84:85], 0 op_sel_hi:[0,1,0] neg_lo:[1,0,0] neg_hi:[1,0,0]
	v_cvt_pk_bf16_f32 v24, v24, v25
	v_cvt_pk_bf16_f32 v25, v22, v23
	ds_write_b64 v186, v[24:25] offset:1088
	ds_read_b32 v22, v187 offset:88
	s_waitcnt lgkmcnt(0)
	v_pk_fma_f32 v[24:25], v[22:23], v[70:71], 0 op_sel_hi:[0,1,0] neg_lo:[1,0,0] neg_hi:[1,0,0]
	v_pk_fma_f32 v[22:23], v[22:23], v[72:73], 0 op_sel_hi:[0,1,0] neg_lo:[1,0,0] neg_hi:[1,0,0]
	v_cvt_pk_bf16_f32 v24, v24, v25
	v_cvt_pk_bf16_f32 v25, v22, v23
	ds_write_b64 v186, v[24:25] offset:1632
	ds_read_b32 v22, v187 offset:96
	s_waitcnt lgkmcnt(0)
	v_pk_fma_f32 v[24:25], v[22:23], v[54:55], 0 op_sel_hi:[0,1,0] neg_lo:[1,0,0] neg_hi:[1,0,0]
	v_pk_fma_f32 v[22:23], v[22:23], v[56:57], 0 op_sel_hi:[0,1,0] neg_lo:[1,0,0] neg_hi:[1,0,0]
	v_cvt_pk_bf16_f32 v24, v24, v25
	v_cvt_pk_bf16_f32 v25, v22, v23
	ds_write_b64 v186, v[24:25] offset:2176
	ds_read_b32 v22, v187 offset:104
	s_waitcnt lgkmcnt(0)
	v_pk_fma_f32 v[24:25], v[22:23], v[26:27], 0 op_sel_hi:[0,1,0] neg_lo:[1,0,0] neg_hi:[1,0,0]
	v_pk_fma_f32 v[22:23], v[22:23], v[28:29], 0 op_sel_hi:[0,1,0] neg_lo:[1,0,0] neg_hi:[1,0,0]
	v_cvt_pk_bf16_f32 v24, v24, v25
	v_cvt_pk_bf16_f32 v25, v22, v23
	ds_write_b64 v186, v[24:25] offset:2720
	ds_read_b32 v22, v187 offset:112
	s_waitcnt lgkmcnt(0)
	v_pk_fma_f32 v[14:15], v[22:23], v[14:15], 0 op_sel_hi:[0,1,0] neg_lo:[1,0,0] neg_hi:[1,0,0]
	v_pk_fma_f32 v[16:17], v[22:23], v[16:17], 0 op_sel_hi:[0,1,0] neg_lo:[1,0,0] neg_hi:[1,0,0]
	v_cvt_pk_bf16_f32 v14, v14, v15
	v_cvt_pk_bf16_f32 v15, v16, v17
	ds_write_b64 v186, v[14:15] offset:3264
	ds_read_b32 v14, v187 offset:120
	s_waitcnt lgkmcnt(0)
	v_pk_fma_f32 v[6:7], v[14:15], v[6:7], 0 op_sel_hi:[0,1,0] neg_lo:[1,0,0] neg_hi:[1,0,0]
	v_pk_fma_f32 v[8:9], v[14:15], v[8:9], 0 op_sel_hi:[0,1,0] neg_lo:[1,0,0] neg_hi:[1,0,0]
	v_cvt_pk_bf16_f32 v6, v6, v7
	v_cvt_pk_bf16_f32 v7, v8, v9
	ds_write_b64 v186, v[6:7] offset:3808
	ds_read_b128 a[16:19], v1
	ds_read_b128 a[20:23], v1 offset:64
	ds_read_b128 a[24:27], v1 offset:128
	ds_read_b128 a[28:31], v1 offset:192
	v_lshl_add_u64 v[6:7], v[150:151], 0, s[28:29]
	v_lshl_add_u64 v[8:9], v[152:153], 0, s[28:29]
	v_lshl_add_u64 v[14:15], v[156:157], 0, s[28:29]
	v_lshl_add_u64 v[16:17], v[158:159], 0, s[28:29]
	v_lshl_add_u64 v[22:23], v[160:161], 0, s[28:29]
	v_lshl_add_u64 v[24:25], v[162:163], 0, s[28:29]
	v_lshl_add_u64 v[26:27], v[164:165], 0, s[28:29]
	v_lshl_add_u64 v[28:29], v[166:167], 0, s[28:29]
	global_load_dwordx4 v[110:113], v[6:7], off nt
	global_load_dwordx4 v[90:93], v[8:9], off nt
	global_load_dwordx4 v[70:73], v[14:15], off nt
	global_load_dwordx4 v[50:53], v[16:17], off nt
	global_load_dwordx4 v[34:37], v[22:23], off nt
	s_nop 0
	global_load_dwordx4 v[22:25], v[24:25], off nt
	s_nop 0
	global_load_dwordx4 v[14:17], v[26:27], off nt
	global_load_dwordx4 v[6:9], v[28:29], off nt
	s_waitcnt vmcnt(23)
	s_waitcnt vmcnt(22)
	s_waitcnt vmcnt(21)
	s_waitcnt vmcnt(20)
	s_waitcnt vmcnt(19)
	s_waitcnt vmcnt(18)
	s_waitcnt vmcnt(17)
	s_waitcnt vmcnt(16)
	ds_read_b32 v26, v187 offset:128
	s_waitcnt lgkmcnt(0)
	v_pk_fma_f32 v[28:29], v[26:27], v[106:107], 0 op_sel_hi:[0,1,0] neg_lo:[1,0,0] neg_hi:[1,0,0]
	v_pk_fma_f32 v[26:27], v[26:27], v[108:109], 0 op_sel_hi:[0,1,0] neg_lo:[1,0,0] neg_hi:[1,0,0]
	v_cvt_pk_bf16_f32 v28, v28, v29
	v_cvt_pk_bf16_f32 v29, v26, v27
	ds_write_b64 v186, v[28:29]
	ds_read_b32 v26, v187 offset:136
	s_waitcnt lgkmcnt(0)
	v_pk_fma_f32 v[28:29], v[26:27], v[98:99], 0 op_sel_hi:[0,1,0] neg_lo:[1,0,0] neg_hi:[1,0,0]
	v_pk_fma_f32 v[26:27], v[26:27], v[100:101], 0 op_sel_hi:[0,1,0] neg_lo:[1,0,0] neg_hi:[1,0,0]
	v_cvt_pk_bf16_f32 v28, v28, v29
	v_cvt_pk_bf16_f32 v29, v26, v27
	ds_write_b64 v186, v[28:29] offset:544
	ds_read_b32 v26, v187 offset:144
	s_waitcnt lgkmcnt(0)
	v_pk_fma_f32 v[28:29], v[26:27], v[78:79], 0 op_sel_hi:[0,1,0] neg_lo:[1,0,0] neg_hi:[1,0,0]
	v_pk_fma_f32 v[26:27], v[26:27], v[80:81], 0 op_sel_hi:[0,1,0] neg_lo:[1,0,0] neg_hi:[1,0,0]
	v_cvt_pk_bf16_f32 v28, v28, v29
	v_cvt_pk_bf16_f32 v29, v26, v27
	ds_write_b64 v186, v[28:29] offset:1088
	ds_read_b32 v26, v187 offset:152
	s_waitcnt lgkmcnt(0)
	v_pk_fma_f32 v[28:29], v[26:27], v[66:67], 0 op_sel_hi:[0,1,0] neg_lo:[1,0,0] neg_hi:[1,0,0]
	v_pk_fma_f32 v[26:27], v[26:27], v[68:69], 0 op_sel_hi:[0,1,0] neg_lo:[1,0,0] neg_hi:[1,0,0]
	v_cvt_pk_bf16_f32 v28, v28, v29
	v_cvt_pk_bf16_f32 v29, v26, v27
	ds_write_b64 v186, v[28:29] offset:1632
	ds_read_b32 v26, v187 offset:160
	s_waitcnt lgkmcnt(0)
	v_pk_fma_f32 v[28:29], v[26:27], v[38:39], 0 op_sel_hi:[0,1,0] neg_lo:[1,0,0] neg_hi:[1,0,0]
	v_pk_fma_f32 v[26:27], v[26:27], v[40:41], 0 op_sel_hi:[0,1,0] neg_lo:[1,0,0] neg_hi:[1,0,0]
	v_cvt_pk_bf16_f32 v28, v28, v29
	v_cvt_pk_bf16_f32 v29, v26, v27
	ds_write_b64 v186, v[28:29] offset:2176
	ds_read_b32 v26, v187 offset:168
	s_waitcnt lgkmcnt(0)
	v_pk_fma_f32 v[18:19], v[26:27], v[18:19], 0 op_sel_hi:[0,1,0] neg_lo:[1,0,0] neg_hi:[1,0,0]
	v_pk_fma_f32 v[20:21], v[26:27], v[20:21], 0 op_sel_hi:[0,1,0] neg_lo:[1,0,0] neg_hi:[1,0,0]
	v_cvt_pk_bf16_f32 v18, v18, v19
	v_cvt_pk_bf16_f32 v19, v20, v21
	ds_write_b64 v186, v[18:19] offset:2720
	ds_read_b32 v18, v187 offset:176
	s_waitcnt lgkmcnt(0)
	v_pk_fma_f32 v[10:11], v[18:19], v[10:11], 0 op_sel_hi:[0,1,0] neg_lo:[1,0,0] neg_hi:[1,0,0]
	v_pk_fma_f32 v[12:13], v[18:19], v[12:13], 0 op_sel_hi:[0,1,0] neg_lo:[1,0,0] neg_hi:[1,0,0]
	v_cvt_pk_bf16_f32 v10, v10, v11
	v_cvt_pk_bf16_f32 v11, v12, v13
	ds_write_b64 v186, v[10:11] offset:3264
	ds_read_b32 v10, v187 offset:184
	s_waitcnt lgkmcnt(0)
	v_pk_fma_f32 v[2:3], v[10:11], v[2:3], 0 op_sel_hi:[0,1,0] neg_lo:[1,0,0] neg_hi:[1,0,0]
	v_pk_fma_f32 v[4:5], v[10:11], v[4:5], 0 op_sel_hi:[0,1,0] neg_lo:[1,0,0] neg_hi:[1,0,0]
	v_cvt_pk_bf16_f32 v2, v2, v3
	v_cvt_pk_bf16_f32 v3, v4, v5
	ds_write_b64 v186, v[2:3] offset:3808
	ds_read_b128 a[32:35], v1
	ds_read_b128 a[36:39], v1 offset:64
	ds_read_b128 a[40:43], v1 offset:128
	ds_read_b128 a[44:47], v1 offset:192
	v_lshl_add_u64 v[2:3], v[168:169], 0, s[28:29]
	v_lshl_add_u64 v[4:5], v[170:171], 0, s[28:29]
	v_lshl_add_u64 v[10:11], v[172:173], 0, s[28:29]
	v_lshl_add_u64 v[12:13], v[174:175], 0, s[28:29]
	v_lshl_add_u64 v[18:19], v[176:177], 0, s[28:29]
	v_lshl_add_u64 v[20:21], v[178:179], 0, s[28:29]
	v_lshl_add_u64 v[26:27], v[180:181], 0, s[28:29]
	v_lshl_add_u64 v[28:29], v[182:183], 0, s[28:29]
	global_load_dwordx4 v[106:109], v[2:3], off nt
	global_load_dwordx4 v[94:97], v[4:5], off nt
	global_load_dwordx4 v[66:69], v[10:11], off nt
	global_load_dwordx4 v[54:57], v[12:13], off nt
	global_load_dwordx4 v[38:41], v[18:19], off nt
	s_nop 0
	global_load_dwordx4 v[18:21], v[20:21], off nt
	s_nop 0
	global_load_dwordx4 v[10:13], v[26:27], off nt
	global_load_dwordx4 v[2:5], v[28:29], off nt
	v_mov_b32_e32 v26, v197
	s_waitcnt vmcnt(23)
	s_waitcnt vmcnt(22)
	s_waitcnt vmcnt(21)
	s_waitcnt vmcnt(20)
	s_waitcnt vmcnt(19)
	s_waitcnt vmcnt(18)
	s_waitcnt vmcnt(17)
	s_waitcnt vmcnt(16)
	ds_read_b32 v26, v187
	s_waitcnt lgkmcnt(0)
	v_pk_fma_f32 v[28:29], v[26:27], v[102:103], 0 op_sel_hi:[0,1,0] neg_lo:[1,0,0] neg_hi:[1,0,0]
	v_pk_fma_f32 v[26:27], v[26:27], v[104:105], 0 op_sel_hi:[0,1,0] neg_lo:[1,0,0] neg_hi:[1,0,0]
	v_cvt_pk_bf16_f32 v28, v28, v29
	v_cvt_pk_bf16_f32 v29, v26, v27
	ds_write_b64 v186, v[28:29]
	ds_read_b32 v26, v187 offset:8
	s_waitcnt lgkmcnt(0)
	v_pk_fma_f32 v[28:29], v[26:27], v[86:87], 0 op_sel_hi:[0,1,0] neg_lo:[1,0,0] neg_hi:[1,0,0]
	v_pk_fma_f32 v[26:27], v[26:27], v[88:89], 0 op_sel_hi:[0,1,0] neg_lo:[1,0,0] neg_hi:[1,0,0]
	v_cvt_pk_bf16_f32 v28, v28, v29
	v_cvt_pk_bf16_f32 v29, v26, v27
	ds_write_b64 v186, v[28:29] offset:544
	ds_read_b32 v26, v187 offset:16
	s_waitcnt lgkmcnt(0)
	v_pk_fma_f32 v[28:29], v[26:27], v[74:75], 0 op_sel_hi:[0,1,0] neg_lo:[1,0,0] neg_hi:[1,0,0]
	v_pk_fma_f32 v[26:27], v[26:27], v[76:77], 0 op_sel_hi:[0,1,0] neg_lo:[1,0,0] neg_hi:[1,0,0]
	v_cvt_pk_bf16_f32 v28, v28, v29
	v_cvt_pk_bf16_f32 v29, v26, v27
	ds_write_b64 v186, v[28:29] offset:1088
	ds_read_b32 v26, v187 offset:24
	s_waitcnt lgkmcnt(0)
	v_pk_fma_f32 v[28:29], v[26:27], v[62:63], 0 op_sel_hi:[0,1,0] neg_lo:[1,0,0] neg_hi:[1,0,0]
	v_pk_fma_f32 v[26:27], v[26:27], v[64:65], 0 op_sel_hi:[0,1,0] neg_lo:[1,0,0] neg_hi:[1,0,0]
	v_cvt_pk_bf16_f32 v28, v28, v29
	v_cvt_pk_bf16_f32 v29, v26, v27
	ds_write_b64 v186, v[28:29] offset:1632
	ds_read_b32 v26, v187 offset:32
	s_waitcnt lgkmcnt(0)
	v_pk_fma_f32 v[28:29], v[26:27], v[58:59], 0 op_sel_hi:[0,1,0] neg_lo:[1,0,0] neg_hi:[1,0,0]
	v_pk_fma_f32 v[26:27], v[26:27], v[60:61], 0 op_sel_hi:[0,1,0] neg_lo:[1,0,0] neg_hi:[1,0,0]
	v_cvt_pk_bf16_f32 v28, v28, v29
	v_cvt_pk_bf16_f32 v29, v26, v27
	ds_write_b64 v186, v[28:29] offset:2176
	ds_read_b32 v26, v187 offset:40
	s_waitcnt lgkmcnt(0)
	v_pk_fma_f32 v[28:29], v[26:27], v[46:47], 0 op_sel_hi:[0,1,0] neg_lo:[1,0,0] neg_hi:[1,0,0]
	v_pk_fma_f32 v[26:27], v[26:27], v[48:49], 0 op_sel_hi:[0,1,0] neg_lo:[1,0,0] neg_hi:[1,0,0]
	v_cvt_pk_bf16_f32 v28, v28, v29
	v_cvt_pk_bf16_f32 v29, v26, v27
	ds_write_b64 v186, v[28:29] offset:2720
	ds_read_b32 v26, v187 offset:48
	s_waitcnt lgkmcnt(0)
	v_pk_fma_f32 v[28:29], v[26:27], v[42:43], 0 op_sel_hi:[0,1,0] neg_lo:[1,0,0] neg_hi:[1,0,0]
	v_pk_fma_f32 v[26:27], v[26:27], v[44:45], 0 op_sel_hi:[0,1,0] neg_lo:[1,0,0] neg_hi:[1,0,0]
	v_cvt_pk_bf16_f32 v28, v28, v29
	v_cvt_pk_bf16_f32 v29, v26, v27
	ds_write_b64 v186, v[28:29] offset:3264
	ds_read_b32 v26, v187 offset:56
	s_waitcnt lgkmcnt(0)
	v_pk_fma_f32 v[28:29], v[26:27], v[30:31], 0 op_sel_hi:[0,1,0] neg_lo:[1,0,0] neg_hi:[1,0,0]
	v_pk_fma_f32 v[26:27], v[26:27], v[32:33], 0 op_sel_hi:[0,1,0] neg_lo:[1,0,0] neg_hi:[1,0,0]
	v_cvt_pk_bf16_f32 v28, v28, v29
	v_cvt_pk_bf16_f32 v29, v26, v27
	ds_write_b64 v186, v[28:29] offset:3808
	ds_read_b128 a[48:51], v1
	ds_read_b128 a[52:55], v1 offset:64
	ds_read_b128 a[56:59], v1 offset:128
	ds_read_b128 a[60:63], v1 offset:192
	v_lshl_add_u64 v[26:27], v[130:131], 0, s[26:27]
	v_add_co_u32_e32 v28, vcc, s7, v26
	s_nop 1
	v_addc_co_u32_e32 v29, vcc, 0, v27, vcc
	global_load_dwordx4 v[86:89], v[26:27], off nt
	global_load_dwordx4 v[82:85], v[28:29], off nt
	v_add_co_u32_e32 v28, vcc, s36, v26
	s_nop 1
	v_addc_co_u32_e32 v29, vcc, 0, v27, vcc
	v_add_co_u32_e32 v30, vcc, s37, v26
	s_nop 1
	v_addc_co_u32_e32 v31, vcc, 0, v27, vcc
	global_load_dwordx4 v[78:81], v[28:29], off nt
	global_load_dwordx4 v[58:61], v[30:31], off nt
	v_add_co_u32_e32 v28, vcc, s38, v26
	s_nop 1
	v_addc_co_u32_e32 v29, vcc, 0, v27, vcc
	v_add_co_u32_e32 v30, vcc, s39, v26
	s_nop 1
	v_addc_co_u32_e32 v31, vcc, 0, v27, vcc
	global_load_dwordx4 v[46:49], v[28:29], off nt
	global_load_dwordx4 v[42:45], v[30:31], off nt
	v_add_co_u32_e32 v28, vcc, s41, v26
	s_nop 1
	v_addc_co_u32_e32 v29, vcc, 0, v27, vcc
	v_add_co_u32_e32 v26, vcc, s42, v26
	s_nop 1
	v_addc_co_u32_e32 v27, vcc, 0, v27, vcc
	global_load_dwordx4 v[30:33], v[28:29], off nt
	s_nop 0
	global_load_dwordx4 v[26:29], v[26:27], off nt
	v_mov_b32_e32 v62, v197
	s_waitcnt vmcnt(23)
	s_waitcnt vmcnt(22)
	s_waitcnt vmcnt(21)
	s_waitcnt vmcnt(20)
	s_waitcnt vmcnt(19)
	s_waitcnt vmcnt(18)
	s_waitcnt vmcnt(17)
	s_waitcnt vmcnt(16)
	ds_read_b32 v62, v187 offset:64
	s_waitcnt lgkmcnt(0)
	v_pk_fma_f32 v[64:65], v[62:63], v[110:111], 0 op_sel_hi:[0,1,0] neg_lo:[1,0,0] neg_hi:[1,0,0]
	v_pk_fma_f32 v[62:63], v[62:63], v[112:113], 0 op_sel_hi:[0,1,0] neg_lo:[1,0,0] neg_hi:[1,0,0]
	v_cvt_pk_bf16_f32 v64, v64, v65
	v_cvt_pk_bf16_f32 v65, v62, v63
	ds_write_b64 v186, v[64:65]
	ds_read_b32 v62, v187 offset:72
	s_waitcnt lgkmcnt(0)
	v_pk_fma_f32 v[64:65], v[62:63], v[90:91], 0 op_sel_hi:[0,1,0] neg_lo:[1,0,0] neg_hi:[1,0,0]
	v_pk_fma_f32 v[62:63], v[62:63], v[92:93], 0 op_sel_hi:[0,1,0] neg_lo:[1,0,0] neg_hi:[1,0,0]
	v_cvt_pk_bf16_f32 v64, v64, v65
	v_cvt_pk_bf16_f32 v65, v62, v63
	ds_write_b64 v186, v[64:65] offset:544
	ds_read_b32 v62, v187 offset:80
	s_waitcnt lgkmcnt(0)
	v_pk_fma_f32 v[64:65], v[62:63], v[70:71], 0 op_sel_hi:[0,1,0] neg_lo:[1,0,0] neg_hi:[1,0,0]
	v_pk_fma_f32 v[62:63], v[62:63], v[72:73], 0 op_sel_hi:[0,1,0] neg_lo:[1,0,0] neg_hi:[1,0,0]
	v_cvt_pk_bf16_f32 v64, v64, v65
	v_cvt_pk_bf16_f32 v65, v62, v63
	ds_write_b64 v186, v[64:65] offset:1088
	ds_read_b32 v62, v187 offset:88
	s_waitcnt lgkmcnt(0)
	v_pk_fma_f32 v[50:51], v[62:63], v[50:51], 0 op_sel_hi:[0,1,0] neg_lo:[1,0,0] neg_hi:[1,0,0]
	v_pk_fma_f32 v[52:53], v[62:63], v[52:53], 0 op_sel_hi:[0,1,0] neg_lo:[1,0,0] neg_hi:[1,0,0]
	v_cvt_pk_bf16_f32 v50, v50, v51
	v_cvt_pk_bf16_f32 v51, v52, v53
	ds_write_b64 v186, v[50:51] offset:1632
	ds_read_b32 v50, v187 offset:96
	s_waitcnt lgkmcnt(0)
	v_pk_fma_f32 v[34:35], v[50:51], v[34:35], 0 op_sel_hi:[0,1,0] neg_lo:[1,0,0] neg_hi:[1,0,0]
	v_pk_fma_f32 v[36:37], v[50:51], v[36:37], 0 op_sel_hi:[0,1,0] neg_lo:[1,0,0] neg_hi:[1,0,0]
	v_cvt_pk_bf16_f32 v34, v34, v35
	v_cvt_pk_bf16_f32 v35, v36, v37
	ds_write_b64 v186, v[34:35] offset:2176
	ds_read_b32 v34, v187 offset:104
	s_waitcnt lgkmcnt(0)
	v_pk_fma_f32 v[22:23], v[34:35], v[22:23], 0 op_sel_hi:[0,1,0] neg_lo:[1,0,0] neg_hi:[1,0,0]
	v_pk_fma_f32 v[24:25], v[34:35], v[24:25], 0 op_sel_hi:[0,1,0] neg_lo:[1,0,0] neg_hi:[1,0,0]
	v_cvt_pk_bf16_f32 v22, v22, v23
	v_cvt_pk_bf16_f32 v23, v24, v25
	ds_write_b64 v186, v[22:23] offset:2720
	ds_read_b32 v22, v187 offset:112
	s_waitcnt lgkmcnt(0)
	v_pk_fma_f32 v[14:15], v[22:23], v[14:15], 0 op_sel_hi:[0,1,0] neg_lo:[1,0,0] neg_hi:[1,0,0]
	v_pk_fma_f32 v[16:17], v[22:23], v[16:17], 0 op_sel_hi:[0,1,0] neg_lo:[1,0,0] neg_hi:[1,0,0]
	v_cvt_pk_bf16_f32 v14, v14, v15
	v_cvt_pk_bf16_f32 v15, v16, v17
	ds_write_b64 v186, v[14:15] offset:3264
	ds_read_b32 v14, v187 offset:120
	s_waitcnt lgkmcnt(0)
	v_pk_fma_f32 v[6:7], v[14:15], v[6:7], 0 op_sel_hi:[0,1,0] neg_lo:[1,0,0] neg_hi:[1,0,0]
	v_pk_fma_f32 v[8:9], v[14:15], v[8:9], 0 op_sel_hi:[0,1,0] neg_lo:[1,0,0] neg_hi:[1,0,0]
	v_cvt_pk_bf16_f32 v6, v6, v7
	v_cvt_pk_bf16_f32 v7, v8, v9
	ds_write_b64 v186, v[6:7] offset:3808
	ds_read_b128 a[64:67], v1
	ds_read_b128 a[68:71], v1 offset:64
	ds_read_b128 a[72:75], v1 offset:128
	ds_read_b128 a[76:79], v1 offset:192
	v_lshl_add_u64 v[6:7], v[150:151], 0, s[26:27]
	v_lshl_add_u64 v[8:9], v[152:153], 0, s[26:27]
	v_lshl_add_u64 v[14:15], v[156:157], 0, s[26:27]
	v_lshl_add_u64 v[16:17], v[158:159], 0, s[26:27]
	v_lshl_add_u64 v[22:23], v[160:161], 0, s[26:27]
	v_lshl_add_u64 v[24:25], v[162:163], 0, s[26:27]
	v_lshl_add_u64 v[70:71], v[164:165], 0, s[26:27]
	v_lshl_add_u64 v[72:73], v[166:167], 0, s[26:27]
	global_load_dwordx4 v[110:113], v[6:7], off nt
	global_load_dwordx4 v[98:101], v[8:9], off nt
	global_load_dwordx4 v[62:65], v[14:15], off nt
	global_load_dwordx4 v[50:53], v[16:17], off nt
	global_load_dwordx4 v[34:37], v[22:23], off nt
	s_nop 0
	global_load_dwordx4 v[22:25], v[24:25], off nt
	s_nop 0
	global_load_dwordx4 v[14:17], v[70:71], off nt
	global_load_dwordx4 v[6:9], v[72:73], off nt
	s_waitcnt vmcnt(23)
	s_waitcnt vmcnt(22)
	s_waitcnt vmcnt(21)
	s_waitcnt vmcnt(20)
	s_waitcnt vmcnt(19)
	s_waitcnt vmcnt(18)
	s_waitcnt vmcnt(17)
	s_waitcnt vmcnt(16)
	ds_read_b32 v70, v187 offset:128
	s_waitcnt lgkmcnt(0)
	v_pk_fma_f32 v[72:73], v[70:71], v[106:107], 0 op_sel_hi:[0,1,0] neg_lo:[1,0,0] neg_hi:[1,0,0]
	v_pk_fma_f32 v[70:71], v[70:71], v[108:109], 0 op_sel_hi:[0,1,0] neg_lo:[1,0,0] neg_hi:[1,0,0]
	v_cvt_pk_bf16_f32 v72, v72, v73
	v_cvt_pk_bf16_f32 v73, v70, v71
	ds_write_b64 v186, v[72:73]
	ds_read_b32 v70, v187 offset:136
	s_waitcnt lgkmcnt(0)
	v_pk_fma_f32 v[72:73], v[70:71], v[94:95], 0 op_sel_hi:[0,1,0] neg_lo:[1,0,0] neg_hi:[1,0,0]
	v_pk_fma_f32 v[70:71], v[70:71], v[96:97], 0 op_sel_hi:[0,1,0] neg_lo:[1,0,0] neg_hi:[1,0,0]
	v_cvt_pk_bf16_f32 v72, v72, v73
	v_cvt_pk_bf16_f32 v73, v70, v71
	ds_write_b64 v186, v[72:73] offset:544
	ds_read_b32 v70, v187 offset:144
	s_waitcnt lgkmcnt(0)
	v_pk_fma_f32 v[66:67], v[70:71], v[66:67], 0 op_sel_hi:[0,1,0] neg_lo:[1,0,0] neg_hi:[1,0,0]
	v_pk_fma_f32 v[68:69], v[70:71], v[68:69], 0 op_sel_hi:[0,1,0] neg_lo:[1,0,0] neg_hi:[1,0,0]
	v_cvt_pk_bf16_f32 v66, v66, v67
	v_cvt_pk_bf16_f32 v67, v68, v69
	ds_write_b64 v186, v[66:67] offset:1088
	ds_read_b32 v66, v187 offset:152
	s_waitcnt lgkmcnt(0)
	v_pk_fma_f32 v[54:55], v[66:67], v[54:55], 0 op_sel_hi:[0,1,0] neg_lo:[1,0,0] neg_hi:[1,0,0]
	v_pk_fma_f32 v[56:57], v[66:67], v[56:57], 0 op_sel_hi:[0,1,0] neg_lo:[1,0,0] neg_hi:[1,0,0]
	v_cvt_pk_bf16_f32 v54, v54, v55
	v_cvt_pk_bf16_f32 v55, v56, v57
	ds_write_b64 v186, v[54:55] offset:1632
	ds_read_b32 v54, v187 offset:160
	s_waitcnt lgkmcnt(0)
	v_pk_fma_f32 v[38:39], v[54:55], v[38:39], 0 op_sel_hi:[0,1,0] neg_lo:[1,0,0] neg_hi:[1,0,0]
	v_pk_fma_f32 v[40:41], v[54:55], v[40:41], 0 op_sel_hi:[0,1,0] neg_lo:[1,0,0] neg_hi:[1,0,0]
	v_cvt_pk_bf16_f32 v38, v38, v39
	v_cvt_pk_bf16_f32 v39, v40, v41
	ds_write_b64 v186, v[38:39] offset:2176
	ds_read_b32 v38, v187 offset:168
	s_waitcnt lgkmcnt(0)
	v_pk_fma_f32 v[18:19], v[38:39], v[18:19], 0 op_sel_hi:[0,1,0] neg_lo:[1,0,0] neg_hi:[1,0,0]
	v_pk_fma_f32 v[20:21], v[38:39], v[20:21], 0 op_sel_hi:[0,1,0] neg_lo:[1,0,0] neg_hi:[1,0,0]
	v_cvt_pk_bf16_f32 v18, v18, v19
	v_cvt_pk_bf16_f32 v19, v20, v21
	ds_write_b64 v186, v[18:19] offset:2720
	ds_read_b32 v18, v187 offset:176
	s_waitcnt lgkmcnt(0)
	v_pk_fma_f32 v[10:11], v[18:19], v[10:11], 0 op_sel_hi:[0,1,0] neg_lo:[1,0,0] neg_hi:[1,0,0]
	v_pk_fma_f32 v[12:13], v[18:19], v[12:13], 0 op_sel_hi:[0,1,0] neg_lo:[1,0,0] neg_hi:[1,0,0]
	v_cvt_pk_bf16_f32 v10, v10, v11
	v_cvt_pk_bf16_f32 v11, v12, v13
	ds_write_b64 v186, v[10:11] offset:3264
	ds_read_b32 v10, v187 offset:184
	s_waitcnt lgkmcnt(0)
	v_pk_fma_f32 v[2:3], v[10:11], v[2:3], 0 op_sel_hi:[0,1,0] neg_lo:[1,0,0] neg_hi:[1,0,0]
	v_pk_fma_f32 v[4:5], v[10:11], v[4:5], 0 op_sel_hi:[0,1,0] neg_lo:[1,0,0] neg_hi:[1,0,0]
	v_cvt_pk_bf16_f32 v2, v2, v3
	v_cvt_pk_bf16_f32 v3, v4, v5
	ds_write_b64 v186, v[2:3] offset:3808
	ds_read_b128 a[80:83], v1
	ds_read_b128 a[84:87], v1 offset:64
	ds_read_b128 a[88:91], v1 offset:128
	ds_read_b128 a[92:95], v1 offset:192
	v_lshl_add_u64 v[2:3], v[168:169], 0, s[26:27]
	v_lshl_add_u64 v[4:5], v[170:171], 0, s[26:27]
	v_lshl_add_u64 v[10:11], v[172:173], 0, s[26:27]
	v_lshl_add_u64 v[12:13], v[174:175], 0, s[26:27]
	v_lshl_add_u64 v[18:19], v[176:177], 0, s[26:27]
	v_lshl_add_u64 v[20:21], v[178:179], 0, s[26:27]
	v_lshl_add_u64 v[66:67], v[180:181], 0, s[26:27]
	v_lshl_add_u64 v[68:69], v[182:183], 0, s[26:27]
	global_load_dwordx4 v[106:109], v[2:3], off nt
	global_load_dwordx4 v[94:97], v[4:5], off nt
	global_load_dwordx4 v[74:77], v[10:11], off nt
	global_load_dwordx4 v[54:57], v[12:13], off nt
	global_load_dwordx4 v[38:41], v[18:19], off nt
	s_nop 0
	global_load_dwordx4 v[18:21], v[20:21], off nt
	s_nop 0
	global_load_dwordx4 v[10:13], v[66:67], off nt
	global_load_dwordx4 v[2:5], v[68:69], off nt
	v_mov_b32_e32 v66, v196
	s_waitcnt vmcnt(23)
	s_waitcnt vmcnt(22)
	s_waitcnt vmcnt(21)
	s_waitcnt vmcnt(20)
	s_waitcnt vmcnt(19)
	s_waitcnt vmcnt(18)
	s_waitcnt vmcnt(17)
	s_waitcnt vmcnt(16)
	ds_read_b32 v66, v187
	s_waitcnt lgkmcnt(0)
	v_pk_fma_f32 v[68:69], v[66:67], v[86:87], 0 op_sel_hi:[0,1,0] neg_lo:[1,0,0] neg_hi:[1,0,0]
	v_pk_fma_f32 v[66:67], v[66:67], v[88:89], 0 op_sel_hi:[0,1,0] neg_lo:[1,0,0] neg_hi:[1,0,0]
	v_cvt_pk_bf16_f32 v68, v68, v69
	v_cvt_pk_bf16_f32 v69, v66, v67
	ds_write_b64 v186, v[68:69]
	ds_read_b32 v66, v187 offset:8
	s_waitcnt lgkmcnt(0)
	v_pk_fma_f32 v[68:69], v[66:67], v[82:83], 0 op_sel_hi:[0,1,0] neg_lo:[1,0,0] neg_hi:[1,0,0]
	v_pk_fma_f32 v[66:67], v[66:67], v[84:85], 0 op_sel_hi:[0,1,0] neg_lo:[1,0,0] neg_hi:[1,0,0]
	v_cvt_pk_bf16_f32 v68, v68, v69
	v_cvt_pk_bf16_f32 v69, v66, v67
	ds_write_b64 v186, v[68:69] offset:544
	ds_read_b32 v66, v187 offset:16
	s_waitcnt lgkmcnt(0)
	v_pk_fma_f32 v[68:69], v[66:67], v[78:79], 0 op_sel_hi:[0,1,0] neg_lo:[1,0,0] neg_hi:[1,0,0]
	v_pk_fma_f32 v[66:67], v[66:67], v[80:81], 0 op_sel_hi:[0,1,0] neg_lo:[1,0,0] neg_hi:[1,0,0]
	v_cvt_pk_bf16_f32 v68, v68, v69
	v_cvt_pk_bf16_f32 v69, v66, v67
	ds_write_b64 v186, v[68:69] offset:1088
	ds_read_b32 v66, v187 offset:24
	s_waitcnt lgkmcnt(0)
	v_pk_fma_f32 v[58:59], v[66:67], v[58:59], 0 op_sel_hi:[0,1,0] neg_lo:[1,0,0] neg_hi:[1,0,0]
	v_pk_fma_f32 v[60:61], v[66:67], v[60:61], 0 op_sel_hi:[0,1,0] neg_lo:[1,0,0] neg_hi:[1,0,0]
	v_cvt_pk_bf16_f32 v58, v58, v59
	v_cvt_pk_bf16_f32 v59, v60, v61
	ds_write_b64 v186, v[58:59] offset:1632
	ds_read_b32 v58, v187 offset:32
	s_waitcnt lgkmcnt(0)
	v_pk_fma_f32 v[46:47], v[58:59], v[46:47], 0 op_sel_hi:[0,1,0] neg_lo:[1,0,0] neg_hi:[1,0,0]
	v_pk_fma_f32 v[48:49], v[58:59], v[48:49], 0 op_sel_hi:[0,1,0] neg_lo:[1,0,0] neg_hi:[1,0,0]
	v_cvt_pk_bf16_f32 v46, v46, v47
	v_cvt_pk_bf16_f32 v47, v48, v49
	ds_write_b64 v186, v[46:47] offset:2176
	ds_read_b32 v46, v187 offset:40
	s_waitcnt lgkmcnt(0)
	v_pk_fma_f32 v[42:43], v[46:47], v[42:43], 0 op_sel_hi:[0,1,0] neg_lo:[1,0,0] neg_hi:[1,0,0]
	v_pk_fma_f32 v[44:45], v[46:47], v[44:45], 0 op_sel_hi:[0,1,0] neg_lo:[1,0,0] neg_hi:[1,0,0]
	v_cvt_pk_bf16_f32 v42, v42, v43
	v_cvt_pk_bf16_f32 v43, v44, v45
	ds_write_b64 v186, v[42:43] offset:2720
	ds_read_b32 v42, v187 offset:48
	s_waitcnt lgkmcnt(0)
	v_pk_fma_f32 v[30:31], v[42:43], v[30:31], 0 op_sel_hi:[0,1,0] neg_lo:[1,0,0] neg_hi:[1,0,0]
	v_pk_fma_f32 v[32:33], v[42:43], v[32:33], 0 op_sel_hi:[0,1,0] neg_lo:[1,0,0] neg_hi:[1,0,0]
	v_cvt_pk_bf16_f32 v30, v30, v31
	v_cvt_pk_bf16_f32 v31, v32, v33
	ds_write_b64 v186, v[30:31] offset:3264
	ds_read_b32 v30, v187 offset:56
	s_waitcnt lgkmcnt(0)
	v_pk_fma_f32 v[26:27], v[30:31], v[26:27], 0 op_sel_hi:[0,1,0] neg_lo:[1,0,0] neg_hi:[1,0,0]
	v_pk_fma_f32 v[28:29], v[30:31], v[28:29], 0 op_sel_hi:[0,1,0] neg_lo:[1,0,0] neg_hi:[1,0,0]
	v_cvt_pk_bf16_f32 v26, v26, v27
	v_cvt_pk_bf16_f32 v27, v28, v29
	ds_write_b64 v186, v[26:27] offset:3808
	ds_read_b128 a[96:99], v1
	ds_read_b128 a[100:103], v1 offset:64
	ds_read_b128 a[104:107], v1 offset:128
	ds_read_b128 a[108:111], v1 offset:192
	v_lshl_add_u64 v[26:27], v[130:131], 0, s[24:25]
	v_add_co_u32_e32 v28, vcc, s7, v26
	s_nop 1
	v_addc_co_u32_e32 v29, vcc, 0, v27, vcc
	global_load_dwordx4 v[102:105], v[26:27], off nt
	global_load_dwordx4 v[90:93], v[28:29], off nt
	v_add_co_u32_e32 v28, vcc, s36, v26
	s_nop 1
	v_addc_co_u32_e32 v29, vcc, 0, v27, vcc
	v_add_co_u32_e32 v30, vcc, s37, v26
	s_nop 1
	v_addc_co_u32_e32 v31, vcc, 0, v27, vcc
	global_load_dwordx4 v[86:89], v[28:29], off nt
	global_load_dwordx4 v[70:73], v[30:31], off nt
	v_add_co_u32_e32 v28, vcc, s38, v26
	s_nop 1
	v_addc_co_u32_e32 v29, vcc, 0, v27, vcc
	v_add_co_u32_e32 v30, vcc, s39, v26
	s_nop 1
	v_addc_co_u32_e32 v31, vcc, 0, v27, vcc
	global_load_dwordx4 v[66:69], v[28:29], off nt
	global_load_dwordx4 v[46:49], v[30:31], off nt
	v_add_co_u32_e32 v28, vcc, s41, v26
	s_nop 1
	v_addc_co_u32_e32 v29, vcc, 0, v27, vcc
	v_add_co_u32_e32 v26, vcc, s42, v26
	s_nop 1
	v_addc_co_u32_e32 v27, vcc, 0, v27, vcc
	global_load_dwordx4 v[42:45], v[28:29], off nt
	global_load_dwordx4 v[30:33], v[26:27], off nt
	v_mov_b32_e32 v26, v196
	s_waitcnt vmcnt(23)
	s_waitcnt vmcnt(22)
	s_waitcnt vmcnt(21)
	s_waitcnt vmcnt(20)
	s_waitcnt vmcnt(19)
	s_waitcnt vmcnt(18)
	s_waitcnt vmcnt(17)
	s_waitcnt vmcnt(16)
	ds_read_b32 v26, v187 offset:64
	s_waitcnt lgkmcnt(0)
	v_pk_fma_f32 v[28:29], v[26:27], v[110:111], 0 op_sel_hi:[0,1,0] neg_lo:[1,0,0] neg_hi:[1,0,0]
	v_pk_fma_f32 v[26:27], v[26:27], v[112:113], 0 op_sel_hi:[0,1,0] neg_lo:[1,0,0] neg_hi:[1,0,0]
	v_cvt_pk_bf16_f32 v28, v28, v29
	v_cvt_pk_bf16_f32 v29, v26, v27
	ds_write_b64 v186, v[28:29]
	ds_read_b32 v26, v187 offset:72
	s_waitcnt lgkmcnt(0)
	v_pk_fma_f32 v[28:29], v[26:27], v[98:99], 0 op_sel_hi:[0,1,0] neg_lo:[1,0,0] neg_hi:[1,0,0]
	v_pk_fma_f32 v[26:27], v[26:27], v[100:101], 0 op_sel_hi:[0,1,0] neg_lo:[1,0,0] neg_hi:[1,0,0]
	v_cvt_pk_bf16_f32 v28, v28, v29
	v_cvt_pk_bf16_f32 v29, v26, v27
	ds_write_b64 v186, v[28:29] offset:544
	ds_read_b32 v26, v187 offset:80
	s_waitcnt lgkmcnt(0)
	v_pk_fma_f32 v[28:29], v[26:27], v[62:63], 0 op_sel_hi:[0,1,0] neg_lo:[1,0,0] neg_hi:[1,0,0]
	v_pk_fma_f32 v[26:27], v[26:27], v[64:65], 0 op_sel_hi:[0,1,0] neg_lo:[1,0,0] neg_hi:[1,0,0]
	v_cvt_pk_bf16_f32 v28, v28, v29
	v_cvt_pk_bf16_f32 v29, v26, v27
	ds_write_b64 v186, v[28:29] offset:1088
	ds_read_b32 v26, v187 offset:88
	s_waitcnt lgkmcnt(0)
	v_pk_fma_f32 v[28:29], v[26:27], v[50:51], 0 op_sel_hi:[0,1,0] neg_lo:[1,0,0] neg_hi:[1,0,0]
	v_pk_fma_f32 v[26:27], v[26:27], v[52:53], 0 op_sel_hi:[0,1,0] neg_lo:[1,0,0] neg_hi:[1,0,0]
	v_cvt_pk_bf16_f32 v28, v28, v29
	v_cvt_pk_bf16_f32 v29, v26, v27
	ds_write_b64 v186, v[28:29] offset:1632
	ds_read_b32 v26, v187 offset:96
	s_waitcnt lgkmcnt(0)
	v_pk_fma_f32 v[28:29], v[26:27], v[34:35], 0 op_sel_hi:[0,1,0] neg_lo:[1,0,0] neg_hi:[1,0,0]
	v_pk_fma_f32 v[26:27], v[26:27], v[36:37], 0 op_sel_hi:[0,1,0] neg_lo:[1,0,0] neg_hi:[1,0,0]
	v_cvt_pk_bf16_f32 v28, v28, v29
	v_cvt_pk_bf16_f32 v29, v26, v27
	ds_write_b64 v186, v[28:29] offset:2176
	ds_read_b32 v26, v187 offset:104
	s_waitcnt lgkmcnt(0)
	v_pk_fma_f32 v[22:23], v[26:27], v[22:23], 0 op_sel_hi:[0,1,0] neg_lo:[1,0,0] neg_hi:[1,0,0]
	v_pk_fma_f32 v[24:25], v[26:27], v[24:25], 0 op_sel_hi:[0,1,0] neg_lo:[1,0,0] neg_hi:[1,0,0]
	v_cvt_pk_bf16_f32 v22, v22, v23
	v_cvt_pk_bf16_f32 v23, v24, v25
	ds_write_b64 v186, v[22:23] offset:2720
	ds_read_b32 v22, v187 offset:112
	s_waitcnt lgkmcnt(0)
	v_pk_fma_f32 v[14:15], v[22:23], v[14:15], 0 op_sel_hi:[0,1,0] neg_lo:[1,0,0] neg_hi:[1,0,0]
	v_pk_fma_f32 v[16:17], v[22:23], v[16:17], 0 op_sel_hi:[0,1,0] neg_lo:[1,0,0] neg_hi:[1,0,0]
	v_cvt_pk_bf16_f32 v14, v14, v15
	v_cvt_pk_bf16_f32 v15, v16, v17
	ds_write_b64 v186, v[14:15] offset:3264
	ds_read_b32 v14, v187 offset:120
	s_waitcnt lgkmcnt(0)
	v_pk_fma_f32 v[6:7], v[14:15], v[6:7], 0 op_sel_hi:[0,1,0] neg_lo:[1,0,0] neg_hi:[1,0,0]
	v_pk_fma_f32 v[8:9], v[14:15], v[8:9], 0 op_sel_hi:[0,1,0] neg_lo:[1,0,0] neg_hi:[1,0,0]
	v_cvt_pk_bf16_f32 v6, v6, v7
	v_cvt_pk_bf16_f32 v7, v8, v9
	ds_write_b64 v186, v[6:7] offset:3808
	ds_read_b128 a[112:115], v1
	ds_read_b128 a[116:119], v1 offset:64
	ds_read_b128 a[120:123], v1 offset:128
	ds_read_b128 a[124:127], v1 offset:192
	v_lshl_add_u64 v[6:7], v[150:151], 0, s[24:25]
	v_lshl_add_u64 v[8:9], v[152:153], 0, s[24:25]
	v_lshl_add_u64 v[14:15], v[156:157], 0, s[24:25]
	v_lshl_add_u64 v[16:17], v[158:159], 0, s[24:25]
	v_lshl_add_u64 v[22:23], v[160:161], 0, s[24:25]
	v_lshl_add_u64 v[24:25], v[162:163], 0, s[24:25]
	v_lshl_add_u64 v[26:27], v[164:165], 0, s[24:25]
	v_lshl_add_u64 v[28:29], v[166:167], 0, s[24:25]
	global_load_dwordx4 v[110:113], v[6:7], off nt
	global_load_dwordx4 v[98:101], v[8:9], off nt
	global_load_dwordx4 v[78:81], v[14:15], off nt
	global_load_dwordx4 v[58:61], v[16:17], off nt
	global_load_dwordx4 v[34:37], v[22:23], off nt
	s_nop 0
	global_load_dwordx4 v[22:25], v[24:25], off nt
	s_nop 0
	global_load_dwordx4 v[14:17], v[26:27], off nt
	global_load_dwordx4 v[6:9], v[28:29], off nt
	s_waitcnt vmcnt(23)
	s_waitcnt vmcnt(22)
	s_waitcnt vmcnt(21)
	s_waitcnt vmcnt(20)
	s_waitcnt vmcnt(19)
	s_waitcnt vmcnt(18)
	s_waitcnt vmcnt(17)
	s_waitcnt vmcnt(16)
	ds_read_b32 v26, v187 offset:128
	s_waitcnt lgkmcnt(0)
	v_pk_fma_f32 v[28:29], v[26:27], v[106:107], 0 op_sel_hi:[0,1,0] neg_lo:[1,0,0] neg_hi:[1,0,0]
	v_pk_fma_f32 v[26:27], v[26:27], v[108:109], 0 op_sel_hi:[0,1,0] neg_lo:[1,0,0] neg_hi:[1,0,0]
	v_cvt_pk_bf16_f32 v28, v28, v29
	v_cvt_pk_bf16_f32 v29, v26, v27
	ds_write_b64 v186, v[28:29]
	ds_read_b32 v26, v187 offset:136
	s_waitcnt lgkmcnt(0)
	v_pk_fma_f32 v[28:29], v[26:27], v[94:95], 0 op_sel_hi:[0,1,0] neg_lo:[1,0,0] neg_hi:[1,0,0]
	v_pk_fma_f32 v[26:27], v[26:27], v[96:97], 0 op_sel_hi:[0,1,0] neg_lo:[1,0,0] neg_hi:[1,0,0]
	v_cvt_pk_bf16_f32 v28, v28, v29
	v_cvt_pk_bf16_f32 v29, v26, v27
	ds_write_b64 v186, v[28:29] offset:544
	ds_read_b32 v26, v187 offset:144
	s_waitcnt lgkmcnt(0)
	v_pk_fma_f32 v[28:29], v[26:27], v[74:75], 0 op_sel_hi:[0,1,0] neg_lo:[1,0,0] neg_hi:[1,0,0]
	v_pk_fma_f32 v[26:27], v[26:27], v[76:77], 0 op_sel_hi:[0,1,0] neg_lo:[1,0,0] neg_hi:[1,0,0]
	v_cvt_pk_bf16_f32 v28, v28, v29
	v_cvt_pk_bf16_f32 v29, v26, v27
	ds_write_b64 v186, v[28:29] offset:1088
	ds_read_b32 v26, v187 offset:152
	s_waitcnt lgkmcnt(0)
	v_pk_fma_f32 v[28:29], v[26:27], v[54:55], 0 op_sel_hi:[0,1,0] neg_lo:[1,0,0] neg_hi:[1,0,0]
	v_pk_fma_f32 v[26:27], v[26:27], v[56:57], 0 op_sel_hi:[0,1,0] neg_lo:[1,0,0] neg_hi:[1,0,0]
	v_cvt_pk_bf16_f32 v28, v28, v29
	v_cvt_pk_bf16_f32 v29, v26, v27
	ds_write_b64 v186, v[28:29] offset:1632
	ds_read_b32 v26, v187 offset:160
	s_waitcnt lgkmcnt(0)
	v_pk_fma_f32 v[28:29], v[26:27], v[38:39], 0 op_sel_hi:[0,1,0] neg_lo:[1,0,0] neg_hi:[1,0,0]
	v_pk_fma_f32 v[26:27], v[26:27], v[40:41], 0 op_sel_hi:[0,1,0] neg_lo:[1,0,0] neg_hi:[1,0,0]
	v_cvt_pk_bf16_f32 v28, v28, v29
	v_cvt_pk_bf16_f32 v29, v26, v27
	ds_write_b64 v186, v[28:29] offset:2176
	ds_read_b32 v26, v187 offset:168
	s_waitcnt lgkmcnt(0)
	v_pk_fma_f32 v[18:19], v[26:27], v[18:19], 0 op_sel_hi:[0,1,0] neg_lo:[1,0,0] neg_hi:[1,0,0]
	v_pk_fma_f32 v[20:21], v[26:27], v[20:21], 0 op_sel_hi:[0,1,0] neg_lo:[1,0,0] neg_hi:[1,0,0]
	v_cvt_pk_bf16_f32 v18, v18, v19
	v_cvt_pk_bf16_f32 v19, v20, v21
	ds_write_b64 v186, v[18:19] offset:2720
	ds_read_b32 v18, v187 offset:176
	s_waitcnt lgkmcnt(0)
	v_pk_fma_f32 v[10:11], v[18:19], v[10:11], 0 op_sel_hi:[0,1,0] neg_lo:[1,0,0] neg_hi:[1,0,0]
	v_pk_fma_f32 v[12:13], v[18:19], v[12:13], 0 op_sel_hi:[0,1,0] neg_lo:[1,0,0] neg_hi:[1,0,0]
	v_cvt_pk_bf16_f32 v10, v10, v11
	v_cvt_pk_bf16_f32 v11, v12, v13
	ds_write_b64 v186, v[10:11] offset:3264
	ds_read_b32 v10, v187 offset:184
	s_waitcnt lgkmcnt(0)
	v_pk_fma_f32 v[2:3], v[10:11], v[2:3], 0 op_sel_hi:[0,1,0] neg_lo:[1,0,0] neg_hi:[1,0,0]
	v_pk_fma_f32 v[4:5], v[10:11], v[4:5], 0 op_sel_hi:[0,1,0] neg_lo:[1,0,0] neg_hi:[1,0,0]
	v_cvt_pk_bf16_f32 v2, v2, v3
	v_cvt_pk_bf16_f32 v3, v4, v5
	ds_write_b64 v186, v[2:3] offset:3808
	ds_read_b128 a[128:131], v1
	ds_read_b128 a[132:135], v1 offset:64
	ds_read_b128 a[136:139], v1 offset:128
	ds_read_b128 a[140:143], v1 offset:192
	v_lshl_add_u64 v[2:3], v[168:169], 0, s[24:25]
	v_lshl_add_u64 v[4:5], v[170:171], 0, s[24:25]
	v_lshl_add_u64 v[10:11], v[172:173], 0, s[24:25]
	v_lshl_add_u64 v[12:13], v[174:175], 0, s[24:25]
	v_lshl_add_u64 v[18:19], v[176:177], 0, s[24:25]
	v_lshl_add_u64 v[20:21], v[178:179], 0, s[24:25]
	v_lshl_add_u64 v[50:51], v[180:181], 0, s[24:25]
	v_lshl_add_u64 v[52:53], v[182:183], 0, s[24:25]
	global_load_dwordx4 v[114:117], v[2:3], off nt
	global_load_dwordx4 v[94:97], v[4:5], off nt
	global_load_dwordx4 v[82:85], v[10:11], off nt
	global_load_dwordx4 v[62:65], v[12:13], off nt
	global_load_dwordx4 v[38:41], v[18:19], off nt
	global_load_dwordx4 v[26:29], v[20:21], off nt
	s_nop 0
	global_load_dwordx4 v[10:13], v[50:51], off nt
	global_load_dwordx4 v[2:5], v[52:53], off nt
	v_mov_b32_e32 v18, v195
	s_waitcnt vmcnt(23)
	s_waitcnt vmcnt(22)
	s_waitcnt vmcnt(21)
	s_waitcnt vmcnt(20)
	s_waitcnt vmcnt(19)
	s_waitcnt vmcnt(18)
	s_waitcnt vmcnt(17)
	s_waitcnt vmcnt(16)
	ds_read_b32 v18, v187
	s_waitcnt lgkmcnt(0)
	v_pk_fma_f32 v[20:21], v[18:19], v[102:103], 0 op_sel_hi:[0,1,0] neg_lo:[1,0,0] neg_hi:[1,0,0]
	v_pk_fma_f32 v[18:19], v[18:19], v[104:105], 0 op_sel_hi:[0,1,0] neg_lo:[1,0,0] neg_hi:[1,0,0]
	v_cvt_pk_bf16_f32 v20, v20, v21
	v_cvt_pk_bf16_f32 v21, v18, v19
	ds_write_b64 v186, v[20:21]
	ds_read_b32 v18, v187 offset:8
	s_waitcnt lgkmcnt(0)
	v_pk_fma_f32 v[20:21], v[18:19], v[90:91], 0 op_sel_hi:[0,1,0] neg_lo:[1,0,0] neg_hi:[1,0,0]
	v_pk_fma_f32 v[18:19], v[18:19], v[92:93], 0 op_sel_hi:[0,1,0] neg_lo:[1,0,0] neg_hi:[1,0,0]
	v_cvt_pk_bf16_f32 v20, v20, v21
	v_cvt_pk_bf16_f32 v21, v18, v19
	ds_write_b64 v186, v[20:21] offset:544
	ds_read_b32 v18, v187 offset:16
	s_waitcnt lgkmcnt(0)
	v_pk_fma_f32 v[20:21], v[18:19], v[86:87], 0 op_sel_hi:[0,1,0] neg_lo:[1,0,0] neg_hi:[1,0,0]
	v_pk_fma_f32 v[18:19], v[18:19], v[88:89], 0 op_sel_hi:[0,1,0] neg_lo:[1,0,0] neg_hi:[1,0,0]
	v_cvt_pk_bf16_f32 v20, v20, v21
	v_cvt_pk_bf16_f32 v21, v18, v19
	ds_write_b64 v186, v[20:21] offset:1088
	ds_read_b32 v18, v187 offset:24
	s_waitcnt lgkmcnt(0)
	v_pk_fma_f32 v[20:21], v[18:19], v[70:71], 0 op_sel_hi:[0,1,0] neg_lo:[1,0,0] neg_hi:[1,0,0]
	v_pk_fma_f32 v[18:19], v[18:19], v[72:73], 0 op_sel_hi:[0,1,0] neg_lo:[1,0,0] neg_hi:[1,0,0]
	v_cvt_pk_bf16_f32 v20, v20, v21
	v_cvt_pk_bf16_f32 v21, v18, v19
	ds_write_b64 v186, v[20:21] offset:1632
	ds_read_b32 v18, v187 offset:32
	s_waitcnt lgkmcnt(0)
	v_pk_fma_f32 v[20:21], v[18:19], v[66:67], 0 op_sel_hi:[0,1,0] neg_lo:[1,0,0] neg_hi:[1,0,0]
	v_pk_fma_f32 v[18:19], v[18:19], v[68:69], 0 op_sel_hi:[0,1,0] neg_lo:[1,0,0] neg_hi:[1,0,0]
	v_cvt_pk_bf16_f32 v20, v20, v21
	v_cvt_pk_bf16_f32 v21, v18, v19
	ds_write_b64 v186, v[20:21] offset:2176
	ds_read_b32 v18, v187 offset:40
	s_waitcnt lgkmcnt(0)
	v_pk_fma_f32 v[20:21], v[18:19], v[46:47], 0 op_sel_hi:[0,1,0] neg_lo:[1,0,0] neg_hi:[1,0,0]
	v_pk_fma_f32 v[18:19], v[18:19], v[48:49], 0 op_sel_hi:[0,1,0] neg_lo:[1,0,0] neg_hi:[1,0,0]
	v_cvt_pk_bf16_f32 v20, v20, v21
	v_cvt_pk_bf16_f32 v21, v18, v19
	ds_write_b64 v186, v[20:21] offset:2720
	ds_read_b32 v18, v187 offset:48
	s_waitcnt lgkmcnt(0)
	v_pk_fma_f32 v[20:21], v[18:19], v[42:43], 0 op_sel_hi:[0,1,0] neg_lo:[1,0,0] neg_hi:[1,0,0]
	v_pk_fma_f32 v[18:19], v[18:19], v[44:45], 0 op_sel_hi:[0,1,0] neg_lo:[1,0,0] neg_hi:[1,0,0]
	v_cvt_pk_bf16_f32 v20, v20, v21
	v_cvt_pk_bf16_f32 v21, v18, v19
	ds_write_b64 v186, v[20:21] offset:3264
	ds_read_b32 v18, v187 offset:56
	s_waitcnt lgkmcnt(0)
	v_pk_fma_f32 v[20:21], v[18:19], v[30:31], 0 op_sel_hi:[0,1,0] neg_lo:[1,0,0] neg_hi:[1,0,0]
	v_pk_fma_f32 v[18:19], v[18:19], v[32:33], 0 op_sel_hi:[0,1,0] neg_lo:[1,0,0] neg_hi:[1,0,0]
	v_cvt_pk_bf16_f32 v20, v20, v21
	v_cvt_pk_bf16_f32 v21, v18, v19
	ds_write_b64 v186, v[20:21] offset:3808
	ds_read_b128 a[144:147], v1
	ds_read_b128 a[148:151], v1 offset:64
	ds_read_b128 a[152:155], v1 offset:128
	ds_read_b128 a[156:159], v1 offset:192
	v_lshl_add_u64 v[18:19], v[130:131], 0, s[22:23]
	v_add_co_u32_e32 v20, vcc, s7, v18
	s_nop 1
	v_addc_co_u32_e32 v21, vcc, 0, v19, vcc
	global_load_dwordx4 v[106:109], v[18:19], off nt
	global_load_dwordx4 v[90:93], v[20:21], off nt
	v_add_co_u32_e32 v20, vcc, s36, v18
	s_nop 1
	v_addc_co_u32_e32 v21, vcc, 0, v19, vcc
	v_add_co_u32_e32 v30, vcc, s37, v18
	s_nop 1
	v_addc_co_u32_e32 v31, vcc, 0, v19, vcc
	global_load_dwordx4 v[86:89], v[20:21], off nt
	global_load_dwordx4 v[74:77], v[30:31], off nt
	v_add_co_u32_e32 v20, vcc, s38, v18
	s_nop 1
	v_addc_co_u32_e32 v21, vcc, 0, v19, vcc
	v_add_co_u32_e32 v30, vcc, s39, v18
	s_nop 1
	v_addc_co_u32_e32 v31, vcc, 0, v19, vcc
	global_load_dwordx4 v[70:73], v[20:21], off nt
	global_load_dwordx4 v[54:57], v[30:31], off nt
	v_add_co_u32_e32 v20, vcc, s41, v18
	s_nop 1
	v_addc_co_u32_e32 v21, vcc, 0, v19, vcc
	v_add_co_u32_e32 v18, vcc, s42, v18
	s_nop 1
	v_addc_co_u32_e32 v19, vcc, 0, v19, vcc
	global_load_dwordx4 v[50:53], v[20:21], off nt
	global_load_dwordx4 v[46:49], v[18:19], off nt
	v_mov_b32_e32 v18, v195
	s_waitcnt vmcnt(23)
	s_waitcnt vmcnt(22)
	s_waitcnt vmcnt(21)
	s_waitcnt vmcnt(20)
	s_waitcnt vmcnt(19)
	s_waitcnt vmcnt(18)
	s_waitcnt vmcnt(17)
	s_waitcnt vmcnt(16)
	ds_read_b32 v18, v187 offset:64
	s_waitcnt lgkmcnt(0)
	v_pk_fma_f32 v[20:21], v[18:19], v[110:111], 0 op_sel_hi:[0,1,0] neg_lo:[1,0,0] neg_hi:[1,0,0]
	v_pk_fma_f32 v[18:19], v[18:19], v[112:113], 0 op_sel_hi:[0,1,0] neg_lo:[1,0,0] neg_hi:[1,0,0]
	v_cvt_pk_bf16_f32 v20, v20, v21
	v_cvt_pk_bf16_f32 v21, v18, v19
	ds_write_b64 v186, v[20:21]
	ds_read_b32 v18, v187 offset:72
	s_waitcnt lgkmcnt(0)
	v_pk_fma_f32 v[20:21], v[18:19], v[98:99], 0 op_sel_hi:[0,1,0] neg_lo:[1,0,0] neg_hi:[1,0,0]
	v_pk_fma_f32 v[18:19], v[18:19], v[100:101], 0 op_sel_hi:[0,1,0] neg_lo:[1,0,0] neg_hi:[1,0,0]
	v_cvt_pk_bf16_f32 v20, v20, v21
	v_cvt_pk_bf16_f32 v21, v18, v19
	ds_write_b64 v186, v[20:21] offset:544
	ds_read_b32 v18, v187 offset:80
	s_waitcnt lgkmcnt(0)
	v_pk_fma_f32 v[20:21], v[18:19], v[78:79], 0 op_sel_hi:[0,1,0] neg_lo:[1,0,0] neg_hi:[1,0,0]
	v_pk_fma_f32 v[18:19], v[18:19], v[80:81], 0 op_sel_hi:[0,1,0] neg_lo:[1,0,0] neg_hi:[1,0,0]
	v_cvt_pk_bf16_f32 v20, v20, v21
	v_cvt_pk_bf16_f32 v21, v18, v19
	ds_write_b64 v186, v[20:21] offset:1088
	ds_read_b32 v18, v187 offset:88
	s_waitcnt lgkmcnt(0)
	v_pk_fma_f32 v[20:21], v[18:19], v[58:59], 0 op_sel_hi:[0,1,0] neg_lo:[1,0,0] neg_hi:[1,0,0]
	v_pk_fma_f32 v[18:19], v[18:19], v[60:61], 0 op_sel_hi:[0,1,0] neg_lo:[1,0,0] neg_hi:[1,0,0]
	v_cvt_pk_bf16_f32 v20, v20, v21
	v_cvt_pk_bf16_f32 v21, v18, v19
	ds_write_b64 v186, v[20:21] offset:1632
	ds_read_b32 v18, v187 offset:96
	s_waitcnt lgkmcnt(0)
	v_pk_fma_f32 v[20:21], v[18:19], v[34:35], 0 op_sel_hi:[0,1,0] neg_lo:[1,0,0] neg_hi:[1,0,0]
	v_pk_fma_f32 v[18:19], v[18:19], v[36:37], 0 op_sel_hi:[0,1,0] neg_lo:[1,0,0] neg_hi:[1,0,0]
	v_cvt_pk_bf16_f32 v20, v20, v21
	v_cvt_pk_bf16_f32 v21, v18, v19
	ds_write_b64 v186, v[20:21] offset:2176
	ds_read_b32 v18, v187 offset:104
	s_waitcnt lgkmcnt(0)
	v_pk_fma_f32 v[20:21], v[18:19], v[22:23], 0 op_sel_hi:[0,1,0] neg_lo:[1,0,0] neg_hi:[1,0,0]
	v_pk_fma_f32 v[18:19], v[18:19], v[24:25], 0 op_sel_hi:[0,1,0] neg_lo:[1,0,0] neg_hi:[1,0,0]
	v_cvt_pk_bf16_f32 v20, v20, v21
	v_cvt_pk_bf16_f32 v21, v18, v19
	ds_write_b64 v186, v[20:21] offset:2720
	ds_read_b32 v18, v187 offset:112
	s_waitcnt lgkmcnt(0)
	v_pk_fma_f32 v[14:15], v[18:19], v[14:15], 0 op_sel_hi:[0,1,0] neg_lo:[1,0,0] neg_hi:[1,0,0]
	v_pk_fma_f32 v[16:17], v[18:19], v[16:17], 0 op_sel_hi:[0,1,0] neg_lo:[1,0,0] neg_hi:[1,0,0]
	v_cvt_pk_bf16_f32 v14, v14, v15
	v_cvt_pk_bf16_f32 v15, v16, v17
	ds_write_b64 v186, v[14:15] offset:3264
	ds_read_b32 v14, v187 offset:120
	s_waitcnt lgkmcnt(0)
	v_pk_fma_f32 v[6:7], v[14:15], v[6:7], 0 op_sel_hi:[0,1,0] neg_lo:[1,0,0] neg_hi:[1,0,0]
	v_pk_fma_f32 v[8:9], v[14:15], v[8:9], 0 op_sel_hi:[0,1,0] neg_lo:[1,0,0] neg_hi:[1,0,0]
	v_cvt_pk_bf16_f32 v6, v6, v7
	v_cvt_pk_bf16_f32 v7, v8, v9
	ds_write_b64 v186, v[6:7] offset:3808
	ds_read_b128 a[160:163], v1
	ds_read_b128 a[164:167], v1 offset:64
	ds_read_b128 a[168:171], v1 offset:128
	ds_read_b128 a[172:175], v1 offset:192
	v_lshl_add_u64 v[6:7], v[150:151], 0, s[22:23]
	v_lshl_add_u64 v[18:19], v[160:161], 0, s[22:23]
	v_lshl_add_u64 v[20:21], v[162:163], 0, s[22:23]
	v_lshl_add_u64 v[22:23], v[164:165], 0, s[22:23]
	v_lshl_add_u64 v[8:9], v[152:153], 0, s[22:23]
	v_lshl_add_u64 v[14:15], v[156:157], 0, s[22:23]
	v_lshl_add_u64 v[16:17], v[158:159], 0, s[22:23]
	v_lshl_add_u64 v[34:35], v[166:167], 0, s[22:23]
	global_load_dwordx4 v[110:113], v[6:7], off nt
	global_load_dwordx4 v[98:101], v[8:9], off nt
	global_load_dwordx4 v[78:81], v[14:15], off nt
	global_load_dwordx4 v[66:69], v[16:17], off nt
	global_load_dwordx4 v[58:61], v[18:19], off nt
	global_load_dwordx4 v[30:33], v[20:21], off nt
	s_nop 0
	global_load_dwordx4 v[22:25], v[22:23], off nt
	s_nop 0
	global_load_dwordx4 v[18:21], v[34:35], off nt
	s_waitcnt vmcnt(23)
	s_waitcnt vmcnt(22)
	s_waitcnt vmcnt(21)
	s_waitcnt vmcnt(20)
	s_waitcnt vmcnt(19)
	s_waitcnt vmcnt(18)
	s_waitcnt vmcnt(17)
	s_waitcnt vmcnt(16)
	ds_read_b32 v6, v187 offset:128
	s_waitcnt lgkmcnt(0)
	v_pk_fma_f32 v[8:9], v[6:7], v[114:115], 0 op_sel_hi:[0,1,0] neg_lo:[1,0,0] neg_hi:[1,0,0]
	v_pk_fma_f32 v[6:7], v[6:7], v[116:117], 0 op_sel_hi:[0,1,0] neg_lo:[1,0,0] neg_hi:[1,0,0]
	v_cvt_pk_bf16_f32 v8, v8, v9
	v_cvt_pk_bf16_f32 v9, v6, v7
	ds_write_b64 v186, v[8:9]
	ds_read_b32 v6, v187 offset:136
	s_waitcnt lgkmcnt(0)
	v_pk_fma_f32 v[8:9], v[6:7], v[94:95], 0 op_sel_hi:[0,1,0] neg_lo:[1,0,0] neg_hi:[1,0,0]
	v_pk_fma_f32 v[6:7], v[6:7], v[96:97], 0 op_sel_hi:[0,1,0] neg_lo:[1,0,0] neg_hi:[1,0,0]
	v_cvt_pk_bf16_f32 v8, v8, v9
	v_cvt_pk_bf16_f32 v9, v6, v7
	ds_write_b64 v186, v[8:9] offset:544
	ds_read_b32 v6, v187 offset:144
	s_waitcnt lgkmcnt(0)
	v_pk_fma_f32 v[8:9], v[6:7], v[82:83], 0 op_sel_hi:[0,1,0] neg_lo:[1,0,0] neg_hi:[1,0,0]
	v_pk_fma_f32 v[6:7], v[6:7], v[84:85], 0 op_sel_hi:[0,1,0] neg_lo:[1,0,0] neg_hi:[1,0,0]
	v_cvt_pk_bf16_f32 v8, v8, v9
	v_cvt_pk_bf16_f32 v9, v6, v7
	ds_write_b64 v186, v[8:9] offset:1088
	ds_read_b32 v6, v187 offset:152
	s_waitcnt lgkmcnt(0)
	v_pk_fma_f32 v[8:9], v[6:7], v[62:63], 0 op_sel_hi:[0,1,0] neg_lo:[1,0,0] neg_hi:[1,0,0]
	v_pk_fma_f32 v[6:7], v[6:7], v[64:65], 0 op_sel_hi:[0,1,0] neg_lo:[1,0,0] neg_hi:[1,0,0]
	v_cvt_pk_bf16_f32 v8, v8, v9
	v_cvt_pk_bf16_f32 v9, v6, v7
	ds_write_b64 v186, v[8:9] offset:1632
	ds_read_b32 v6, v187 offset:160
	s_waitcnt lgkmcnt(0)
	v_pk_fma_f32 v[8:9], v[6:7], v[38:39], 0 op_sel_hi:[0,1,0] neg_lo:[1,0,0] neg_hi:[1,0,0]
	v_pk_fma_f32 v[6:7], v[6:7], v[40:41], 0 op_sel_hi:[0,1,0] neg_lo:[1,0,0] neg_hi:[1,0,0]
	v_cvt_pk_bf16_f32 v8, v8, v9
	v_cvt_pk_bf16_f32 v9, v6, v7
	ds_write_b64 v186, v[8:9] offset:2176
	ds_read_b32 v6, v187 offset:168
	s_waitcnt lgkmcnt(0)
	v_pk_fma_f32 v[8:9], v[6:7], v[26:27], 0 op_sel_hi:[0,1,0] neg_lo:[1,0,0] neg_hi:[1,0,0]
	v_pk_fma_f32 v[6:7], v[6:7], v[28:29], 0 op_sel_hi:[0,1,0] neg_lo:[1,0,0] neg_hi:[1,0,0]
	v_cvt_pk_bf16_f32 v8, v8, v9
	v_cvt_pk_bf16_f32 v9, v6, v7
	ds_write_b64 v186, v[8:9] offset:2720
	ds_read_b32 v6, v187 offset:176
	s_waitcnt lgkmcnt(0)
	v_pk_fma_f32 v[8:9], v[6:7], v[10:11], 0 op_sel_hi:[0,1,0] neg_lo:[1,0,0] neg_hi:[1,0,0]
	v_pk_fma_f32 v[6:7], v[6:7], v[12:13], 0 op_sel_hi:[0,1,0] neg_lo:[1,0,0] neg_hi:[1,0,0]
	v_cvt_pk_bf16_f32 v8, v8, v9
	v_cvt_pk_bf16_f32 v9, v6, v7
	ds_write_b64 v186, v[8:9] offset:3264
	ds_read_b32 v6, v187 offset:184
	s_waitcnt lgkmcnt(0)
	v_pk_fma_f32 v[2:3], v[6:7], v[2:3], 0 op_sel_hi:[0,1,0] neg_lo:[1,0,0] neg_hi:[1,0,0]
	v_pk_fma_f32 v[4:5], v[6:7], v[4:5], 0 op_sel_hi:[0,1,0] neg_lo:[1,0,0] neg_hi:[1,0,0]
	v_cvt_pk_bf16_f32 v2, v2, v3
	v_cvt_pk_bf16_f32 v3, v4, v5
	ds_write_b64 v186, v[2:3] offset:3808
	ds_read_b128 a[176:179], v1
	ds_read_b128 a[180:183], v1 offset:64
	ds_read_b128 a[184:187], v1 offset:128
	ds_read_b128 a[188:191], v1 offset:192
	v_lshl_add_u64 v[2:3], v[168:169], 0, s[22:23]
	v_lshl_add_u64 v[4:5], v[170:171], 0, s[22:23]
	v_lshl_add_u64 v[6:7], v[172:173], 0, s[22:23]
	v_lshl_add_u64 v[8:9], v[174:175], 0, s[22:23]
	v_lshl_add_u64 v[10:11], v[176:177], 0, s[22:23]
	v_lshl_add_u64 v[12:13], v[178:179], 0, s[22:23]
	v_lshl_add_u64 v[14:15], v[180:181], 0, s[22:23]
	v_lshl_add_u64 v[16:17], v[182:183], 0, s[22:23]
	global_load_dwordx4 v[114:117], v[2:3], off nt
	global_load_dwordx4 v[102:105], v[4:5], off nt
	global_load_dwordx4 v[94:97], v[6:7], off nt
	global_load_dwordx4 v[82:85], v[8:9], off nt
	global_load_dwordx4 v[62:65], v[10:11], off nt
	global_load_dwordx4 v[42:45], v[12:13], off nt
	global_load_dwordx4 v[38:41], v[14:15], off nt
	global_load_dwordx4 v[34:37], v[16:17], off nt
	v_mov_b32_e32 v2, v194
	s_waitcnt vmcnt(23)
	s_waitcnt vmcnt(22)
	s_waitcnt vmcnt(21)
	s_waitcnt vmcnt(20)
	s_waitcnt vmcnt(19)
	s_waitcnt vmcnt(18)
	s_waitcnt vmcnt(17)
	s_waitcnt vmcnt(16)
	ds_read_b32 v2, v187
	s_waitcnt lgkmcnt(0)
	v_pk_fma_f32 v[4:5], v[2:3], v[106:107], 0 op_sel_hi:[0,1,0] neg_lo:[1,0,0] neg_hi:[1,0,0]
	v_pk_fma_f32 v[2:3], v[2:3], v[108:109], 0 op_sel_hi:[0,1,0] neg_lo:[1,0,0] neg_hi:[1,0,0]
	v_cvt_pk_bf16_f32 v4, v4, v5
	v_cvt_pk_bf16_f32 v5, v2, v3
	ds_write_b64 v186, v[4:5]
	ds_read_b32 v2, v187 offset:8
	s_waitcnt lgkmcnt(0)
	v_pk_fma_f32 v[4:5], v[2:3], v[90:91], 0 op_sel_hi:[0,1,0] neg_lo:[1,0,0] neg_hi:[1,0,0]
	v_pk_fma_f32 v[2:3], v[2:3], v[92:93], 0 op_sel_hi:[0,1,0] neg_lo:[1,0,0] neg_hi:[1,0,0]
	v_cvt_pk_bf16_f32 v4, v4, v5
	v_cvt_pk_bf16_f32 v5, v2, v3
	ds_write_b64 v186, v[4:5] offset:544
	ds_read_b32 v2, v187 offset:16
	s_waitcnt lgkmcnt(0)
	v_pk_fma_f32 v[4:5], v[2:3], v[86:87], 0 op_sel_hi:[0,1,0] neg_lo:[1,0,0] neg_hi:[1,0,0]
	v_pk_fma_f32 v[2:3], v[2:3], v[88:89], 0 op_sel_hi:[0,1,0] neg_lo:[1,0,0] neg_hi:[1,0,0]
	v_cvt_pk_bf16_f32 v4, v4, v5
	v_cvt_pk_bf16_f32 v5, v2, v3
	ds_write_b64 v186, v[4:5] offset:1088
	ds_read_b32 v2, v187 offset:24
	s_waitcnt lgkmcnt(0)
	v_pk_fma_f32 v[4:5], v[2:3], v[74:75], 0 op_sel_hi:[0,1,0] neg_lo:[1,0,0] neg_hi:[1,0,0]
	v_pk_fma_f32 v[2:3], v[2:3], v[76:77], 0 op_sel_hi:[0,1,0] neg_lo:[1,0,0] neg_hi:[1,0,0]
	v_cvt_pk_bf16_f32 v4, v4, v5
	v_cvt_pk_bf16_f32 v5, v2, v3
	ds_write_b64 v186, v[4:5] offset:1632
	ds_read_b32 v2, v187 offset:32
	s_waitcnt lgkmcnt(0)
	v_pk_fma_f32 v[4:5], v[2:3], v[70:71], 0 op_sel_hi:[0,1,0] neg_lo:[1,0,0] neg_hi:[1,0,0]
	v_pk_fma_f32 v[2:3], v[2:3], v[72:73], 0 op_sel_hi:[0,1,0] neg_lo:[1,0,0] neg_hi:[1,0,0]
	v_cvt_pk_bf16_f32 v4, v4, v5
	v_cvt_pk_bf16_f32 v5, v2, v3
	ds_write_b64 v186, v[4:5] offset:2176
	ds_read_b32 v2, v187 offset:40
	s_waitcnt lgkmcnt(0)
	v_pk_fma_f32 v[4:5], v[2:3], v[54:55], 0 op_sel_hi:[0,1,0] neg_lo:[1,0,0] neg_hi:[1,0,0]
	v_pk_fma_f32 v[2:3], v[2:3], v[56:57], 0 op_sel_hi:[0,1,0] neg_lo:[1,0,0] neg_hi:[1,0,0]
	v_cvt_pk_bf16_f32 v4, v4, v5
	v_cvt_pk_bf16_f32 v5, v2, v3
	ds_write_b64 v186, v[4:5] offset:2720
	ds_read_b32 v2, v187 offset:48
	s_waitcnt lgkmcnt(0)
	v_pk_fma_f32 v[4:5], v[2:3], v[50:51], 0 op_sel_hi:[0,1,0] neg_lo:[1,0,0] neg_hi:[1,0,0]
	v_pk_fma_f32 v[2:3], v[2:3], v[52:53], 0 op_sel_hi:[0,1,0] neg_lo:[1,0,0] neg_hi:[1,0,0]
	v_cvt_pk_bf16_f32 v4, v4, v5
	v_cvt_pk_bf16_f32 v5, v2, v3
	ds_write_b64 v186, v[4:5] offset:3264
	ds_read_b32 v2, v187 offset:56
	s_waitcnt lgkmcnt(0)
	v_pk_fma_f32 v[4:5], v[2:3], v[46:47], 0 op_sel_hi:[0,1,0] neg_lo:[1,0,0] neg_hi:[1,0,0]
	v_pk_fma_f32 v[2:3], v[2:3], v[48:49], 0 op_sel_hi:[0,1,0] neg_lo:[1,0,0] neg_hi:[1,0,0]
	v_cvt_pk_bf16_f32 v4, v4, v5
	v_cvt_pk_bf16_f32 v5, v2, v3
	ds_write_b64 v186, v[4:5] offset:3808
	ds_read_b128 a[192:195], v1
	ds_read_b128 a[196:199], v1 offset:64
	ds_read_b128 a[200:203], v1 offset:128
	ds_read_b128 a[204:207], v1 offset:192
	v_lshl_add_u64 v[118:119], v[130:131], 0, s[20:21]
	v_add_co_u32_e32 v126, vcc, s7, v118
	s_nop 1
	v_addc_co_u32_e32 v127, vcc, 0, v119, vcc
	v_add_co_u32_e32 v128, vcc, s36, v118
	global_load_dwordx4 v[90:93], v[118:119], off nt
	global_load_dwordx4 v[86:89], v[126:127], off nt
	v_addc_co_u32_e32 v129, vcc, 0, v119, vcc
	v_add_co_u32_e32 v134, vcc, s37, v118
	s_nop 1
	v_addc_co_u32_e32 v135, vcc, 0, v119, vcc
	v_add_co_u32_e32 v136, vcc, s38, v118
	global_load_dwordx4 v[54:57], v[128:129], off nt
	global_load_dwordx4 v[50:53], v[134:135], off nt
	v_addc_co_u32_e32 v137, vcc, 0, v119, vcc
	v_add_co_u32_e32 v138, vcc, s39, v118
	s_nop 1
	v_addc_co_u32_e32 v139, vcc, 0, v119, vcc
	v_add_co_u32_e32 v140, vcc, s41, v118
	global_load_dwordx4 v[14:17], v[136:137], off nt
	global_load_dwordx4 v[10:13], v[138:139], off nt
	v_addc_co_u32_e32 v141, vcc, 0, v119, vcc
	v_add_co_u32_e32 v142, vcc, s42, v118
	s_nop 1
	v_addc_co_u32_e32 v143, vcc, 0, v119, vcc
	global_load_dwordx4 v[6:9], v[140:141], off nt
	global_load_dwordx4 v[2:5], v[142:143], off nt
	v_mov_b32_e32 v26, v194
	s_waitcnt vmcnt(23)
	s_waitcnt vmcnt(22)
	s_waitcnt vmcnt(21)
	s_waitcnt vmcnt(20)
	s_waitcnt vmcnt(19)
	s_waitcnt vmcnt(18)
	s_waitcnt vmcnt(17)
	s_waitcnt vmcnt(16)
	ds_read_b32 v26, v187 offset:64
	s_waitcnt lgkmcnt(0)
	v_pk_fma_f32 v[28:29], v[26:27], v[110:111], 0 op_sel_hi:[0,1,0] neg_lo:[1,0,0] neg_hi:[1,0,0]
	v_pk_fma_f32 v[26:27], v[26:27], v[112:113], 0 op_sel_hi:[0,1,0] neg_lo:[1,0,0] neg_hi:[1,0,0]
	v_cvt_pk_bf16_f32 v28, v28, v29
	v_cvt_pk_bf16_f32 v29, v26, v27
	ds_write_b64 v186, v[28:29]
	ds_read_b32 v26, v187 offset:72
	s_waitcnt lgkmcnt(0)
	v_pk_fma_f32 v[28:29], v[26:27], v[98:99], 0 op_sel_hi:[0,1,0] neg_lo:[1,0,0] neg_hi:[1,0,0]
	v_pk_fma_f32 v[26:27], v[26:27], v[100:101], 0 op_sel_hi:[0,1,0] neg_lo:[1,0,0] neg_hi:[1,0,0]
	v_cvt_pk_bf16_f32 v28, v28, v29
	v_cvt_pk_bf16_f32 v29, v26, v27
	ds_write_b64 v186, v[28:29] offset:544
	ds_read_b32 v26, v187 offset:80
	s_waitcnt lgkmcnt(0)
	v_pk_fma_f32 v[28:29], v[26:27], v[78:79], 0 op_sel_hi:[0,1,0] neg_lo:[1,0,0] neg_hi:[1,0,0]
	v_pk_fma_f32 v[26:27], v[26:27], v[80:81], 0 op_sel_hi:[0,1,0] neg_lo:[1,0,0] neg_hi:[1,0,0]
	v_cvt_pk_bf16_f32 v28, v28, v29
	v_cvt_pk_bf16_f32 v29, v26, v27
	ds_write_b64 v186, v[28:29] offset:1088
	ds_read_b32 v26, v187 offset:88
	s_waitcnt lgkmcnt(0)
	v_pk_fma_f32 v[28:29], v[26:27], v[66:67], 0 op_sel_hi:[0,1,0] neg_lo:[1,0,0] neg_hi:[1,0,0]
	v_pk_fma_f32 v[26:27], v[26:27], v[68:69], 0 op_sel_hi:[0,1,0] neg_lo:[1,0,0] neg_hi:[1,0,0]
	v_cvt_pk_bf16_f32 v28, v28, v29
	v_cvt_pk_bf16_f32 v29, v26, v27
	ds_write_b64 v186, v[28:29] offset:1632
	ds_read_b32 v26, v187 offset:96
	s_waitcnt lgkmcnt(0)
	v_pk_fma_f32 v[28:29], v[26:27], v[58:59], 0 op_sel_hi:[0,1,0] neg_lo:[1,0,0] neg_hi:[1,0,0]
	v_pk_fma_f32 v[26:27], v[26:27], v[60:61], 0 op_sel_hi:[0,1,0] neg_lo:[1,0,0] neg_hi:[1,0,0]
	v_cvt_pk_bf16_f32 v28, v28, v29
	v_cvt_pk_bf16_f32 v29, v26, v27
	ds_write_b64 v186, v[28:29] offset:2176
	ds_read_b32 v26, v187 offset:104
	s_waitcnt lgkmcnt(0)
	v_pk_fma_f32 v[28:29], v[26:27], v[30:31], 0 op_sel_hi:[0,1,0] neg_lo:[1,0,0] neg_hi:[1,0,0]
	v_pk_fma_f32 v[26:27], v[26:27], v[32:33], 0 op_sel_hi:[0,1,0] neg_lo:[1,0,0] neg_hi:[1,0,0]
	v_cvt_pk_bf16_f32 v28, v28, v29
	v_cvt_pk_bf16_f32 v29, v26, v27
	ds_write_b64 v186, v[28:29] offset:2720
	ds_read_b32 v26, v187 offset:112
	s_waitcnt lgkmcnt(0)
	v_pk_fma_f32 v[22:23], v[26:27], v[22:23], 0 op_sel_hi:[0,1,0] neg_lo:[1,0,0] neg_hi:[1,0,0]
	v_pk_fma_f32 v[24:25], v[26:27], v[24:25], 0 op_sel_hi:[0,1,0] neg_lo:[1,0,0] neg_hi:[1,0,0]
	v_cvt_pk_bf16_f32 v22, v22, v23
	v_cvt_pk_bf16_f32 v23, v24, v25
	ds_write_b64 v186, v[22:23] offset:3264
	ds_read_b32 v22, v187 offset:120
	s_waitcnt lgkmcnt(0)
	v_pk_fma_f32 v[18:19], v[22:23], v[18:19], 0 op_sel_hi:[0,1,0] neg_lo:[1,0,0] neg_hi:[1,0,0]
	v_pk_fma_f32 v[20:21], v[22:23], v[20:21], 0 op_sel_hi:[0,1,0] neg_lo:[1,0,0] neg_hi:[1,0,0]
	v_cvt_pk_bf16_f32 v18, v18, v19
	v_cvt_pk_bf16_f32 v19, v20, v21
	ds_write_b64 v186, v[18:19] offset:3808
	ds_read_b128 a[208:211], v1
	ds_read_b128 a[212:215], v1 offset:64
	ds_read_b128 a[216:219], v1 offset:128
	ds_read_b128 a[220:223], v1 offset:192
	v_lshl_add_u64 v[18:19], v[150:151], 0, s[20:21]
	v_lshl_add_u64 v[20:21], v[152:153], 0, s[20:21]
	v_lshl_add_u64 v[22:23], v[156:157], 0, s[20:21]
	v_lshl_add_u64 v[24:25], v[158:159], 0, s[20:21]
	v_lshl_add_u64 v[26:27], v[160:161], 0, s[20:21]
	v_lshl_add_u64 v[28:29], v[162:163], 0, s[20:21]
	v_lshl_add_u64 v[46:47], v[164:165], 0, s[20:21]
	v_lshl_add_u64 v[48:49], v[166:167], 0, s[20:21]
	global_load_dwordx4 v[78:81], v[18:19], off nt
	global_load_dwordx4 v[74:77], v[20:21], off nt
	global_load_dwordx4 v[70:73], v[22:23], off nt
	global_load_dwordx4 v[66:69], v[24:25], off nt
	global_load_dwordx4 v[30:33], v[26:27], off nt
	s_nop 0
	global_load_dwordx4 v[26:29], v[28:29], off nt
	s_nop 0
	global_load_dwordx4 v[22:25], v[46:47], off nt
	global_load_dwordx4 v[18:21], v[48:49], off nt
	s_waitcnt vmcnt(23)
	s_waitcnt vmcnt(22)
	s_waitcnt vmcnt(21)
	s_waitcnt vmcnt(20)
	s_waitcnt vmcnt(19)
	s_waitcnt vmcnt(18)
	s_waitcnt vmcnt(17)
	s_waitcnt vmcnt(16)
	ds_read_b32 v46, v187 offset:128
	s_waitcnt lgkmcnt(0)
	v_pk_fma_f32 v[48:49], v[46:47], v[114:115], 0 op_sel_hi:[0,1,0] neg_lo:[1,0,0] neg_hi:[1,0,0]
	v_pk_fma_f32 v[46:47], v[46:47], v[116:117], 0 op_sel_hi:[0,1,0] neg_lo:[1,0,0] neg_hi:[1,0,0]
	v_cvt_pk_bf16_f32 v48, v48, v49
	v_cvt_pk_bf16_f32 v49, v46, v47
	ds_write_b64 v186, v[48:49]
	ds_read_b32 v46, v187 offset:136
	s_waitcnt lgkmcnt(0)
	v_pk_fma_f32 v[48:49], v[46:47], v[102:103], 0 op_sel_hi:[0,1,0] neg_lo:[1,0,0] neg_hi:[1,0,0]
	v_pk_fma_f32 v[46:47], v[46:47], v[104:105], 0 op_sel_hi:[0,1,0] neg_lo:[1,0,0] neg_hi:[1,0,0]
	v_cvt_pk_bf16_f32 v48, v48, v49
	v_cvt_pk_bf16_f32 v49, v46, v47
	ds_write_b64 v186, v[48:49] offset:544
	ds_read_b32 v46, v187 offset:144
	s_waitcnt lgkmcnt(0)
	v_pk_fma_f32 v[48:49], v[46:47], v[94:95], 0 op_sel_hi:[0,1,0] neg_lo:[1,0,0] neg_hi:[1,0,0]
	v_pk_fma_f32 v[46:47], v[46:47], v[96:97], 0 op_sel_hi:[0,1,0] neg_lo:[1,0,0] neg_hi:[1,0,0]
	v_cvt_pk_bf16_f32 v48, v48, v49
	v_cvt_pk_bf16_f32 v49, v46, v47
	ds_write_b64 v186, v[48:49] offset:1088
	ds_read_b32 v46, v187 offset:152
	s_waitcnt lgkmcnt(0)
	v_pk_fma_f32 v[48:49], v[46:47], v[82:83], 0 op_sel_hi:[0,1,0] neg_lo:[1,0,0] neg_hi:[1,0,0]
	v_pk_fma_f32 v[46:47], v[46:47], v[84:85], 0 op_sel_hi:[0,1,0] neg_lo:[1,0,0] neg_hi:[1,0,0]
	v_cvt_pk_bf16_f32 v48, v48, v49
	v_cvt_pk_bf16_f32 v49, v46, v47
	ds_write_b64 v186, v[48:49] offset:1632
	ds_read_b32 v46, v187 offset:160
	s_waitcnt lgkmcnt(0)
	v_pk_fma_f32 v[48:49], v[46:47], v[62:63], 0 op_sel_hi:[0,1,0] neg_lo:[1,0,0] neg_hi:[1,0,0]
	v_pk_fma_f32 v[46:47], v[46:47], v[64:65], 0 op_sel_hi:[0,1,0] neg_lo:[1,0,0] neg_hi:[1,0,0]
	v_cvt_pk_bf16_f32 v48, v48, v49
	v_cvt_pk_bf16_f32 v49, v46, v47
	ds_write_b64 v186, v[48:49] offset:2176
	ds_read_b32 v46, v187 offset:168
	s_waitcnt lgkmcnt(0)
	v_pk_fma_f32 v[42:43], v[46:47], v[42:43], 0 op_sel_hi:[0,1,0] neg_lo:[1,0,0] neg_hi:[1,0,0]
	v_pk_fma_f32 v[44:45], v[46:47], v[44:45], 0 op_sel_hi:[0,1,0] neg_lo:[1,0,0] neg_hi:[1,0,0]
	v_cvt_pk_bf16_f32 v42, v42, v43
	v_cvt_pk_bf16_f32 v43, v44, v45
	ds_write_b64 v186, v[42:43] offset:2720
	ds_read_b32 v42, v187 offset:176
	s_waitcnt lgkmcnt(0)
	v_pk_fma_f32 v[38:39], v[42:43], v[38:39], 0 op_sel_hi:[0,1,0] neg_lo:[1,0,0] neg_hi:[1,0,0]
	v_pk_fma_f32 v[40:41], v[42:43], v[40:41], 0 op_sel_hi:[0,1,0] neg_lo:[1,0,0] neg_hi:[1,0,0]
	v_cvt_pk_bf16_f32 v38, v38, v39
	v_cvt_pk_bf16_f32 v39, v40, v41
	ds_write_b64 v186, v[38:39] offset:3264
	ds_read_b32 v38, v187 offset:184
	s_waitcnt lgkmcnt(0)
	v_pk_fma_f32 v[34:35], v[38:39], v[34:35], 0 op_sel_hi:[0,1,0] neg_lo:[1,0,0] neg_hi:[1,0,0]
	v_pk_fma_f32 v[36:37], v[38:39], v[36:37], 0 op_sel_hi:[0,1,0] neg_lo:[1,0,0] neg_hi:[1,0,0]
	v_cvt_pk_bf16_f32 v34, v34, v35
	v_cvt_pk_bf16_f32 v35, v36, v37
	ds_write_b64 v186, v[34:35] offset:3808
	ds_read_b128 a[224:227], v1
	ds_read_b128 a[228:231], v1 offset:64
	ds_read_b128 a[232:235], v1 offset:128
	ds_read_b128 a[236:239], v1 offset:192
	v_lshl_add_u64 v[34:35], v[168:169], 0, s[20:21]
	v_lshl_add_u64 v[36:37], v[170:171], 0, s[20:21]
	v_lshl_add_u64 v[38:39], v[172:173], 0, s[20:21]
	v_lshl_add_u64 v[40:41], v[174:175], 0, s[20:21]
	v_lshl_add_u64 v[42:43], v[176:177], 0, s[20:21]
	v_lshl_add_u64 v[44:45], v[178:179], 0, s[20:21]
	v_lshl_add_u64 v[58:59], v[180:181], 0, s[20:21]
	v_lshl_add_u64 v[60:61], v[182:183], 0, s[20:21]
	global_load_dwordx4 v[122:125], v[34:35], off nt
	global_load_dwordx4 v[106:109], v[36:37], off nt
	global_load_dwordx4 v[94:97], v[38:39], off nt
	global_load_dwordx4 v[82:85], v[40:41], off nt
	global_load_dwordx4 v[46:49], v[42:43], off nt
	s_nop 0
	global_load_dwordx4 v[42:45], v[44:45], off nt
	s_nop 0
	global_load_dwordx4 v[38:41], v[58:59], off nt
	global_load_dwordx4 v[34:37], v[60:61], off nt
	v_mov_b32_e32 v98, v133
	s_waitcnt vmcnt(23)
	s_waitcnt vmcnt(22)
	s_waitcnt vmcnt(21)
	s_waitcnt vmcnt(20)
	s_waitcnt vmcnt(19)
	s_waitcnt vmcnt(18)
	s_waitcnt vmcnt(17)
	s_waitcnt vmcnt(16)
	ds_read_b32 v58, v187
	v_add_u32_e32 v99, 1, v98
	v_cmp_eq_u32_e32 vcc, v98, v132
	s_nop 1
	v_cndmask_b32_e64 v60, 0, 1.0, vcc
	v_cmp_eq_u32_e32 vcc, v99, v132
	s_nop 1
	v_cndmask_b32_e64 v61, 0, 1.0, vcc
	s_waitcnt lgkmcnt(0)
	v_pk_fma_f32 v[62:63], v[58:59], v[90:91], v[60:61] op_sel_hi:[0,1,1] neg_lo:[1,0,0] neg_hi:[1,0,0]
	v_add_u32_e32 v90, 3, v98
	v_add_u32_e32 v91, 2, v98
	v_cmp_eq_u32_e32 vcc, v90, v132
	v_cvt_pk_bf16_f32 v62, v62, v63
	s_nop 0
	v_cndmask_b32_e64 v65, 0, 1.0, vcc
	v_cmp_eq_u32_e32 vcc, v91, v132
	s_nop 1
	v_cndmask_b32_e64 v64, 0, 1.0, vcc
	v_pk_fma_f32 v[58:59], v[58:59], v[92:93], v[64:65] op_sel_hi:[0,1,1] neg_lo:[1,0,0] neg_hi:[1,0,0]
	v_cvt_pk_bf16_f32 v63, v58, v59
	ds_write_b64 v186, v[62:63]
	ds_read_b32 v58, v187 offset:8
	v_cmp_eq_u32_e32 vcc, v98, v193
	s_nop 1
	v_cndmask_b32_e64 v62, 0, 1.0, vcc
	v_cmp_eq_u32_e32 vcc, v99, v193
	s_nop 1
	v_cndmask_b32_e64 v63, 0, 1.0, vcc
	v_cmp_eq_u32_e32 vcc, v90, v193
	s_waitcnt lgkmcnt(0)
	v_pk_fma_f32 v[62:63], v[58:59], v[86:87], v[62:63] op_sel_hi:[0,1,1] neg_lo:[1,0,0] neg_hi:[1,0,0]
	v_cvt_pk_bf16_f32 v62, v62, v63
	v_cndmask_b32_e64 v61, 0, 1.0, vcc
	v_pk_fma_f32 v[58:59], v[58:59], v[88:89], v[60:61] op_sel_hi:[0,1,1] neg_lo:[1,0,0] neg_hi:[1,0,0]
	v_cvt_pk_bf16_f32 v63, v58, v59
	ds_write_b64 v186, v[62:63] offset:544
	ds_read_b32 v58, v187 offset:16
	v_cmp_eq_u32_e32 vcc, v98, v192
	s_nop 1
	v_cndmask_b32_e64 v60, 0, 1.0, vcc
	v_cmp_eq_u32_e32 vcc, v99, v192
	s_nop 1
	v_cndmask_b32_e64 v61, 0, 1.0, vcc
	v_cmp_eq_u32_e32 vcc, v90, v192
	s_waitcnt lgkmcnt(0)
	v_pk_fma_f32 v[54:55], v[58:59], v[54:55], v[60:61] op_sel_hi:[0,1,1] neg_lo:[1,0,0] neg_hi:[1,0,0]
	v_cvt_pk_bf16_f32 v54, v54, v55
	v_cndmask_b32_e64 v61, 0, 1.0, vcc
	v_cmp_eq_u32_e32 vcc, v91, v192
	s_nop 1
	v_cndmask_b32_e64 v60, 0, 1.0, vcc
	v_pk_fma_f32 v[56:57], v[58:59], v[56:57], v[60:61] op_sel_hi:[0,1,1] neg_lo:[1,0,0] neg_hi:[1,0,0]
	v_cvt_pk_bf16_f32 v55, v56, v57
	ds_write_b64 v186, v[54:55] offset:1088
	ds_read_b32 v54, v187 offset:24
	v_cmp_eq_u32_e32 vcc, v98, v190
	s_nop 1
	v_cndmask_b32_e64 v56, 0, 1.0, vcc
	v_cmp_eq_u32_e32 vcc, v99, v190
	s_nop 1
	v_cndmask_b32_e64 v57, 0, 1.0, vcc
	v_cmp_eq_u32_e32 vcc, v90, v190
	s_waitcnt lgkmcnt(0)
	v_pk_fma_f32 v[50:51], v[54:55], v[50:51], v[56:57] op_sel_hi:[0,1,1] neg_lo:[1,0,0] neg_hi:[1,0,0]
	v_cvt_pk_bf16_f32 v50, v50, v51
	v_cndmask_b32_e64 v57, 0, 1.0, vcc
	v_cmp_eq_u32_e32 vcc, v91, v190
	s_nop 1
	v_cndmask_b32_e64 v56, 0, 1.0, vcc
	v_pk_fma_f32 v[52:53], v[54:55], v[52:53], v[56:57] op_sel_hi:[0,1,1] neg_lo:[1,0,0] neg_hi:[1,0,0]
	v_cvt_pk_bf16_f32 v51, v52, v53
	ds_write_b64 v186, v[50:51] offset:1632
	ds_read_b32 v50, v187 offset:32
	v_cmp_eq_u32_e32 vcc, v98, v149
	s_nop 1
	v_cndmask_b32_e64 v52, 0, 1.0, vcc
	v_cmp_eq_u32_e32 vcc, v99, v149
	s_nop 1
	v_cndmask_b32_e64 v53, 0, 1.0, vcc
	v_cmp_eq_u32_e32 vcc, v90, v149
	s_waitcnt lgkmcnt(0)
	v_pk_fma_f32 v[14:15], v[50:51], v[14:15], v[52:53] op_sel_hi:[0,1,1] neg_lo:[1,0,0] neg_hi:[1,0,0]
	v_cvt_pk_bf16_f32 v14, v14, v15
	v_cndmask_b32_e64 v53, 0, 1.0, vcc
	v_cmp_eq_u32_e32 vcc, v91, v149
	s_nop 1
	v_cndmask_b32_e64 v52, 0, 1.0, vcc
	v_pk_fma_f32 v[16:17], v[50:51], v[16:17], v[52:53] op_sel_hi:[0,1,1] neg_lo:[1,0,0] neg_hi:[1,0,0]
	v_cvt_pk_bf16_f32 v15, v16, v17
	ds_write_b64 v186, v[14:15] offset:2176
	ds_read_b32 v14, v187 offset:40
	v_cmp_eq_u32_e32 vcc, v98, v148
	s_nop 1
	v_cndmask_b32_e64 v16, 0, 1.0, vcc
	v_cmp_eq_u32_e32 vcc, v99, v148
	s_nop 1
	v_cndmask_b32_e64 v17, 0, 1.0, vcc
	v_cmp_eq_u32_e32 vcc, v90, v148
	s_waitcnt lgkmcnt(0)
	v_pk_fma_f32 v[10:11], v[14:15], v[10:11], v[16:17] op_sel_hi:[0,1,1] neg_lo:[1,0,0] neg_hi:[1,0,0]
	v_cvt_pk_bf16_f32 v10, v10, v11
	v_cndmask_b32_e64 v17, 0, 1.0, vcc
	v_cmp_eq_u32_e32 vcc, v91, v148
	s_nop 1
	v_cndmask_b32_e64 v16, 0, 1.0, vcc
	v_pk_fma_f32 v[12:13], v[14:15], v[12:13], v[16:17] op_sel_hi:[0,1,1] neg_lo:[1,0,0] neg_hi:[1,0,0]
	v_cvt_pk_bf16_f32 v11, v12, v13
	ds_write_b64 v186, v[10:11] offset:2720
	ds_read_b32 v10, v187 offset:48
	v_cmp_eq_u32_e32 vcc, v98, v147
	s_nop 1
	v_cndmask_b32_e64 v12, 0, 1.0, vcc
	v_cmp_eq_u32_e32 vcc, v99, v147
	s_nop 1
	v_cndmask_b32_e64 v13, 0, 1.0, vcc
	v_cmp_eq_u32_e32 vcc, v90, v147
	s_waitcnt lgkmcnt(0)
	v_pk_fma_f32 v[6:7], v[10:11], v[6:7], v[12:13] op_sel_hi:[0,1,1] neg_lo:[1,0,0] neg_hi:[1,0,0]
	v_cvt_pk_bf16_f32 v6, v6, v7
	v_cndmask_b32_e64 v13, 0, 1.0, vcc
	v_cmp_eq_u32_e32 vcc, v91, v147
	s_nop 1
	v_cndmask_b32_e64 v12, 0, 1.0, vcc
	v_pk_fma_f32 v[8:9], v[10:11], v[8:9], v[12:13] op_sel_hi:[0,1,1] neg_lo:[1,0,0] neg_hi:[1,0,0]
	v_cvt_pk_bf16_f32 v7, v8, v9
	ds_write_b64 v186, v[6:7] offset:3264
	ds_read_b32 v6, v187 offset:56
	v_cmp_eq_u32_e32 vcc, v98, v146
	s_nop 1
	v_cndmask_b32_e64 v8, 0, 1.0, vcc
	v_cmp_eq_u32_e32 vcc, v99, v146
	s_nop 1
	v_cndmask_b32_e64 v9, 0, 1.0, vcc
	v_cmp_eq_u32_e32 vcc, v90, v146
	s_waitcnt lgkmcnt(0)
	v_pk_fma_f32 v[2:3], v[6:7], v[2:3], v[8:9] op_sel_hi:[0,1,1] neg_lo:[1,0,0] neg_hi:[1,0,0]
	v_cvt_pk_bf16_f32 v2, v2, v3
	v_cndmask_b32_e64 v9, 0, 1.0, vcc
	v_cmp_eq_u32_e32 vcc, v91, v146
	s_nop 1
	v_cndmask_b32_e64 v8, 0, 1.0, vcc
	v_pk_fma_f32 v[4:5], v[6:7], v[4:5], v[8:9] op_sel_hi:[0,1,1] neg_lo:[1,0,0] neg_hi:[1,0,0]
	v_cvt_pk_bf16_f32 v3, v4, v5
	ds_write_b64 v186, v[2:3] offset:3808
	ds_read_b128 v[2:5], v1
	ds_read_b128 v[6:9], v1 offset:64
	ds_read_b128 v[10:13], v1 offset:128
	ds_read_b128 v[14:17], v1 offset:192
	global_load_dwordx4 v[118:121], v[118:119], off offset:512 nt
	s_nop 0
	global_load_dwordx4 v[110:113], v[126:127], off offset:512 nt
	global_load_dwordx4 v[98:101], v[128:129], off offset:512 nt
	global_load_dwordx4 v[86:89], v[134:135], off offset:512 nt
	global_load_dwordx4 v[62:65], v[136:137], off offset:512 nt
	global_load_dwordx4 v[58:61], v[138:139], off offset:512 nt
	global_load_dwordx4 v[54:57], v[140:141], off offset:512 nt
	global_load_dwordx4 v[50:53], v[142:143], off offset:512 nt
	v_mov_b32_e32 v91, v133
	s_waitcnt vmcnt(23)
	s_waitcnt vmcnt(22)
	s_waitcnt vmcnt(21)
	s_waitcnt vmcnt(20)
	s_waitcnt vmcnt(19)
	s_waitcnt vmcnt(18)
	s_waitcnt vmcnt(17)
	s_waitcnt vmcnt(16)
	ds_read_b32 v90, v187 offset:64
	v_or_b32_e32 v138, 16, v132
	v_add_u32_e32 v102, 1, v91
	v_cmp_eq_u32_e32 vcc, v91, v138
	v_add_u32_e32 v103, 3, v91
	v_add_u32_e32 v104, 2, v91
	v_cndmask_b32_e64 v92, 0, 1.0, vcc
	v_cmp_eq_u32_e32 vcc, v102, v138
	v_or_b32_e32 v139, 18, v132
	v_or_b32_e32 v140, 20, v132
	v_cndmask_b32_e64 v93, 0, 1.0, vcc
	v_cmp_eq_u32_e32 vcc, v103, v138
	s_waitcnt lgkmcnt(0)
	v_pk_fma_f32 v[78:79], v[90:91], v[78:79], v[92:93] op_sel_hi:[0,1,1] neg_lo:[1,0,0] neg_hi:[1,0,0]
	v_cvt_pk_bf16_f32 v78, v78, v79
	v_cndmask_b32_e64 v93, 0, 1.0, vcc
	v_cmp_eq_u32_e32 vcc, v104, v138
	v_or_b32_e32 v141, 22, v132
	v_or_b32_e32 v142, 24, v132
	v_cndmask_b32_e64 v92, 0, 1.0, vcc
	v_pk_fma_f32 v[80:81], v[90:91], v[80:81], v[92:93] op_sel_hi:[0,1,1] neg_lo:[1,0,0] neg_hi:[1,0,0]
	v_cvt_pk_bf16_f32 v79, v80, v81
	ds_write_b64 v186, v[78:79]
	ds_read_b32 v78, v187 offset:72
	v_cmp_eq_u32_e32 vcc, v91, v139
	v_or_b32_e32 v143, 26, v132
	v_or_b32_e32 v144, 28, v132
	v_cndmask_b32_e64 v80, 0, 1.0, vcc
	v_cmp_eq_u32_e32 vcc, v102, v139
	v_or_b32_e32 v145, 30, v132
	s_nop 0
	v_cndmask_b32_e64 v81, 0, 1.0, vcc
	v_cmp_eq_u32_e32 vcc, v103, v139
	s_waitcnt lgkmcnt(0)
	v_pk_fma_f32 v[74:75], v[78:79], v[74:75], v[80:81] op_sel_hi:[0,1,1] neg_lo:[1,0,0] neg_hi:[1,0,0]
	v_cvt_pk_bf16_f32 v74, v74, v75
	v_cndmask_b32_e64 v81, 0, 1.0, vcc
	v_cmp_eq_u32_e32 vcc, v104, v139
	s_nop 1
	v_cndmask_b32_e64 v80, 0, 1.0, vcc
	v_pk_fma_f32 v[76:77], v[78:79], v[76:77], v[80:81] op_sel_hi:[0,1,1] neg_lo:[1,0,0] neg_hi:[1,0,0]
	v_cvt_pk_bf16_f32 v75, v76, v77
	ds_write_b64 v186, v[74:75] offset:544
	ds_read_b32 v74, v187 offset:80
	v_cmp_eq_u32_e32 vcc, v91, v140
	s_nop 1
	v_cndmask_b32_e64 v76, 0, 1.0, vcc
	v_cmp_eq_u32_e32 vcc, v102, v140
	s_nop 1
	v_cndmask_b32_e64 v77, 0, 1.0, vcc
	v_cmp_eq_u32_e32 vcc, v103, v140
	s_waitcnt lgkmcnt(0)
	v_pk_fma_f32 v[70:71], v[74:75], v[70:71], v[76:77] op_sel_hi:[0,1,1] neg_lo:[1,0,0] neg_hi:[1,0,0]
	v_cvt_pk_bf16_f32 v70, v70, v71
	v_cndmask_b32_e64 v77, 0, 1.0, vcc
	v_cmp_eq_u32_e32 vcc, v104, v140
	s_nop 1
	v_cndmask_b32_e64 v76, 0, 1.0, vcc
	v_pk_fma_f32 v[72:73], v[74:75], v[72:73], v[76:77] op_sel_hi:[0,1,1] neg_lo:[1,0,0] neg_hi:[1,0,0]
	v_cvt_pk_bf16_f32 v71, v72, v73
	ds_write_b64 v186, v[70:71] offset:1088
	ds_read_b32 v70, v187 offset:88
	v_cmp_eq_u32_e32 vcc, v91, v141
	s_nop 1
	v_cndmask_b32_e64 v72, 0, 1.0, vcc
	v_cmp_eq_u32_e32 vcc, v102, v141
	s_nop 1
	v_cndmask_b32_e64 v73, 0, 1.0, vcc
	v_cmp_eq_u32_e32 vcc, v103, v141
	s_waitcnt lgkmcnt(0)
	v_pk_fma_f32 v[66:67], v[70:71], v[66:67], v[72:73] op_sel_hi:[0,1,1] neg_lo:[1,0,0] neg_hi:[1,0,0]
	v_cvt_pk_bf16_f32 v66, v66, v67
	v_cndmask_b32_e64 v73, 0, 1.0, vcc
	v_cmp_eq_u32_e32 vcc, v104, v141
	s_nop 1
	v_cndmask_b32_e64 v72, 0, 1.0, vcc
	v_pk_fma_f32 v[68:69], v[70:71], v[68:69], v[72:73] op_sel_hi:[0,1,1] neg_lo:[1,0,0] neg_hi:[1,0,0]
	v_cvt_pk_bf16_f32 v67, v68, v69
	ds_write_b64 v186, v[66:67] offset:1632
	ds_read_b32 v66, v187 offset:96
	v_cmp_eq_u32_e32 vcc, v91, v142
	s_nop 1
	v_cndmask_b32_e64 v68, 0, 1.0, vcc
	v_cmp_eq_u32_e32 vcc, v102, v142
	s_nop 1
	v_cndmask_b32_e64 v69, 0, 1.0, vcc
	v_cmp_eq_u32_e32 vcc, v103, v142
	s_waitcnt lgkmcnt(0)
	v_pk_fma_f32 v[30:31], v[66:67], v[30:31], v[68:69] op_sel_hi:[0,1,1] neg_lo:[1,0,0] neg_hi:[1,0,0]
	v_cvt_pk_bf16_f32 v30, v30, v31
	v_cndmask_b32_e64 v69, 0, 1.0, vcc
	v_cmp_eq_u32_e32 vcc, v104, v142
	s_nop 1
	v_cndmask_b32_e64 v68, 0, 1.0, vcc
	v_pk_fma_f32 v[32:33], v[66:67], v[32:33], v[68:69] op_sel_hi:[0,1,1] neg_lo:[1,0,0] neg_hi:[1,0,0]
	v_cvt_pk_bf16_f32 v31, v32, v33
	ds_write_b64 v186, v[30:31] offset:2176
	ds_read_b32 v30, v187 offset:104
	v_cmp_eq_u32_e32 vcc, v91, v143
	s_nop 1
	v_cndmask_b32_e64 v32, 0, 1.0, vcc
	v_cmp_eq_u32_e32 vcc, v102, v143
	s_nop 1
	v_cndmask_b32_e64 v33, 0, 1.0, vcc
	v_cmp_eq_u32_e32 vcc, v103, v143
	s_waitcnt lgkmcnt(0)
	v_pk_fma_f32 v[26:27], v[30:31], v[26:27], v[32:33] op_sel_hi:[0,1,1] neg_lo:[1,0,0] neg_hi:[1,0,0]
	v_cvt_pk_bf16_f32 v26, v26, v27
	v_cndmask_b32_e64 v33, 0, 1.0, vcc
	v_cmp_eq_u32_e32 vcc, v104, v143
	s_nop 1
	v_cndmask_b32_e64 v32, 0, 1.0, vcc
	v_pk_fma_f32 v[28:29], v[30:31], v[28:29], v[32:33] op_sel_hi:[0,1,1] neg_lo:[1,0,0] neg_hi:[1,0,0]
	v_cvt_pk_bf16_f32 v27, v28, v29
	ds_write_b64 v186, v[26:27] offset:2720
	ds_read_b32 v26, v187 offset:112
	v_cmp_eq_u32_e32 vcc, v91, v144
	s_nop 1
	v_cndmask_b32_e64 v28, 0, 1.0, vcc
	v_cmp_eq_u32_e32 vcc, v102, v144
	s_nop 1
	v_cndmask_b32_e64 v29, 0, 1.0, vcc
	v_cmp_eq_u32_e32 vcc, v103, v144
	s_waitcnt lgkmcnt(0)
	v_pk_fma_f32 v[22:23], v[26:27], v[22:23], v[28:29] op_sel_hi:[0,1,1] neg_lo:[1,0,0] neg_hi:[1,0,0]
	v_cvt_pk_bf16_f32 v22, v22, v23
	v_cndmask_b32_e64 v29, 0, 1.0, vcc
	v_cmp_eq_u32_e32 vcc, v104, v144
	s_nop 1
	v_cndmask_b32_e64 v28, 0, 1.0, vcc
	v_pk_fma_f32 v[24:25], v[26:27], v[24:25], v[28:29] op_sel_hi:[0,1,1] neg_lo:[1,0,0] neg_hi:[1,0,0]
	v_cvt_pk_bf16_f32 v23, v24, v25
	ds_write_b64 v186, v[22:23] offset:3264
	ds_read_b32 v22, v187 offset:120
	v_cmp_eq_u32_e32 vcc, v91, v145
	s_nop 1
	v_cndmask_b32_e64 v24, 0, 1.0, vcc
	v_cmp_eq_u32_e32 vcc, v102, v145
	s_nop 1
	v_cndmask_b32_e64 v25, 0, 1.0, vcc
	v_cmp_eq_u32_e32 vcc, v103, v145
	s_waitcnt lgkmcnt(0)
	v_pk_fma_f32 v[18:19], v[22:23], v[18:19], v[24:25] op_sel_hi:[0,1,1] neg_lo:[1,0,0] neg_hi:[1,0,0]
	v_cvt_pk_bf16_f32 v18, v18, v19
	v_cndmask_b32_e64 v25, 0, 1.0, vcc
	v_cmp_eq_u32_e32 vcc, v104, v145
	s_nop 1
	v_cndmask_b32_e64 v24, 0, 1.0, vcc
	v_pk_fma_f32 v[20:21], v[22:23], v[20:21], v[24:25] op_sel_hi:[0,1,1] neg_lo:[1,0,0] neg_hi:[1,0,0]
	v_cvt_pk_bf16_f32 v19, v20, v21
	ds_write_b64 v186, v[18:19] offset:3808
	ds_read_b128 v[18:21], v1
	ds_read_b128 v[22:25], v1 offset:64
	ds_read_b128 v[26:29], v1 offset:128
	ds_read_b128 v[30:33], v1 offset:192
	v_lshl_add_u64 v[66:67], v[150:151], 0, s[8:9]
	v_lshl_add_u64 v[68:69], v[152:153], 0, s[8:9]
	v_lshl_add_u64 v[70:71], v[156:157], 0, s[8:9]
	v_lshl_add_u64 v[72:73], v[158:159], 0, s[8:9]
	v_lshl_add_u64 v[74:75], v[160:161], 0, s[8:9]
	v_lshl_add_u64 v[76:77], v[162:163], 0, s[8:9]
	v_lshl_add_u64 v[134:135], v[164:165], 0, s[8:9]
	v_lshl_add_u64 v[136:137], v[166:167], 0, s[8:9]
	global_load_dwordx4 v[126:129], v[66:67], off nt
	global_load_dwordx4 v[114:117], v[68:69], off nt
	global_load_dwordx4 v[102:105], v[70:71], off nt
	global_load_dwordx4 v[90:93], v[72:73], off nt
	global_load_dwordx4 v[78:81], v[74:75], off nt
	s_nop 0
	global_load_dwordx4 v[74:77], v[76:77], off nt
	s_nop 0
	global_load_dwordx4 v[70:73], v[134:135], off nt
	global_load_dwordx4 v[66:69], v[136:137], off nt
	s_waitcnt vmcnt(23)
	s_waitcnt vmcnt(22)
	s_waitcnt vmcnt(21)
	s_waitcnt vmcnt(20)
	s_waitcnt vmcnt(19)
	s_waitcnt vmcnt(18)
	s_waitcnt vmcnt(17)
	s_waitcnt vmcnt(16)
	ds_read_b32 v134, v187 offset:128
	v_or_b32_e32 v194, 32, v132
	v_add_u32_e32 v135, 1, v133
	v_cmp_eq_u32_e32 vcc, v133, v194
	v_add_u32_e32 v202, 3, v133
	v_add_u32_e32 v203, 2, v133
	v_cndmask_b32_e64 v136, 0, 1.0, vcc
	v_cmp_eq_u32_e32 vcc, v135, v194
	v_or_b32_e32 v195, 34, v132
	v_or_b32_e32 v196, 36, v132
	v_cndmask_b32_e64 v137, 0, 1.0, vcc
	v_cmp_eq_u32_e32 vcc, v202, v194
	s_waitcnt lgkmcnt(0)
	v_pk_fma_f32 v[122:123], v[134:135], v[122:123], v[136:137] op_sel_hi:[0,1,1] neg_lo:[1,0,0] neg_hi:[1,0,0]
	v_cvt_pk_bf16_f32 v122, v122, v123
	v_cndmask_b32_e64 v137, 0, 1.0, vcc
	v_cmp_eq_u32_e32 vcc, v203, v194
	v_or_b32_e32 v197, 38, v132
	v_or_b32_e32 v198, 40, v132
	v_cndmask_b32_e64 v136, 0, 1.0, vcc
	v_pk_fma_f32 v[124:125], v[134:135], v[124:125], v[136:137] op_sel_hi:[0,1,1] neg_lo:[1,0,0] neg_hi:[1,0,0]
	v_cvt_pk_bf16_f32 v123, v124, v125
	ds_write_b64 v186, v[122:123]
	ds_read_b32 v122, v187 offset:136
	v_cmp_eq_u32_e32 vcc, v133, v195
	v_or_b32_e32 v199, 42, v132
	v_or_b32_e32 v200, 44, v132
	v_cndmask_b32_e64 v124, 0, 1.0, vcc
	v_cmp_eq_u32_e32 vcc, v135, v195
	v_or_b32_e32 v201, 46, v132
	s_nop 0
	v_cndmask_b32_e64 v125, 0, 1.0, vcc
	v_cmp_eq_u32_e32 vcc, v202, v195
	s_waitcnt lgkmcnt(0)
	v_pk_fma_f32 v[106:107], v[122:123], v[106:107], v[124:125] op_sel_hi:[0,1,1] neg_lo:[1,0,0] neg_hi:[1,0,0]
	v_cvt_pk_bf16_f32 v106, v106, v107
	v_cndmask_b32_e64 v125, 0, 1.0, vcc
	v_cmp_eq_u32_e32 vcc, v203, v195
	s_nop 1
	v_cndmask_b32_e64 v124, 0, 1.0, vcc
	v_pk_fma_f32 v[108:109], v[122:123], v[108:109], v[124:125] op_sel_hi:[0,1,1] neg_lo:[1,0,0] neg_hi:[1,0,0]
	v_cvt_pk_bf16_f32 v107, v108, v109
	ds_write_b64 v186, v[106:107] offset:544
	ds_read_b32 v106, v187 offset:144
	v_cmp_eq_u32_e32 vcc, v133, v196
	s_nop 1
	v_cndmask_b32_e64 v108, 0, 1.0, vcc
	v_cmp_eq_u32_e32 vcc, v135, v196
	s_nop 1
	v_cndmask_b32_e64 v109, 0, 1.0, vcc
	v_cmp_eq_u32_e32 vcc, v202, v196
	s_waitcnt lgkmcnt(0)
	v_pk_fma_f32 v[94:95], v[106:107], v[94:95], v[108:109] op_sel_hi:[0,1,1] neg_lo:[1,0,0] neg_hi:[1,0,0]
	v_cvt_pk_bf16_f32 v94, v94, v95
	v_cndmask_b32_e64 v109, 0, 1.0, vcc
	v_cmp_eq_u32_e32 vcc, v203, v196
	s_nop 1
	v_cndmask_b32_e64 v108, 0, 1.0, vcc
	v_pk_fma_f32 v[96:97], v[106:107], v[96:97], v[108:109] op_sel_hi:[0,1,1] neg_lo:[1,0,0] neg_hi:[1,0,0]
	v_cvt_pk_bf16_f32 v95, v96, v97
	ds_write_b64 v186, v[94:95] offset:1088
	ds_read_b32 v94, v187 offset:152
	v_cmp_eq_u32_e32 vcc, v133, v197
	s_nop 1
	v_cndmask_b32_e64 v96, 0, 1.0, vcc
	v_cmp_eq_u32_e32 vcc, v135, v197
	s_nop 1
	v_cndmask_b32_e64 v97, 0, 1.0, vcc
	v_cmp_eq_u32_e32 vcc, v202, v197
	s_waitcnt lgkmcnt(0)
	v_pk_fma_f32 v[82:83], v[94:95], v[82:83], v[96:97] op_sel_hi:[0,1,1] neg_lo:[1,0,0] neg_hi:[1,0,0]
	v_cvt_pk_bf16_f32 v82, v82, v83
	v_cndmask_b32_e64 v97, 0, 1.0, vcc
	v_cmp_eq_u32_e32 vcc, v203, v197
	s_nop 1
	v_cndmask_b32_e64 v96, 0, 1.0, vcc
	v_pk_fma_f32 v[84:85], v[94:95], v[84:85], v[96:97] op_sel_hi:[0,1,1] neg_lo:[1,0,0] neg_hi:[1,0,0]
	v_cvt_pk_bf16_f32 v83, v84, v85
	ds_write_b64 v186, v[82:83] offset:1632
	ds_read_b32 v82, v187 offset:160
	v_cmp_eq_u32_e32 vcc, v133, v198
	s_nop 1
	v_cndmask_b32_e64 v84, 0, 1.0, vcc
	v_cmp_eq_u32_e32 vcc, v135, v198
	s_nop 1
	v_cndmask_b32_e64 v85, 0, 1.0, vcc
	v_cmp_eq_u32_e32 vcc, v202, v198
	s_waitcnt lgkmcnt(0)
	v_pk_fma_f32 v[46:47], v[82:83], v[46:47], v[84:85] op_sel_hi:[0,1,1] neg_lo:[1,0,0] neg_hi:[1,0,0]
	v_cvt_pk_bf16_f32 v46, v46, v47
	v_cndmask_b32_e64 v85, 0, 1.0, vcc
	v_cmp_eq_u32_e32 vcc, v203, v198
	s_nop 1
	v_cndmask_b32_e64 v84, 0, 1.0, vcc
	v_pk_fma_f32 v[48:49], v[82:83], v[48:49], v[84:85] op_sel_hi:[0,1,1] neg_lo:[1,0,0] neg_hi:[1,0,0]
	v_cvt_pk_bf16_f32 v47, v48, v49
	ds_write_b64 v186, v[46:47] offset:2176
	ds_read_b32 v46, v187 offset:168
	v_cmp_eq_u32_e32 vcc, v133, v199
	s_nop 1
	v_cndmask_b32_e64 v48, 0, 1.0, vcc
	v_cmp_eq_u32_e32 vcc, v135, v199
	s_nop 1
	v_cndmask_b32_e64 v49, 0, 1.0, vcc
	v_cmp_eq_u32_e32 vcc, v202, v199
	s_waitcnt lgkmcnt(0)
	v_pk_fma_f32 v[42:43], v[46:47], v[42:43], v[48:49] op_sel_hi:[0,1,1] neg_lo:[1,0,0] neg_hi:[1,0,0]
	v_cvt_pk_bf16_f32 v42, v42, v43
	v_cndmask_b32_e64 v49, 0, 1.0, vcc
	v_cmp_eq_u32_e32 vcc, v203, v199
	s_nop 1
	v_cndmask_b32_e64 v48, 0, 1.0, vcc
	v_pk_fma_f32 v[44:45], v[46:47], v[44:45], v[48:49] op_sel_hi:[0,1,1] neg_lo:[1,0,0] neg_hi:[1,0,0]
	v_cvt_pk_bf16_f32 v43, v44, v45
	ds_write_b64 v186, v[42:43] offset:2720
	ds_read_b32 v42, v187 offset:176
	v_cmp_eq_u32_e32 vcc, v133, v200
	s_nop 1
	v_cndmask_b32_e64 v44, 0, 1.0, vcc
	v_cmp_eq_u32_e32 vcc, v135, v200
	s_nop 1
	v_cndmask_b32_e64 v45, 0, 1.0, vcc
	v_cmp_eq_u32_e32 vcc, v202, v200
	s_waitcnt lgkmcnt(0)
	v_pk_fma_f32 v[38:39], v[42:43], v[38:39], v[44:45] op_sel_hi:[0,1,1] neg_lo:[1,0,0] neg_hi:[1,0,0]
	v_cvt_pk_bf16_f32 v38, v38, v39
	v_cndmask_b32_e64 v45, 0, 1.0, vcc
	v_cmp_eq_u32_e32 vcc, v203, v200
	s_nop 1
	v_cndmask_b32_e64 v44, 0, 1.0, vcc
	v_pk_fma_f32 v[40:41], v[42:43], v[40:41], v[44:45] op_sel_hi:[0,1,1] neg_lo:[1,0,0] neg_hi:[1,0,0]
	v_cvt_pk_bf16_f32 v39, v40, v41
	ds_write_b64 v186, v[38:39] offset:3264
	ds_read_b32 v38, v187 offset:184
	v_cmp_eq_u32_e32 vcc, v133, v201
	s_nop 1
	v_cndmask_b32_e64 v40, 0, 1.0, vcc
	v_cmp_eq_u32_e32 vcc, v135, v201
	s_nop 1
	v_cndmask_b32_e64 v41, 0, 1.0, vcc
	v_cmp_eq_u32_e32 vcc, v202, v201
	s_waitcnt lgkmcnt(0)
	v_pk_fma_f32 v[34:35], v[38:39], v[34:35], v[40:41] op_sel_hi:[0,1,1] neg_lo:[1,0,0] neg_hi:[1,0,0]
	v_cvt_pk_bf16_f32 v34, v34, v35
	v_cndmask_b32_e64 v41, 0, 1.0, vcc
	v_cmp_eq_u32_e32 vcc, v203, v201
	s_nop 1
	v_cndmask_b32_e64 v40, 0, 1.0, vcc
	v_pk_fma_f32 v[36:37], v[38:39], v[36:37], v[40:41] op_sel_hi:[0,1,1] neg_lo:[1,0,0] neg_hi:[1,0,0]
	v_cvt_pk_bf16_f32 v35, v36, v37
	ds_write_b64 v186, v[34:35] offset:3808
	ds_read_b128 v[34:37], v1
	ds_read_b128 v[38:41], v1 offset:64
	ds_read_b128 v[42:45], v1 offset:128
	ds_read_b128 v[46:49], v1 offset:192
	v_mov_b32_e32 v106, v189
	s_waitcnt vmcnt(15)
	s_waitcnt vmcnt(14)
	s_waitcnt vmcnt(13)
	s_waitcnt vmcnt(12)
	s_waitcnt vmcnt(11)
	s_waitcnt vmcnt(10)
	s_waitcnt vmcnt(9)
	s_waitcnt vmcnt(8)
	ds_read_b32 v82, v187
	v_add_u32_e32 v107, 1, v106
	v_cmp_eq_u32_e32 vcc, v106, v132
	v_add_u32_e32 v108, 3, v106
	v_add_u32_e32 v109, 2, v106
	v_cndmask_b32_e64 v84, 0, 1.0, vcc
	v_cmp_eq_u32_e32 vcc, v107, v132
	s_nop 1
	v_cndmask_b32_e64 v85, 0, 1.0, vcc
	v_cmp_eq_u32_e32 vcc, v108, v132
	s_waitcnt lgkmcnt(0)
	v_pk_fma_f32 v[94:95], v[82:83], v[118:119], v[84:85] op_sel_hi:[0,1,1] neg_lo:[1,0,0] neg_hi:[1,0,0]
	v_cvt_pk_bf16_f32 v94, v94, v95
	v_cndmask_b32_e64 v97, 0, 1.0, vcc
	v_cmp_eq_u32_e32 vcc, v109, v132
	s_nop 1
	v_cndmask_b32_e64 v96, 0, 1.0, vcc
	v_pk_fma_f32 v[82:83], v[82:83], v[120:121], v[96:97] op_sel_hi:[0,1,1] neg_lo:[1,0,0] neg_hi:[1,0,0]
	v_cvt_pk_bf16_f32 v95, v82, v83
	ds_write_b64 v186, v[94:95]
	ds_read_b32 v82, v187 offset:8
	v_cmp_eq_u32_e32 vcc, v106, v193
	s_nop 1
	v_cndmask_b32_e64 v94, 0, 1.0, vcc
	v_cmp_eq_u32_e32 vcc, v107, v193
	s_nop 1
	v_cndmask_b32_e64 v95, 0, 1.0, vcc
	v_cmp_eq_u32_e32 vcc, v108, v193
	s_waitcnt lgkmcnt(0)
	v_pk_fma_f32 v[94:95], v[82:83], v[110:111], v[94:95] op_sel_hi:[0,1,1] neg_lo:[1,0,0] neg_hi:[1,0,0]
	v_cvt_pk_bf16_f32 v94, v94, v95
	v_cndmask_b32_e64 v85, 0, 1.0, vcc
	v_pk_fma_f32 v[82:83], v[82:83], v[112:113], v[84:85] op_sel_hi:[0,1,1] neg_lo:[1,0,0] neg_hi:[1,0,0]
	v_cvt_pk_bf16_f32 v95, v82, v83
	ds_write_b64 v186, v[94:95] offset:544
	ds_read_b32 v82, v187 offset:16
	v_cmp_eq_u32_e32 vcc, v106, v192
	s_nop 1
	v_cndmask_b32_e64 v84, 0, 1.0, vcc
	v_cmp_eq_u32_e32 vcc, v107, v192
	s_nop 1
	v_cndmask_b32_e64 v85, 0, 1.0, vcc
	v_cmp_eq_u32_e32 vcc, v108, v192
	s_waitcnt lgkmcnt(0)
	v_pk_fma_f32 v[84:85], v[82:83], v[98:99], v[84:85] op_sel_hi:[0,1,1] neg_lo:[1,0,0] neg_hi:[1,0,0]
	v_cvt_pk_bf16_f32 v84, v84, v85
	v_cndmask_b32_e64 v95, 0, 1.0, vcc
	v_cmp_eq_u32_e32 vcc, v109, v192
	s_nop 1
	v_cndmask_b32_e64 v94, 0, 1.0, vcc
	v_pk_fma_f32 v[82:83], v[82:83], v[100:101], v[94:95] op_sel_hi:[0,1,1] neg_lo:[1,0,0] neg_hi:[1,0,0]
	v_cvt_pk_bf16_f32 v85, v82, v83
	ds_write_b64 v186, v[84:85] offset:1088
	ds_read_b32 v82, v187 offset:24
	v_cmp_eq_u32_e32 vcc, v106, v190
	s_nop 1
	v_cndmask_b32_e64 v84, 0, 1.0, vcc
	v_cmp_eq_u32_e32 vcc, v107, v190
	s_nop 1
	v_cndmask_b32_e64 v85, 0, 1.0, vcc
	v_cmp_eq_u32_e32 vcc, v108, v190
	s_waitcnt lgkmcnt(0)
	v_pk_fma_f32 v[84:85], v[82:83], v[86:87], v[84:85] op_sel_hi:[0,1,1] neg_lo:[1,0,0] neg_hi:[1,0,0]
	v_cvt_pk_bf16_f32 v84, v84, v85
	v_cndmask_b32_e64 v87, 0, 1.0, vcc
	v_cmp_eq_u32_e32 vcc, v109, v190
	s_nop 1
	v_cndmask_b32_e64 v86, 0, 1.0, vcc
	v_pk_fma_f32 v[82:83], v[82:83], v[88:89], v[86:87] op_sel_hi:[0,1,1] neg_lo:[1,0,0] neg_hi:[1,0,0]
	v_cvt_pk_bf16_f32 v85, v82, v83
	ds_write_b64 v186, v[84:85] offset:1632
	ds_read_b32 v82, v187 offset:32
	v_cmp_eq_u32_e32 vcc, v106, v149
	s_nop 1
	v_cndmask_b32_e64 v84, 0, 1.0, vcc
	v_cmp_eq_u32_e32 vcc, v107, v149
	s_nop 1
	v_cndmask_b32_e64 v85, 0, 1.0, vcc
	v_cmp_eq_u32_e32 vcc, v108, v149
	s_waitcnt lgkmcnt(0)
	v_pk_fma_f32 v[62:63], v[82:83], v[62:63], v[84:85] op_sel_hi:[0,1,1] neg_lo:[1,0,0] neg_hi:[1,0,0]
	v_cvt_pk_bf16_f32 v62, v62, v63
	v_cndmask_b32_e64 v85, 0, 1.0, vcc
	v_cmp_eq_u32_e32 vcc, v109, v149
	s_nop 1
	v_cndmask_b32_e64 v84, 0, 1.0, vcc
	v_pk_fma_f32 v[64:65], v[82:83], v[64:65], v[84:85] op_sel_hi:[0,1,1] neg_lo:[1,0,0] neg_hi:[1,0,0]
	v_cvt_pk_bf16_f32 v63, v64, v65
	ds_write_b64 v186, v[62:63] offset:2176
	ds_read_b32 v62, v187 offset:40
	v_cmp_eq_u32_e32 vcc, v106, v148
	s_nop 1
	v_cndmask_b32_e64 v64, 0, 1.0, vcc
	v_cmp_eq_u32_e32 vcc, v107, v148
	s_nop 1
	v_cndmask_b32_e64 v65, 0, 1.0, vcc
	v_cmp_eq_u32_e32 vcc, v108, v148
	s_waitcnt lgkmcnt(0)
	v_pk_fma_f32 v[58:59], v[62:63], v[58:59], v[64:65] op_sel_hi:[0,1,1] neg_lo:[1,0,0] neg_hi:[1,0,0]
	v_cvt_pk_bf16_f32 v58, v58, v59
	v_cndmask_b32_e64 v65, 0, 1.0, vcc
	v_cmp_eq_u32_e32 vcc, v109, v148
	s_nop 1
	v_cndmask_b32_e64 v64, 0, 1.0, vcc
	v_pk_fma_f32 v[60:61], v[62:63], v[60:61], v[64:65] op_sel_hi:[0,1,1] neg_lo:[1,0,0] neg_hi:[1,0,0]
	v_cvt_pk_bf16_f32 v59, v60, v61
	ds_write_b64 v186, v[58:59] offset:2720
	ds_read_b32 v58, v187 offset:48
	v_cmp_eq_u32_e32 vcc, v106, v147
	s_nop 1
	v_cndmask_b32_e64 v60, 0, 1.0, vcc
	v_cmp_eq_u32_e32 vcc, v107, v147
	s_nop 1
	v_cndmask_b32_e64 v61, 0, 1.0, vcc
	v_cmp_eq_u32_e32 vcc, v108, v147
	s_waitcnt lgkmcnt(0)
	v_pk_fma_f32 v[54:55], v[58:59], v[54:55], v[60:61] op_sel_hi:[0,1,1] neg_lo:[1,0,0] neg_hi:[1,0,0]
	v_cvt_pk_bf16_f32 v54, v54, v55
	v_cndmask_b32_e64 v61, 0, 1.0, vcc
	v_cmp_eq_u32_e32 vcc, v109, v147
	s_nop 1
	v_cndmask_b32_e64 v60, 0, 1.0, vcc
	v_pk_fma_f32 v[56:57], v[58:59], v[56:57], v[60:61] op_sel_hi:[0,1,1] neg_lo:[1,0,0] neg_hi:[1,0,0]
	v_cvt_pk_bf16_f32 v55, v56, v57
	ds_write_b64 v186, v[54:55] offset:3264
	ds_read_b32 v54, v187 offset:56
	v_cmp_eq_u32_e32 vcc, v106, v146
	s_nop 1
	v_cndmask_b32_e64 v56, 0, 1.0, vcc
	v_cmp_eq_u32_e32 vcc, v107, v146
	s_nop 1
	v_cndmask_b32_e64 v57, 0, 1.0, vcc
	v_cmp_eq_u32_e32 vcc, v108, v146
	s_waitcnt lgkmcnt(0)
	v_pk_fma_f32 v[50:51], v[54:55], v[50:51], v[56:57] op_sel_hi:[0,1,1] neg_lo:[1,0,0] neg_hi:[1,0,0]
	v_cvt_pk_bf16_f32 v50, v50, v51
	v_cndmask_b32_e64 v57, 0, 1.0, vcc
	v_cmp_eq_u32_e32 vcc, v109, v146
	s_nop 1
	v_cndmask_b32_e64 v56, 0, 1.0, vcc
	v_pk_fma_f32 v[52:53], v[54:55], v[52:53], v[56:57] op_sel_hi:[0,1,1] neg_lo:[1,0,0] neg_hi:[1,0,0]
	v_cvt_pk_bf16_f32 v51, v52, v53
	ds_write_b64 v186, v[50:51] offset:3808
	ds_read_b128 v[50:53], v1
	ds_read_b128 v[54:57], v1 offset:64
	ds_read_b128 v[58:61], v1 offset:128
	ds_read_b128 v[62:65], v1 offset:192
	v_lshl_add_u64 v[82:83], v[168:169], 0, s[8:9]
	v_lshl_add_u64 v[84:85], v[170:171], 0, s[8:9]
	v_lshl_add_u64 v[86:87], v[172:173], 0, s[8:9]
	v_lshl_add_u64 v[88:89], v[174:175], 0, s[8:9]
	v_lshl_add_u64 v[94:95], v[176:177], 0, s[8:9]
	v_lshl_add_u64 v[96:97], v[178:179], 0, s[8:9]
	v_lshl_add_u64 v[122:123], v[180:181], 0, s[8:9]
	v_lshl_add_u64 v[124:125], v[182:183], 0, s[8:9]
	global_load_dwordx4 v[134:137], v[82:83], off nt
	global_load_dwordx4 v[118:121], v[84:85], off nt
	global_load_dwordx4 v[110:113], v[86:87], off nt
	global_load_dwordx4 v[106:109], v[88:89], off nt
	global_load_dwordx4 v[98:101], v[94:95], off nt
	s_nop 0
	global_load_dwordx4 v[94:97], v[96:97], off nt
	s_nop 0
	global_load_dwordx4 v[86:89], v[122:123], off nt
	global_load_dwordx4 v[82:85], v[124:125], off nt
	v_mov_b32_e32 v132, v189
	s_waitcnt vmcnt(15)
	s_waitcnt vmcnt(14)
	s_waitcnt vmcnt(13)
	s_waitcnt vmcnt(12)
	s_waitcnt vmcnt(11)
	s_waitcnt vmcnt(10)
	s_waitcnt vmcnt(9)
	s_waitcnt vmcnt(8)
	ds_read_b32 v122, v187 offset:64
	v_add_u32_e32 v133, 1, v132
	v_cmp_eq_u32_e32 vcc, v132, v138
	v_add_u32_e32 v146, 3, v132
	v_add_u32_e32 v147, 2, v132
	v_cndmask_b32_e64 v124, 0, 1.0, vcc
	v_cmp_eq_u32_e32 vcc, v133, v138
	s_nop 1
	v_cndmask_b32_e64 v125, 0, 1.0, vcc
	v_cmp_eq_u32_e32 vcc, v146, v138
	s_waitcnt lgkmcnt(0)
	v_pk_fma_f32 v[124:125], v[122:123], v[126:127], v[124:125] op_sel_hi:[0,1,1] neg_lo:[1,0,0] neg_hi:[1,0,0]
	v_cvt_pk_bf16_f32 v124, v124, v125
	v_cndmask_b32_e64 v127, 0, 1.0, vcc
	v_cmp_eq_u32_e32 vcc, v147, v138
	s_nop 1
	v_cndmask_b32_e64 v126, 0, 1.0, vcc
	v_pk_fma_f32 v[122:123], v[122:123], v[128:129], v[126:127] op_sel_hi:[0,1,1] neg_lo:[1,0,0] neg_hi:[1,0,0]
	v_cvt_pk_bf16_f32 v125, v122, v123
	ds_write_b64 v186, v[124:125]
	ds_read_b32 v122, v187 offset:72
	v_cmp_eq_u32_e32 vcc, v132, v139
	s_nop 1
	v_cndmask_b32_e64 v124, 0, 1.0, vcc
	v_cmp_eq_u32_e32 vcc, v133, v139
	s_nop 1
	v_cndmask_b32_e64 v125, 0, 1.0, vcc
	v_cmp_eq_u32_e32 vcc, v146, v139
	s_waitcnt lgkmcnt(0)
	v_pk_fma_f32 v[114:115], v[122:123], v[114:115], v[124:125] op_sel_hi:[0,1,1] neg_lo:[1,0,0] neg_hi:[1,0,0]
	v_cvt_pk_bf16_f32 v114, v114, v115
	v_cndmask_b32_e64 v125, 0, 1.0, vcc
	v_cmp_eq_u32_e32 vcc, v147, v139
	s_nop 1
	v_cndmask_b32_e64 v124, 0, 1.0, vcc
	v_pk_fma_f32 v[116:117], v[122:123], v[116:117], v[124:125] op_sel_hi:[0,1,1] neg_lo:[1,0,0] neg_hi:[1,0,0]
	v_cvt_pk_bf16_f32 v115, v116, v117
	ds_write_b64 v186, v[114:115] offset:544
	ds_read_b32 v114, v187 offset:80
	v_cmp_eq_u32_e32 vcc, v132, v140
	s_nop 1
	v_cndmask_b32_e64 v116, 0, 1.0, vcc
	v_cmp_eq_u32_e32 vcc, v133, v140
	s_nop 1
	v_cndmask_b32_e64 v117, 0, 1.0, vcc
	v_cmp_eq_u32_e32 vcc, v146, v140
	s_waitcnt lgkmcnt(0)
	v_pk_fma_f32 v[102:103], v[114:115], v[102:103], v[116:117] op_sel_hi:[0,1,1] neg_lo:[1,0,0] neg_hi:[1,0,0]
	v_cvt_pk_bf16_f32 v102, v102, v103
	v_cndmask_b32_e64 v117, 0, 1.0, vcc
	v_cmp_eq_u32_e32 vcc, v147, v140
	s_nop 1
	v_cndmask_b32_e64 v116, 0, 1.0, vcc
	v_pk_fma_f32 v[104:105], v[114:115], v[104:105], v[116:117] op_sel_hi:[0,1,1] neg_lo:[1,0,0] neg_hi:[1,0,0]
	v_cvt_pk_bf16_f32 v103, v104, v105
	ds_write_b64 v186, v[102:103] offset:1088
	ds_read_b32 v102, v187 offset:88
	v_cmp_eq_u32_e32 vcc, v132, v141
	s_nop 1
	v_cndmask_b32_e64 v104, 0, 1.0, vcc
	v_cmp_eq_u32_e32 vcc, v133, v141
	s_nop 1
	v_cndmask_b32_e64 v105, 0, 1.0, vcc
	v_cmp_eq_u32_e32 vcc, v146, v141
	s_waitcnt lgkmcnt(0)
	v_pk_fma_f32 v[90:91], v[102:103], v[90:91], v[104:105] op_sel_hi:[0,1,1] neg_lo:[1,0,0] neg_hi:[1,0,0]
	v_cvt_pk_bf16_f32 v90, v90, v91
	v_cndmask_b32_e64 v105, 0, 1.0, vcc
	v_cmp_eq_u32_e32 vcc, v147, v141
	s_nop 1
	v_cndmask_b32_e64 v104, 0, 1.0, vcc
	v_pk_fma_f32 v[92:93], v[102:103], v[92:93], v[104:105] op_sel_hi:[0,1,1] neg_lo:[1,0,0] neg_hi:[1,0,0]
	v_cvt_pk_bf16_f32 v91, v92, v93
	ds_write_b64 v186, v[90:91] offset:1632
	ds_read_b32 v90, v187 offset:96
	v_cmp_eq_u32_e32 vcc, v132, v142
	s_nop 1
	v_cndmask_b32_e64 v92, 0, 1.0, vcc
	v_cmp_eq_u32_e32 vcc, v133, v142
	s_nop 1
	v_cndmask_b32_e64 v93, 0, 1.0, vcc
	v_cmp_eq_u32_e32 vcc, v146, v142
	s_waitcnt lgkmcnt(0)
	v_pk_fma_f32 v[78:79], v[90:91], v[78:79], v[92:93] op_sel_hi:[0,1,1] neg_lo:[1,0,0] neg_hi:[1,0,0]
	v_cvt_pk_bf16_f32 v78, v78, v79
	v_cndmask_b32_e64 v93, 0, 1.0, vcc
	v_cmp_eq_u32_e32 vcc, v147, v142
	s_nop 1
	v_cndmask_b32_e64 v92, 0, 1.0, vcc
	v_pk_fma_f32 v[80:81], v[90:91], v[80:81], v[92:93] op_sel_hi:[0,1,1] neg_lo:[1,0,0] neg_hi:[1,0,0]
	v_cvt_pk_bf16_f32 v79, v80, v81
	ds_write_b64 v186, v[78:79] offset:2176
	ds_read_b32 v78, v187 offset:104
	v_cmp_eq_u32_e32 vcc, v132, v143
	s_nop 1
	v_cndmask_b32_e64 v80, 0, 1.0, vcc
	v_cmp_eq_u32_e32 vcc, v133, v143
	s_nop 1
	v_cndmask_b32_e64 v81, 0, 1.0, vcc
	v_cmp_eq_u32_e32 vcc, v146, v143
	s_waitcnt lgkmcnt(0)
	v_pk_fma_f32 v[74:75], v[78:79], v[74:75], v[80:81] op_sel_hi:[0,1,1] neg_lo:[1,0,0] neg_hi:[1,0,0]
	v_cvt_pk_bf16_f32 v74, v74, v75
	v_cndmask_b32_e64 v81, 0, 1.0, vcc
	v_cmp_eq_u32_e32 vcc, v147, v143
	s_nop 1
	v_cndmask_b32_e64 v80, 0, 1.0, vcc
	v_pk_fma_f32 v[76:77], v[78:79], v[76:77], v[80:81] op_sel_hi:[0,1,1] neg_lo:[1,0,0] neg_hi:[1,0,0]
	v_cvt_pk_bf16_f32 v75, v76, v77
	ds_write_b64 v186, v[74:75] offset:2720
	ds_read_b32 v74, v187 offset:112
	v_cmp_eq_u32_e32 vcc, v132, v144
	s_nop 1
	v_cndmask_b32_e64 v76, 0, 1.0, vcc
	v_cmp_eq_u32_e32 vcc, v133, v144
	s_nop 1
	v_cndmask_b32_e64 v77, 0, 1.0, vcc
	v_cmp_eq_u32_e32 vcc, v146, v144
	s_waitcnt lgkmcnt(0)
	v_pk_fma_f32 v[70:71], v[74:75], v[70:71], v[76:77] op_sel_hi:[0,1,1] neg_lo:[1,0,0] neg_hi:[1,0,0]
	v_cvt_pk_bf16_f32 v70, v70, v71
	v_cndmask_b32_e64 v77, 0, 1.0, vcc
	v_cmp_eq_u32_e32 vcc, v147, v144
	s_nop 1
	v_cndmask_b32_e64 v76, 0, 1.0, vcc
	v_pk_fma_f32 v[72:73], v[74:75], v[72:73], v[76:77] op_sel_hi:[0,1,1] neg_lo:[1,0,0] neg_hi:[1,0,0]
	v_cvt_pk_bf16_f32 v71, v72, v73
	ds_write_b64 v186, v[70:71] offset:3264
	ds_read_b32 v70, v187 offset:120
	v_cmp_eq_u32_e32 vcc, v132, v145
	s_nop 1
	v_cndmask_b32_e64 v72, 0, 1.0, vcc
	v_cmp_eq_u32_e32 vcc, v133, v145
	s_nop 1
	v_cndmask_b32_e64 v73, 0, 1.0, vcc
	v_cmp_eq_u32_e32 vcc, v146, v145
	s_waitcnt lgkmcnt(0)
	v_pk_fma_f32 v[66:67], v[70:71], v[66:67], v[72:73] op_sel_hi:[0,1,1] neg_lo:[1,0,0] neg_hi:[1,0,0]
	v_cvt_pk_bf16_f32 v66, v66, v67
	v_cndmask_b32_e64 v73, 0, 1.0, vcc
	v_cmp_eq_u32_e32 vcc, v147, v145
	s_nop 1
	v_cndmask_b32_e64 v72, 0, 1.0, vcc
	v_pk_fma_f32 v[68:69], v[70:71], v[68:69], v[72:73] op_sel_hi:[0,1,1] neg_lo:[1,0,0] neg_hi:[1,0,0]
	v_cvt_pk_bf16_f32 v67, v68, v69
	ds_write_b64 v186, v[66:67] offset:3808
	ds_read_b128 v[66:69], v1
	ds_read_b128 v[70:73], v1 offset:64
	ds_read_b128 v[74:77], v1 offset:128
	ds_read_b128 v[78:81], v1 offset:192
	v_lshl_add_u64 v[90:91], v[130:131], 0, s[0:1]
	v_add_co_u32_e32 v92, vcc, s7, v90
	s_nop 1
	v_addc_co_u32_e32 v93, vcc, 0, v91, vcc
	global_load_dwordx4 v[146:149], v[90:91], off nt
	global_load_dwordx4 v[142:145], v[92:93], off nt
	v_add_co_u32_e32 v92, vcc, s36, v90
	s_nop 1
	v_addc_co_u32_e32 v93, vcc, 0, v91, vcc
	v_add_co_u32_e32 v102, vcc, s37, v90
	s_nop 1
	v_addc_co_u32_e32 v103, vcc, 0, v91, vcc
	global_load_dwordx4 v[138:141], v[92:93], off nt
	global_load_dwordx4 v[130:133], v[102:103], off nt
	v_add_co_u32_e32 v92, vcc, s38, v90
	s_nop 1
	v_addc_co_u32_e32 v93, vcc, 0, v91, vcc
	v_add_co_u32_e32 v102, vcc, s39, v90
	s_nop 1
	v_addc_co_u32_e32 v103, vcc, 0, v91, vcc
	global_load_dwordx4 v[126:129], v[92:93], off nt
	global_load_dwordx4 v[122:125], v[102:103], off nt
	v_add_co_u32_e32 v92, vcc, s41, v90
	s_nop 1
	v_addc_co_u32_e32 v93, vcc, 0, v91, vcc
	v_add_co_u32_e32 v90, vcc, s42, v90
	s_nop 1
	v_addc_co_u32_e32 v91, vcc, 0, v91, vcc
	global_load_dwordx4 v[114:117], v[92:93], off nt
	global_load_dwordx4 v[102:105], v[90:91], off nt
	s_waitcnt vmcnt(15)
	s_waitcnt vmcnt(14)
	s_waitcnt vmcnt(13)
	s_waitcnt vmcnt(12)
	s_waitcnt vmcnt(11)
	s_waitcnt vmcnt(10)
	s_waitcnt vmcnt(9)
	s_waitcnt vmcnt(8)
	ds_read_b32 v90, v187 offset:128
	v_add_u32_e32 v190, 1, v189
	v_cmp_eq_u32_e32 vcc, v189, v194
	v_add_u32_e32 v192, 3, v189
	v_add_u32_e32 v193, 2, v189
	v_cndmask_b32_e64 v92, 0, 1.0, vcc
	v_cmp_eq_u32_e32 vcc, v190, v194
	s_nop 1
	v_cndmask_b32_e64 v93, 0, 1.0, vcc
	v_cmp_eq_u32_e32 vcc, v192, v194
	s_waitcnt lgkmcnt(0)
	v_pk_fma_f32 v[92:93], v[90:91], v[134:135], v[92:93] op_sel_hi:[0,1,1] neg_lo:[1,0,0] neg_hi:[1,0,0]
	v_cvt_pk_bf16_f32 v92, v92, v93
	v_cndmask_b32_e64 v135, 0, 1.0, vcc
	v_cmp_eq_u32_e32 vcc, v193, v194
	s_nop 1
	v_cndmask_b32_e64 v134, 0, 1.0, vcc
	v_pk_fma_f32 v[90:91], v[90:91], v[136:137], v[134:135] op_sel_hi:[0,1,1] neg_lo:[1,0,0] neg_hi:[1,0,0]
	v_cvt_pk_bf16_f32 v93, v90, v91
	ds_write_b64 v186, v[92:93]
	ds_read_b32 v90, v187 offset:136
	v_cmp_eq_u32_e32 vcc, v189, v195
	s_nop 1
	v_cndmask_b32_e64 v92, 0, 1.0, vcc
	v_cmp_eq_u32_e32 vcc, v190, v195
	s_nop 1
	v_cndmask_b32_e64 v93, 0, 1.0, vcc
	v_cmp_eq_u32_e32 vcc, v192, v195
	s_waitcnt lgkmcnt(0)
	v_pk_fma_f32 v[92:93], v[90:91], v[118:119], v[92:93] op_sel_hi:[0,1,1] neg_lo:[1,0,0] neg_hi:[1,0,0]
	v_cvt_pk_bf16_f32 v92, v92, v93
	v_cndmask_b32_e64 v119, 0, 1.0, vcc
	v_cmp_eq_u32_e32 vcc, v193, v195
	s_nop 1
	v_cndmask_b32_e64 v118, 0, 1.0, vcc
	v_pk_fma_f32 v[90:91], v[90:91], v[120:121], v[118:119] op_sel_hi:[0,1,1] neg_lo:[1,0,0] neg_hi:[1,0,0]
	v_cvt_pk_bf16_f32 v93, v90, v91
	ds_write_b64 v186, v[92:93] offset:544
	ds_read_b32 v90, v187 offset:144
	v_cmp_eq_u32_e32 vcc, v189, v196
	s_nop 1
	v_cndmask_b32_e64 v92, 0, 1.0, vcc
	v_cmp_eq_u32_e32 vcc, v190, v196
	s_nop 1
	v_cndmask_b32_e64 v93, 0, 1.0, vcc
	v_cmp_eq_u32_e32 vcc, v192, v196
	s_waitcnt lgkmcnt(0)
	v_pk_fma_f32 v[92:93], v[90:91], v[110:111], v[92:93] op_sel_hi:[0,1,1] neg_lo:[1,0,0] neg_hi:[1,0,0]
	v_cvt_pk_bf16_f32 v92, v92, v93
	v_cndmask_b32_e64 v111, 0, 1.0, vcc
	v_cmp_eq_u32_e32 vcc, v193, v196
	s_nop 1
	v_cndmask_b32_e64 v110, 0, 1.0, vcc
	v_pk_fma_f32 v[90:91], v[90:91], v[112:113], v[110:111] op_sel_hi:[0,1,1] neg_lo:[1,0,0] neg_hi:[1,0,0]
	v_cvt_pk_bf16_f32 v93, v90, v91
	ds_write_b64 v186, v[92:93] offset:1088
	ds_read_b32 v90, v187 offset:152
	v_cmp_eq_u32_e32 vcc, v189, v197
	s_nop 1
	v_cndmask_b32_e64 v92, 0, 1.0, vcc
	v_cmp_eq_u32_e32 vcc, v190, v197
	s_nop 1
	v_cndmask_b32_e64 v93, 0, 1.0, vcc
	v_cmp_eq_u32_e32 vcc, v192, v197
	s_waitcnt lgkmcnt(0)
	v_pk_fma_f32 v[92:93], v[90:91], v[106:107], v[92:93] op_sel_hi:[0,1,1] neg_lo:[1,0,0] neg_hi:[1,0,0]
	v_cvt_pk_bf16_f32 v92, v92, v93
	v_cndmask_b32_e64 v107, 0, 1.0, vcc
	v_cmp_eq_u32_e32 vcc, v193, v197
	s_nop 1
	v_cndmask_b32_e64 v106, 0, 1.0, vcc
	v_pk_fma_f32 v[90:91], v[90:91], v[108:109], v[106:107] op_sel_hi:[0,1,1] neg_lo:[1,0,0] neg_hi:[1,0,0]
	v_cvt_pk_bf16_f32 v93, v90, v91
	ds_write_b64 v186, v[92:93] offset:1632
	ds_read_b32 v90, v187 offset:160
	v_cmp_eq_u32_e32 vcc, v189, v198
	s_nop 1
	v_cndmask_b32_e64 v92, 0, 1.0, vcc
	v_cmp_eq_u32_e32 vcc, v190, v198
	s_nop 1
	v_cndmask_b32_e64 v93, 0, 1.0, vcc
	v_cmp_eq_u32_e32 vcc, v192, v198
	s_waitcnt lgkmcnt(0)
	v_pk_fma_f32 v[92:93], v[90:91], v[98:99], v[92:93] op_sel_hi:[0,1,1] neg_lo:[1,0,0] neg_hi:[1,0,0]
	v_cvt_pk_bf16_f32 v92, v92, v93
	v_cndmask_b32_e64 v99, 0, 1.0, vcc
	v_cmp_eq_u32_e32 vcc, v193, v198
	s_nop 1
	v_cndmask_b32_e64 v98, 0, 1.0, vcc
	v_pk_fma_f32 v[90:91], v[90:91], v[100:101], v[98:99] op_sel_hi:[0,1,1] neg_lo:[1,0,0] neg_hi:[1,0,0]
	v_cvt_pk_bf16_f32 v93, v90, v91
	ds_write_b64 v186, v[92:93] offset:2176
	ds_read_b32 v90, v187 offset:168
	v_cmp_eq_u32_e32 vcc, v189, v199
	s_nop 1
	v_cndmask_b32_e64 v92, 0, 1.0, vcc
	v_cmp_eq_u32_e32 vcc, v190, v199
	s_nop 1
	v_cndmask_b32_e64 v93, 0, 1.0, vcc
	v_cmp_eq_u32_e32 vcc, v192, v199
	s_waitcnt lgkmcnt(0)
	v_pk_fma_f32 v[92:93], v[90:91], v[94:95], v[92:93] op_sel_hi:[0,1,1] neg_lo:[1,0,0] neg_hi:[1,0,0]
	v_cvt_pk_bf16_f32 v92, v92, v93
	v_cndmask_b32_e64 v95, 0, 1.0, vcc
	v_cmp_eq_u32_e32 vcc, v193, v199
	s_nop 1
	v_cndmask_b32_e64 v94, 0, 1.0, vcc
	v_pk_fma_f32 v[90:91], v[90:91], v[96:97], v[94:95] op_sel_hi:[0,1,1] neg_lo:[1,0,0] neg_hi:[1,0,0]
	v_cvt_pk_bf16_f32 v93, v90, v91
	ds_write_b64 v186, v[92:93] offset:2720
	ds_read_b32 v90, v187 offset:176
	v_cmp_eq_u32_e32 vcc, v189, v200
	s_nop 1
	v_cndmask_b32_e64 v92, 0, 1.0, vcc
	v_cmp_eq_u32_e32 vcc, v190, v200
	s_nop 1
	v_cndmask_b32_e64 v93, 0, 1.0, vcc
	v_cmp_eq_u32_e32 vcc, v192, v200
	s_waitcnt lgkmcnt(0)
	v_pk_fma_f32 v[86:87], v[90:91], v[86:87], v[92:93] op_sel_hi:[0,1,1] neg_lo:[1,0,0] neg_hi:[1,0,0]
	v_cvt_pk_bf16_f32 v86, v86, v87
	v_cndmask_b32_e64 v93, 0, 1.0, vcc
	v_cmp_eq_u32_e32 vcc, v193, v200
	s_nop 1
	v_cndmask_b32_e64 v92, 0, 1.0, vcc
	v_pk_fma_f32 v[88:89], v[90:91], v[88:89], v[92:93] op_sel_hi:[0,1,1] neg_lo:[1,0,0] neg_hi:[1,0,0]
	v_cvt_pk_bf16_f32 v87, v88, v89
	ds_write_b64 v186, v[86:87] offset:3264
	ds_read_b32 v86, v187 offset:184
	v_cmp_eq_u32_e32 vcc, v189, v201
	s_nop 1
	v_cndmask_b32_e64 v88, 0, 1.0, vcc
	v_cmp_eq_u32_e32 vcc, v190, v201
	s_nop 1
	v_cndmask_b32_e64 v89, 0, 1.0, vcc
	v_cmp_eq_u32_e32 vcc, v192, v201
	s_waitcnt lgkmcnt(0)
	v_pk_fma_f32 v[82:83], v[86:87], v[82:83], v[88:89] op_sel_hi:[0,1,1] neg_lo:[1,0,0] neg_hi:[1,0,0]
	v_cvt_pk_bf16_f32 v82, v82, v83
	v_cndmask_b32_e64 v89, 0, 1.0, vcc
	v_cmp_eq_u32_e32 vcc, v193, v201
	s_nop 1
	v_cndmask_b32_e64 v88, 0, 1.0, vcc
	v_pk_fma_f32 v[84:85], v[86:87], v[84:85], v[88:89] op_sel_hi:[0,1,1] neg_lo:[1,0,0] neg_hi:[1,0,0]
	v_cvt_pk_bf16_f32 v83, v84, v85
	ds_write_b64 v186, v[82:83] offset:3808
	ds_read_b128 v[82:85], v1
	ds_read_b128 v[86:89], v1 offset:64
	ds_read_b128 v[90:93], v1 offset:128
	ds_read_b128 v[94:97], v1 offset:192
	v_lshl_add_u64 v[98:99], v[150:151], 0, s[0:1]
	v_lshl_add_u64 v[192:193], v[164:165], 0, s[0:1]
	v_lshl_add_u64 v[196:197], v[166:167], 0, s[0:1]
	v_lshl_add_u64 v[100:101], v[152:153], 0, s[0:1]
	v_lshl_add_u64 v[106:107], v[156:157], 0, s[0:1]
	v_lshl_add_u64 v[108:109], v[158:159], 0, s[0:1]
	v_lshl_add_u64 v[110:111], v[160:161], 0, s[0:1]
	v_lshl_add_u64 v[112:113], v[162:163], 0, s[0:1]
	global_load_dwordx4 v[118:121], v[98:99], off nt
	global_load_dwordx4 v[134:137], v[100:101], off nt
	global_load_dwordx4 v[150:153], v[106:107], off nt
	global_load_dwordx4 v[156:159], v[108:109], off nt
	global_load_dwordx4 v[160:163], v[110:111], off nt
	global_load_dwordx4 v[164:167], v[112:113], off nt
	s_nop 0
	global_load_dwordx4 v[192:195], v[192:193], off nt
	s_nop 0
	global_load_dwordx4 v[196:199], v[196:197], off nt
	v_mov_b32_e32 v98, v188
	s_waitcnt vmcnt(15)
	s_waitcnt vmcnt(14)
	s_waitcnt vmcnt(13)
	s_waitcnt vmcnt(12)
	s_waitcnt vmcnt(11)
	s_waitcnt vmcnt(10)
	s_waitcnt vmcnt(9)
	s_waitcnt vmcnt(8)
	ds_read_b32 v98, v187
	s_waitcnt lgkmcnt(0)
	v_pk_fma_f32 v[100:101], v[98:99], v[146:147], 0 op_sel_hi:[0,1,0] neg_lo:[1,0,0] neg_hi:[1,0,0]
	v_pk_fma_f32 v[98:99], v[98:99], v[148:149], 0 op_sel_hi:[0,1,0] neg_lo:[1,0,0] neg_hi:[1,0,0]
	v_cvt_pk_bf16_f32 v100, v100, v101
	v_cvt_pk_bf16_f32 v101, v98, v99
	ds_write_b64 v186, v[100:101]
	ds_read_b32 v98, v187 offset:8
	s_waitcnt lgkmcnt(0)
	v_pk_fma_f32 v[100:101], v[98:99], v[142:143], 0 op_sel_hi:[0,1,0] neg_lo:[1,0,0] neg_hi:[1,0,0]
	v_pk_fma_f32 v[98:99], v[98:99], v[144:145], 0 op_sel_hi:[0,1,0] neg_lo:[1,0,0] neg_hi:[1,0,0]
	v_cvt_pk_bf16_f32 v100, v100, v101
	v_cvt_pk_bf16_f32 v101, v98, v99
	ds_write_b64 v186, v[100:101] offset:544
	ds_read_b32 v98, v187 offset:16
	s_waitcnt lgkmcnt(0)
	v_pk_fma_f32 v[100:101], v[98:99], v[138:139], 0 op_sel_hi:[0,1,0] neg_lo:[1,0,0] neg_hi:[1,0,0]
	v_pk_fma_f32 v[98:99], v[98:99], v[140:141], 0 op_sel_hi:[0,1,0] neg_lo:[1,0,0] neg_hi:[1,0,0]
	v_cvt_pk_bf16_f32 v100, v100, v101
	v_cvt_pk_bf16_f32 v101, v98, v99
	ds_write_b64 v186, v[100:101] offset:1088
	ds_read_b32 v98, v187 offset:24
	s_waitcnt lgkmcnt(0)
	v_pk_fma_f32 v[100:101], v[98:99], v[130:131], 0 op_sel_hi:[0,1,0] neg_lo:[1,0,0] neg_hi:[1,0,0]
	v_pk_fma_f32 v[98:99], v[98:99], v[132:133], 0 op_sel_hi:[0,1,0] neg_lo:[1,0,0] neg_hi:[1,0,0]
	v_cvt_pk_bf16_f32 v100, v100, v101
	v_cvt_pk_bf16_f32 v101, v98, v99
	ds_write_b64 v186, v[100:101] offset:1632
	ds_read_b32 v98, v187 offset:32
	s_waitcnt lgkmcnt(0)
	v_pk_fma_f32 v[100:101], v[98:99], v[126:127], 0 op_sel_hi:[0,1,0] neg_lo:[1,0,0] neg_hi:[1,0,0]
	v_pk_fma_f32 v[98:99], v[98:99], v[128:129], 0 op_sel_hi:[0,1,0] neg_lo:[1,0,0] neg_hi:[1,0,0]
	v_cvt_pk_bf16_f32 v100, v100, v101
	v_cvt_pk_bf16_f32 v101, v98, v99
	ds_write_b64 v186, v[100:101] offset:2176
	ds_read_b32 v98, v187 offset:40
	s_waitcnt lgkmcnt(0)
	v_pk_fma_f32 v[100:101], v[98:99], v[122:123], 0 op_sel_hi:[0,1,0] neg_lo:[1,0,0] neg_hi:[1,0,0]
	v_pk_fma_f32 v[98:99], v[98:99], v[124:125], 0 op_sel_hi:[0,1,0] neg_lo:[1,0,0] neg_hi:[1,0,0]
	v_cvt_pk_bf16_f32 v100, v100, v101
	v_cvt_pk_bf16_f32 v101, v98, v99
	ds_write_b64 v186, v[100:101] offset:2720
	ds_read_b32 v98, v187 offset:48
	s_waitcnt lgkmcnt(0)
	v_pk_fma_f32 v[100:101], v[98:99], v[114:115], 0 op_sel_hi:[0,1,0] neg_lo:[1,0,0] neg_hi:[1,0,0]
	v_pk_fma_f32 v[98:99], v[98:99], v[116:117], 0 op_sel_hi:[0,1,0] neg_lo:[1,0,0] neg_hi:[1,0,0]
	v_cvt_pk_bf16_f32 v100, v100, v101
	v_cvt_pk_bf16_f32 v101, v98, v99
	ds_write_b64 v186, v[100:101] offset:3264
	ds_read_b32 v98, v187 offset:56
	s_waitcnt lgkmcnt(0)
	v_pk_fma_f32 v[100:101], v[98:99], v[102:103], 0 op_sel_hi:[0,1,0] neg_lo:[1,0,0] neg_hi:[1,0,0]
	v_pk_fma_f32 v[98:99], v[98:99], v[104:105], 0 op_sel_hi:[0,1,0] neg_lo:[1,0,0] neg_hi:[1,0,0]
	v_cvt_pk_bf16_f32 v100, v100, v101
	v_cvt_pk_bf16_f32 v101, v98, v99
	ds_write_b64 v186, v[100:101] offset:3808
	ds_read_b128 v[98:101], v1
	ds_read_b128 v[102:105], v1 offset:64
	ds_read_b128 v[106:109], v1 offset:128
	ds_read_b128 v[110:113], v1 offset:192
	v_lshl_add_u64 v[114:115], v[168:169], 0, s[0:1]
	v_lshl_add_u64 v[126:127], v[176:177], 0, s[0:1]
	v_lshl_add_u64 v[176:177], v[180:181], 0, s[0:1]
	v_lshl_add_u64 v[180:181], v[182:183], 0, s[0:1]
	v_lshl_add_u64 v[116:117], v[170:171], 0, s[0:1]
	v_lshl_add_u64 v[122:123], v[172:173], 0, s[0:1]
	v_lshl_add_u64 v[124:125], v[174:175], 0, s[0:1]
	v_lshl_add_u64 v[128:129], v[178:179], 0, s[0:1]
	global_load_dwordx4 v[130:133], v[114:115], off nt
	global_load_dwordx4 v[138:141], v[116:117], off nt
	global_load_dwordx4 v[142:145], v[122:123], off nt
	global_load_dwordx4 v[146:149], v[124:125], off nt
	global_load_dwordx4 v[168:171], v[126:127], off nt
	global_load_dwordx4 v[172:175], v[128:129], off nt
	s_nop 0
	global_load_dwordx4 v[176:179], v[176:177], off nt
	s_nop 0
	global_load_dwordx4 v[180:183], v[180:181], off nt
	v_mov_b32_e32 v114, v188
	s_waitcnt vmcnt(15)
	s_waitcnt vmcnt(14)
	s_waitcnt vmcnt(13)
	s_waitcnt vmcnt(12)
	s_waitcnt vmcnt(11)
	s_waitcnt vmcnt(10)
	s_waitcnt vmcnt(9)
	s_waitcnt vmcnt(8)
	ds_read_b32 v114, v187 offset:64
	s_waitcnt lgkmcnt(0)
	v_pk_fma_f32 v[116:117], v[114:115], v[118:119], 0 op_sel_hi:[0,1,0] neg_lo:[1,0,0] neg_hi:[1,0,0]
	v_pk_fma_f32 v[114:115], v[114:115], v[120:121], 0 op_sel_hi:[0,1,0] neg_lo:[1,0,0] neg_hi:[1,0,0]
	v_cvt_pk_bf16_f32 v116, v116, v117
	v_cvt_pk_bf16_f32 v117, v114, v115
	ds_write_b64 v186, v[116:117]
	ds_read_b32 v114, v187 offset:72
	s_waitcnt lgkmcnt(0)
	v_pk_fma_f32 v[116:117], v[114:115], v[134:135], 0 op_sel_hi:[0,1,0] neg_lo:[1,0,0] neg_hi:[1,0,0]
	v_pk_fma_f32 v[114:115], v[114:115], v[136:137], 0 op_sel_hi:[0,1,0] neg_lo:[1,0,0] neg_hi:[1,0,0]
	v_cvt_pk_bf16_f32 v116, v116, v117
	v_cvt_pk_bf16_f32 v117, v114, v115
	ds_write_b64 v186, v[116:117] offset:544
	ds_read_b32 v114, v187 offset:80
	s_waitcnt lgkmcnt(0)
	v_pk_fma_f32 v[116:117], v[114:115], v[150:151], 0 op_sel_hi:[0,1,0] neg_lo:[1,0,0] neg_hi:[1,0,0]
	v_pk_fma_f32 v[114:115], v[114:115], v[152:153], 0 op_sel_hi:[0,1,0] neg_lo:[1,0,0] neg_hi:[1,0,0]
	v_cvt_pk_bf16_f32 v116, v116, v117
	v_cvt_pk_bf16_f32 v117, v114, v115
	ds_write_b64 v186, v[116:117] offset:1088
	ds_read_b32 v114, v187 offset:88
	s_waitcnt lgkmcnt(0)
	v_pk_fma_f32 v[116:117], v[114:115], v[156:157], 0 op_sel_hi:[0,1,0] neg_lo:[1,0,0] neg_hi:[1,0,0]
	v_pk_fma_f32 v[114:115], v[114:115], v[158:159], 0 op_sel_hi:[0,1,0] neg_lo:[1,0,0] neg_hi:[1,0,0]
	v_cvt_pk_bf16_f32 v116, v116, v117
	v_cvt_pk_bf16_f32 v117, v114, v115
	ds_write_b64 v186, v[116:117] offset:1632
	ds_read_b32 v114, v187 offset:96
	s_waitcnt lgkmcnt(0)
	v_pk_fma_f32 v[116:117], v[114:115], v[160:161], 0 op_sel_hi:[0,1,0] neg_lo:[1,0,0] neg_hi:[1,0,0]
	v_pk_fma_f32 v[114:115], v[114:115], v[162:163], 0 op_sel_hi:[0,1,0] neg_lo:[1,0,0] neg_hi:[1,0,0]
	v_cvt_pk_bf16_f32 v116, v116, v117
	v_cvt_pk_bf16_f32 v117, v114, v115
	ds_write_b64 v186, v[116:117] offset:2176
	ds_read_b32 v114, v187 offset:104
	s_waitcnt lgkmcnt(0)
	v_pk_fma_f32 v[116:117], v[114:115], v[164:165], 0 op_sel_hi:[0,1,0] neg_lo:[1,0,0] neg_hi:[1,0,0]
	v_pk_fma_f32 v[114:115], v[114:115], v[166:167], 0 op_sel_hi:[0,1,0] neg_lo:[1,0,0] neg_hi:[1,0,0]
	v_cvt_pk_bf16_f32 v116, v116, v117
	v_cvt_pk_bf16_f32 v117, v114, v115
	ds_write_b64 v186, v[116:117] offset:2720
	ds_read_b32 v114, v187 offset:112
	s_waitcnt lgkmcnt(0)
	v_pk_fma_f32 v[116:117], v[114:115], v[192:193], 0 op_sel_hi:[0,1,0] neg_lo:[1,0,0] neg_hi:[1,0,0]
	v_pk_fma_f32 v[114:115], v[114:115], v[194:195], 0 op_sel_hi:[0,1,0] neg_lo:[1,0,0] neg_hi:[1,0,0]
	v_cvt_pk_bf16_f32 v116, v116, v117
	v_cvt_pk_bf16_f32 v117, v114, v115
	ds_write_b64 v186, v[116:117] offset:3264
	ds_read_b32 v114, v187 offset:120
	s_waitcnt lgkmcnt(0)
	v_pk_fma_f32 v[116:117], v[114:115], v[196:197], 0 op_sel_hi:[0,1,0] neg_lo:[1,0,0] neg_hi:[1,0,0]
	v_pk_fma_f32 v[114:115], v[114:115], v[198:199], 0 op_sel_hi:[0,1,0] neg_lo:[1,0,0] neg_hi:[1,0,0]
	v_cvt_pk_bf16_f32 v116, v116, v117
	v_cvt_pk_bf16_f32 v117, v114, v115
	ds_write_b64 v186, v[116:117] offset:3808
	ds_read_b128 v[114:117], v1
	ds_read_b128 v[118:121], v1 offset:64
	ds_read_b128 v[122:125], v1 offset:128
	ds_read_b128 v[126:129], v1 offset:192
	s_waitcnt vmcnt(7)
	s_waitcnt vmcnt(6)
	s_waitcnt vmcnt(5)
	s_waitcnt vmcnt(4)
	s_waitcnt vmcnt(3)
	s_waitcnt vmcnt(2)
	s_waitcnt vmcnt(1)
	s_waitcnt vmcnt(0)
	ds_read_b32 v134, v187 offset:128
	s_waitcnt lgkmcnt(0)
	v_pk_fma_f32 v[130:131], v[134:135], v[130:131], 0 op_sel_hi:[0,1,0] neg_lo:[1,0,0] neg_hi:[1,0,0]
	v_pk_fma_f32 v[132:133], v[134:135], v[132:133], 0 op_sel_hi:[0,1,0] neg_lo:[1,0,0] neg_hi:[1,0,0]
	v_cvt_pk_bf16_f32 v130, v130, v131
	v_cvt_pk_bf16_f32 v131, v132, v133
	ds_write_b64 v186, v[130:131]
	ds_read_b32 v130, v187 offset:136
	s_waitcnt lgkmcnt(0)
	v_pk_fma_f32 v[132:133], v[130:131], v[138:139], 0 op_sel_hi:[0,1,0] neg_lo:[1,0,0] neg_hi:[1,0,0]
	v_pk_fma_f32 v[130:131], v[130:131], v[140:141], 0 op_sel_hi:[0,1,0] neg_lo:[1,0,0] neg_hi:[1,0,0]
	v_cvt_pk_bf16_f32 v132, v132, v133
	v_cvt_pk_bf16_f32 v133, v130, v131
	ds_write_b64 v186, v[132:133] offset:544
	ds_read_b32 v130, v187 offset:144
	s_waitcnt lgkmcnt(0)
	v_pk_fma_f32 v[132:133], v[130:131], v[142:143], 0 op_sel_hi:[0,1,0] neg_lo:[1,0,0] neg_hi:[1,0,0]
	v_pk_fma_f32 v[130:131], v[130:131], v[144:145], 0 op_sel_hi:[0,1,0] neg_lo:[1,0,0] neg_hi:[1,0,0]
	v_cvt_pk_bf16_f32 v132, v132, v133
	v_cvt_pk_bf16_f32 v133, v130, v131
	ds_write_b64 v186, v[132:133] offset:1088
	ds_read_b32 v130, v187 offset:152
	s_waitcnt lgkmcnt(0)
	v_pk_fma_f32 v[132:133], v[130:131], v[146:147], 0 op_sel_hi:[0,1,0] neg_lo:[1,0,0] neg_hi:[1,0,0]
	v_pk_fma_f32 v[130:131], v[130:131], v[148:149], 0 op_sel_hi:[0,1,0] neg_lo:[1,0,0] neg_hi:[1,0,0]
	v_cvt_pk_bf16_f32 v132, v132, v133
	v_cvt_pk_bf16_f32 v133, v130, v131
	ds_write_b64 v186, v[132:133] offset:1632
	ds_read_b32 v130, v187 offset:160
	s_waitcnt lgkmcnt(0)
	v_pk_fma_f32 v[132:133], v[130:131], v[168:169], 0 op_sel_hi:[0,1,0] neg_lo:[1,0,0] neg_hi:[1,0,0]
	v_pk_fma_f32 v[130:131], v[130:131], v[170:171], 0 op_sel_hi:[0,1,0] neg_lo:[1,0,0] neg_hi:[1,0,0]
	v_cvt_pk_bf16_f32 v132, v132, v133
	v_cvt_pk_bf16_f32 v133, v130, v131
	ds_write_b64 v186, v[132:133] offset:2176
	ds_read_b32 v130, v187 offset:168
	s_waitcnt lgkmcnt(0)
	v_pk_fma_f32 v[132:133], v[130:131], v[172:173], 0 op_sel_hi:[0,1,0] neg_lo:[1,0,0] neg_hi:[1,0,0]
	v_pk_fma_f32 v[130:131], v[130:131], v[174:175], 0 op_sel_hi:[0,1,0] neg_lo:[1,0,0] neg_hi:[1,0,0]
	v_cvt_pk_bf16_f32 v132, v132, v133
	v_cvt_pk_bf16_f32 v133, v130, v131
	ds_write_b64 v186, v[132:133] offset:2720
	ds_read_b32 v130, v187 offset:176
	s_waitcnt lgkmcnt(0)
	v_pk_fma_f32 v[132:133], v[130:131], v[176:177], 0 op_sel_hi:[0,1,0] neg_lo:[1,0,0] neg_hi:[1,0,0]
	v_pk_fma_f32 v[130:131], v[130:131], v[178:179], 0 op_sel_hi:[0,1,0] neg_lo:[1,0,0] neg_hi:[1,0,0]
	v_cvt_pk_bf16_f32 v132, v132, v133
	v_cvt_pk_bf16_f32 v133, v130, v131
	ds_write_b64 v186, v[132:133] offset:3264
	ds_read_b32 v130, v187 offset:184
	s_waitcnt lgkmcnt(0)
	v_pk_fma_f32 v[132:133], v[130:131], v[180:181], 0 op_sel_hi:[0,1,0] neg_lo:[1,0,0] neg_hi:[1,0,0]
	v_pk_fma_f32 v[130:131], v[130:131], v[182:183], 0 op_sel_hi:[0,1,0] neg_lo:[1,0,0] neg_hi:[1,0,0]
	v_cvt_pk_bf16_f32 v132, v132, v133
	v_cvt_pk_bf16_f32 v133, v130, v131
	ds_write_b64 v186, v[132:133] offset:3808
	ds_read_b128 v[130:133], v1
	ds_read_b128 v[134:137], v1 offset:64
	ds_read_b128 v[138:141], v1 offset:128
	ds_read_b128 v[142:145], v1 offset:192
	s_ashr_i32 s7, s6, 31
	s_lshl_b64 s[0:1], s[6:7], 2
	s_add_u32 s0, s4, s0
	s_addc_u32 s1, s5, s1
	v_lshlrev_b32_e32 v1, 4, v0
	s_add_i32 s20, s34, 1
	s_add_i32 s34, s34, -1
	v_or_b32_e32 v153, s10, v206
	s_xor_b32 s26, s3, 2
	s_lshl_b64 s[10:11], s[10:11], 3
	s_and_b32 s20, s20, 3
	s_and_b32 s27, s34, 3
	s_add_u32 s10, s14, s10
	s_addc_u32 s11, s15, s11
	s_lshl_b32 s42, s35, 2
	s_add_i32 s41, s42, 0x26a20
	s_add_i32 s42, s42, 0x26a00
	v_lshlrev_b32_e32 v190, 3, v206
	s_cmp_eq_u32 s35, 3
	v_lshlrev_b32_e32 v150, 3, v0
	v_and_b32_e32 v151, 1, v0
	v_lshl_add_u64 v[0:1], v[154:155], 3, s[14:15]
	v_lshl_add_u64 v[192:193], s[10:11], 0, v[190:191]
	s_cselect_b64 s[10:11], -1, 0
	s_lshl_b32 s14, s3, 2
	s_add_u32 s24, s16, s14
	v_or_b32_e32 v155, 0x20000, v150
	v_add_u32_e32 v156, 0x20880, v150
	v_lshlrev_b32_e32 v150, 1, v153
	s_addc_u32 s25, s17, 0
	s_lshl_b32 s43, s3, 9
	v_lshl_add_u32 v212, s26, 9, v150
	s_lshl_b32 s15, s26, 8
	s_add_i32 s26, s43, 0x200
	v_mov_b32_e32 v152, 0x880
	v_cmp_lt_u32_e64 s[0:1], 15, v206
	v_cmp_eq_u32_e32 vcc, 1, v151
	s_and_b32 s45, s26, 0x600
	s_add_i32 s26, s43, 0x500
	v_cndmask_b32_e32 v211, 0, v152, vcc
	s_and_b32 s56, s26, 0x700
	s_add_i32 s26, s43, 0x540
	v_lshl_add_u32 v213, s20, 9, v150
	v_lshl_add_u32 v214, s27, 9, v150
	s_and_b32 s57, s26, 0x740
	s_add_i32 s26, s43, 0x580
	s_and_b32 s58, s26, 0x780
	s_add_i32 s26, s43, 0x5c0
	s_and_b32 s59, s26, 0x7c0
	s_add_i32 s26, s43, 0x600
	s_and_b32 s60, s26, 0x600
	s_add_i32 s26, s43, 0x640
	s_and_b32 s61, s26, 0x640
	s_add_i32 s26, s43, 0x680
	s_and_b32 s62, s26, 0x680
	s_add_i32 s26, s43, 0x6c0
	s_and_b32 s63, s26, 0x6c0
	s_add_i32 s26, s43, 0x700
	s_and_b32 s64, s26, 0x700
	s_add_i32 s26, s43, 0x740
	s_and_b32 s65, s26, 0x740
	s_add_i32 s26, s43, 0x780
	s_lshl_b32 s14, s27, 8
	s_lshl_b32 s20, s20, 8
	s_add_i32 s27, s43, 0x240
	s_add_i32 s28, s43, 0x280
	s_add_i32 s29, s43, 0x2c0
	s_add_i32 s30, s43, 0x300
	s_add_i32 s31, s43, 0x340
	s_add_i32 s34, s43, 0x380
	s_add_i32 s35, s43, 0x3c0
	s_add_i32 s36, s43, 0x440
	s_add_i32 s37, s43, 0x480
	s_add_i32 s38, s43, 0x4c0
	s_and_b32 s66, s26, 0x780
	s_add_i32 s26, s43, 0x7c0
	s_mul_hi_i32 s23, s18, 0x65
	s_mul_i32 s22, s18, 0x65
	v_cmp_eq_u32_e64 s[4:5], 1, v185
	v_cmp_eq_u32_e64 s[6:7], 2, v185
	v_cmp_eq_u32_e64 s[8:9], 63, v206
	s_xor_b32 s44, s43, 0x400
	s_and_b32 s46, s27, 0x640
	s_and_b32 s47, s28, 0x680
	s_waitcnt lgkmcnt(0)
	v_mov_b32_e32 v146, 0x20000
	s_and_b32 s48, s29, 0x6c0
	s_and_b32 s49, s30, 0x700
	s_and_b32 s50, s31, 0x740
	s_and_b32 s51, s34, 0x780
	s_and_b32 s52, s35, 0x7c0
	s_and_b32 s53, s36, 0x640
	s_and_b32 s54, s37, 0x680
	s_and_b32 s55, s38, 0x6c0
	s_and_b32 s67, s26, 0x7c0
	s_and_b64 s[26:27], s[10:11], s[12:13]
	v_lshl_add_u32 v215, v154, 1, v146
	v_mov_b32_e32 v216, 1
	s_lshl_b32 s28, s14, 3
	s_lshl_b32 s30, s15, 3
	s_lshl_b32 s34, s20, 3
	s_movk_i32 s68, 0x7fff
	s_mov_b32 s69, 0
	v_and_b32_e32 v220, 24, v206
	v_lshlrev_b32_e32 v220, 2, v220
	v_and_b32_e32 v221, 2, v206
	v_lshl_or_b32 v220, v221, 3, v220
	v_and_b32_e32 v221, 32, v206
	v_lshrrev_b32_e32 v221, 2, v221
	v_or_b32_e32 v220, v220, v221
	v_and_b32_e32 v221, 4, v206
	v_or_b32_e32 v220, v220, v221
	v_and_b32_e32 v221, 1, v206
	v_lshl_or_b32 v220, v221, 1, v220
	v_mov_b32_e32 v220, v254
	s_lshr_b32 s76, s19, 8
	s_add_i32 s76, s76, 0x20000
	v_add_u32_e32 v220, s76, v220
	v_add_u32_e32 v225, s45, v220
	v_add_u32_e32 v226, s44, v220
	v_add_u32_e32 v227, s60, v220
	v_add_u32_e32 v228, s43, v220
	v_and_b32_e32 v221, 1, v206
	v_mul_u32_u24_e32 v221, 0x880, v221
	v_lshrrev_b32_e32 v220, 4, v206
	v_lshl_add_u32 v221, v220, 5, v221
	v_and_b32_e32 v220, 2, v206
	v_lshl_add_u32 v221, v220, 3, v221
	v_add_u32_e32 v222, 0x20000, v221
	v_cmp_ne_u32_e32 vcc, 0, v220
	v_mov_b32_e32 v220, 0x44444444
	v_mov_b32_e32 v221, 0xeeeeeeee
	s_nop 1
	v_cndmask_b32_e32 v223, v220, v221, vcc
	v_cmp_lt_u32_e64 s[74:75], 47, v206
	v_mov_b32_e32 v224, v184
	s_lshr_b32 s78, s19, 15
	s_lshl_b32 s79, s78, 11
	v_add_u32_e32 v255, s79, v224
	ds_read_b128 v[166:169], v224 offset:0
	ds_read_b128 v[170:173], v224 offset:1024
	ds_read_b128 v[174:177], v224 offset:2048
	ds_read_b128 v[178:181], v224 offset:3072
	ds_read_b128 v[182:185], v224 offset:4096
	ds_read_b128 v[186:189], v224 offset:5120
	s_mov_b32 s20, 0

.Lj_nopoll0:
	s_waitcnt lgkmcnt(4)
	v_smfmac_f32_16x16x64_bf16 v[146:149], v[194:197], v[10:17], v223
	v_smfmac_f32_16x16x64_bf16 v[154:157], v[194:197], v[26:33], v223
	v_smfmac_f32_16x16x64_bf16 v[158:161], v[194:197], v[42:49], v223
	v_smfmac_f32_16x16x64_bf16 v[162:165], v[194:197], v[174:181], v223
	v_or3_b32 v231, v194, v195, v231
	v_or3_b32 v231, v196, v197, v231
	ds_read_b128 v[174:177], v255 offset:8192
	ds_read_b128 v[178:181], v255 offset:9216
	s_waitcnt lgkmcnt(5)
	v_smfmac_f32_16x16x64_bf16 v[146:149], v[198:201], v[50:57], v223
	v_smfmac_f32_16x16x64_bf16 v[154:157], v[198:201], v[66:73], v223
	v_smfmac_f32_16x16x64_bf16 v[158:161], v[198:201], v[82:89], v223
	v_smfmac_f32_16x16x64_bf16 v[162:165], v[198:201], v[182:189], v223
	v_or3_b32 v231, v198, v199, v231
	v_or3_b32 v231, v200, v201, v231
	ds_read_b128 v[182:185], v255 offset:16384
	ds_read_b128 v[186:189], v255 offset:17408
	s_waitcnt lgkmcnt(6)
	v_smfmac_f32_16x16x64_bf16 v[146:149], v[232:235], v[58:65], v223
	v_smfmac_f32_16x16x64_bf16 v[154:157], v[232:235], v[74:81], v223
	v_smfmac_f32_16x16x64_bf16 v[158:161], v[232:235], v[90:97], v223
	s_waitcnt lgkmcnt(4)
	v_smfmac_f32_16x16x64_bf16 v[162:165], v[232:235], v[166:173], v223
	v_or3_b32 v231, v232, v233, v231
	v_or3_b32 v231, v234, v235, v231
	ds_read_b128 v[166:169], v255 offset:24576
	ds_read_b128 v[170:173], v255 offset:25600
	s_cmp_eq_u32 s20, 0
	s_cbranch_scc1 .Lj_gdone
	s_mov_b32 s29, 0

.Lj_gdone:
	v_add_u32_e32 v240, s45, v229
	v_add_u32_e32 v241, s44, v229
	v_add_u32_e32 v242, s60, v229
	s_cmp_eq_u32 s20, 0
	s_cselect_b64 s[36:37], -1, 0
	s_add_i32 s29, s20, 1
	s_and_b32 s14, s29, 1
	s_lshl_b32 s10, s14, 13
	s_mov_b32 s11, 0
	v_lshl_add_u64 v[250:251], v[0:1], 0, s[10:11]
	s_mul_i32 s15, s14, 0x1100
	v_add_u32_e32 v243, s15, v228
	v_mov_b32_e32 v253, s29
	s_cmp_eq_u32 s78, 1
	s_cbranch_scc1 .Lj_B1
	s_cmp_eq_u32 s78, 2
	s_cbranch_scc1 .Lj_B2
	s_cmp_eq_u32 s78, 3
	s_cbranch_scc1 .Lj_B3
.Lj_B0:
	ds_read_b128 v[150:153], v240 offset:0
	ds_read_b128 v[194:197], v241 offset:0
	ds_read_b128 v[198:201], v242 offset:0
	s_waitcnt lgkmcnt(2)
	v_smfmac_f32_16x16x64_bf16 v[146:149], v[150:153], v[98:105], v223
	v_smfmac_f32_16x16x64_bf16 v[154:157], v[150:153], v[114:121], v223
	v_smfmac_f32_16x16x64_bf16 v[158:161], v[150:153], v[130:137], v223
	v_smfmac_f32_16x16x64_bf16 v[162:165], v[150:153], v[174:181], v223
	v_or3_b32 v231, v150, v151, v231
	v_or3_b32 v231, v152, v153, v231
	ds_read_b128 v[174:177], v224 offset:10240
	ds_read_b128 v[178:181], v224 offset:11264
	s_barrier
	ds_read_b128 v[232:235], v240 offset:128
	ds_read_b128 v[150:153], v240 offset:256
	s_waitcnt lgkmcnt(5)
	v_smfmac_f32_16x16x64_bf16 v[146:149], v[194:197], a[48:55], v223
	v_smfmac_f32_16x16x64_bf16 v[154:157], v[194:197], a[64:71], v223
	v_smfmac_f32_16x16x64_bf16 v[158:161], v[194:197], a[80:87], v223
	v_smfmac_f32_16x16x64_bf16 v[162:165], v[194:197], v[182:189], v223
	v_or3_b32 v231, v194, v195, v231
	v_or3_b32 v231, v196, v197, v231
	ds_read_b128 v[182:185], v224 offset:12288
	ds_read_b128 v[186:189], v224 offset:13312
	ds_read_b128 v[194:197], v240 offset:384
	s_waitcnt lgkmcnt(7)
	v_smfmac_f32_16x16x64_bf16 v[146:149], v[198:201], a[144:151], v223
	v_smfmac_f32_16x16x64_bf16 v[154:157], v[198:201], a[160:167], v223
	v_smfmac_f32_16x16x64_bf16 v[158:161], v[198:201], a[176:183], v223
	v_smfmac_f32_16x16x64_bf16 v[162:165], v[198:201], v[166:173], v223
	v_or3_b32 v231, v198, v199, v231
	v_or3_b32 v231, v200, v201, v231
	ds_read_b128 v[166:169], v224 offset:14336
	ds_read_b128 v[170:173], v224 offset:15360
	ds_read_b128 v[198:201], v241 offset:128
	s_waitcnt lgkmcnt(7)
	v_smfmac_f32_16x16x64_bf16 v[146:149], v[232:235], v[106:113], v223
	v_smfmac_f32_16x16x64_bf16 v[154:157], v[232:235], v[122:129], v223
	v_smfmac_f32_16x16x64_bf16 v[158:161], v[232:235], v[138:145], v223
	v_smfmac_f32_16x16x64_bf16 v[162:165], v[232:235], v[174:181], v223
	v_or3_b32 v231, v232, v233, v231
	v_or3_b32 v231, v234, v235, v231
	ds_read_b128 v[174:177], v224 offset:18432
	ds_read_b128 v[178:181], v224 offset:19456
	ds_read_b128 v[232:235], v241 offset:256
	s_waitcnt lgkmcnt(9)
	v_smfmac_f32_16x16x64_bf16 v[146:149], v[150:153], a[0:7], v223
	v_smfmac_f32_16x16x64_bf16 v[154:157], v[150:153], a[16:23], v223
	v_smfmac_f32_16x16x64_bf16 v[158:161], v[150:153], a[32:39], v223
	s_waitcnt lgkmcnt(7)
	v_smfmac_f32_16x16x64_bf16 v[162:165], v[150:153], v[182:189], v223
	v_or3_b32 v231, v150, v151, v231
	v_or3_b32 v231, v152, v153, v231
	ds_read_b128 v[182:185], v224 offset:20480
	ds_read_b128 v[186:189], v224 offset:21504
	ds_read_b128 v[150:153], v241 offset:384
	s_waitcnt lgkmcnt(9)
	v_smfmac_f32_16x16x64_bf16 v[146:149], v[194:197], a[8:15], v223
	v_smfmac_f32_16x16x64_bf16 v[154:157], v[194:197], a[24:31], v223
	v_smfmac_f32_16x16x64_bf16 v[158:161], v[194:197], a[40:47], v223
	s_waitcnt lgkmcnt(7)
	v_smfmac_f32_16x16x64_bf16 v[162:165], v[194:197], v[166:173], v223
	v_or3_b32 v231, v194, v195, v231
	v_or3_b32 v231, v196, v197, v231
	ds_read_b128 v[166:169], v224 offset:22528
	ds_read_b128 v[170:173], v224 offset:23552
	ds_read_b128 v[194:197], v242 offset:128
	s_waitcnt lgkmcnt(9)
	v_smfmac_f32_16x16x64_bf16 v[146:149], v[198:201], a[56:63], v223
	v_smfmac_f32_16x16x64_bf16 v[154:157], v[198:201], a[72:79], v223
	v_smfmac_f32_16x16x64_bf16 v[158:161], v[198:201], a[88:95], v223
	s_waitcnt lgkmcnt(7)
	v_smfmac_f32_16x16x64_bf16 v[162:165], v[198:201], v[174:181], v223
	v_or3_b32 v231, v198, v199, v231
	v_or3_b32 v231, v200, v201, v231
	ds_read_b128 v[174:177], v224 offset:26624
	ds_read_b128 v[178:181], v224 offset:27648
	ds_read_b128 v[198:201], v242 offset:256
	s_waitcnt lgkmcnt(9)
	v_smfmac_f32_16x16x64_bf16 v[146:149], v[232:235], a[96:103], v223
	v_smfmac_f32_16x16x64_bf16 v[154:157], v[232:235], a[112:119], v223
	v_smfmac_f32_16x16x64_bf16 v[158:161], v[232:235], a[128:135], v223
	s_waitcnt lgkmcnt(7)
	v_smfmac_f32_16x16x64_bf16 v[162:165], v[232:235], v[182:189], v223
	v_or3_b32 v231, v232, v233, v231
	v_or3_b32 v231, v234, v235, v231
	ds_read_b128 v[182:185], v224 offset:28672
	ds_read_b128 v[186:189], v224 offset:29696
	ds_read_b128 v[232:235], v242 offset:384
	s_waitcnt lgkmcnt(9)
	v_smfmac_f32_16x16x64_bf16 v[146:149], v[150:153], a[104:111], v223
	v_smfmac_f32_16x16x64_bf16 v[154:157], v[150:153], a[120:127], v223
	v_smfmac_f32_16x16x64_bf16 v[158:161], v[150:153], a[136:143], v223
	s_waitcnt lgkmcnt(7)
	v_smfmac_f32_16x16x64_bf16 v[162:165], v[150:153], v[166:173], v223
	v_or3_b32 v231, v150, v151, v231
	v_or3_b32 v231, v152, v153, v231
	ds_read_b128 v[166:169], v224 offset:30720
	ds_read_b128 v[170:173], v224 offset:31744
	s_waitcnt lgkmcnt(8)
	v_smfmac_f32_16x16x64_bf16 v[146:149], v[194:197], a[152:159], v223
	v_smfmac_f32_16x16x64_bf16 v[154:157], v[194:197], a[168:175], v223
	v_smfmac_f32_16x16x64_bf16 v[158:161], v[194:197], a[184:191], v223
	s_waitcnt lgkmcnt(6)
	v_smfmac_f32_16x16x64_bf16 v[162:165], v[194:197], v[174:181], v223
	v_or3_b32 v231, v194, v195, v231
	v_or3_b32 v231, v196, v197, v231
	ds_read_b128 v[174:177], v224 offset:2048
	ds_read_b128 v[178:181], v224 offset:3072
	s_waitcnt lgkmcnt(7)
	v_smfmac_f32_16x16x64_bf16 v[146:149], v[198:201], a[192:199], v223
	v_smfmac_f32_16x16x64_bf16 v[154:157], v[198:201], a[208:215], v223
	v_smfmac_f32_16x16x64_bf16 v[158:161], v[198:201], a[224:231], v223
	s_waitcnt lgkmcnt(5)
	v_smfmac_f32_16x16x64_bf16 v[162:165], v[198:201], v[182:189], v223
	v_or3_b32 v231, v198, v199, v231
	v_or3_b32 v231, v200, v201, v231
	ds_read_b128 v[182:185], v224 offset:4096
	ds_read_b128 v[186:189], v224 offset:5120
	s_waitcnt lgkmcnt(6)
	v_smfmac_f32_16x16x64_bf16 v[146:149], v[232:235], a[200:207], v223
	v_smfmac_f32_16x16x64_bf16 v[154:157], v[232:235], a[216:223], v223
	v_smfmac_f32_16x16x64_bf16 v[158:161], v[232:235], a[232:239], v223
	s_waitcnt lgkmcnt(4)
	v_smfmac_f32_16x16x64_bf16 v[162:165], v[232:235], v[166:173], v223
	v_or3_b32 v231, v232, v233, v231
	v_or3_b32 v231, v234, v235, v231
	ds_read_b128 v[166:169], v224 offset:0
	ds_read_b128 v[170:173], v224 offset:1024
	s_branch .Lj_Bend
.Lj_B1:
	ds_read_b128 v[150:153], v240 offset:128
	ds_read_b128 v[194:197], v241 offset:128
	ds_read_b128 v[198:201], v242 offset:128
	s_waitcnt lgkmcnt(2)
	v_smfmac_f32_16x16x64_bf16 v[146:149], v[150:153], v[106:113], v223
	v_smfmac_f32_16x16x64_bf16 v[154:157], v[150:153], v[122:129], v223
	v_smfmac_f32_16x16x64_bf16 v[158:161], v[150:153], v[138:145], v223
	v_smfmac_f32_16x16x64_bf16 v[162:165], v[150:153], v[174:181], v223
	v_or3_b32 v231, v150, v151, v231
	v_or3_b32 v231, v152, v153, v231
	ds_read_b128 v[174:177], v224 offset:8192
	ds_read_b128 v[178:181], v224 offset:9216
	s_barrier
	ds_read_b128 v[232:235], v240 offset:0
	ds_read_b128 v[150:153], v240 offset:256
	s_waitcnt lgkmcnt(5)
	v_smfmac_f32_16x16x64_bf16 v[146:149], v[194:197], a[56:63], v223
	v_smfmac_f32_16x16x64_bf16 v[154:157], v[194:197], a[72:79], v223
	v_smfmac_f32_16x16x64_bf16 v[158:161], v[194:197], a[88:95], v223
	v_smfmac_f32_16x16x64_bf16 v[162:165], v[194:197], v[182:189], v223
	v_or3_b32 v231, v194, v195, v231
	v_or3_b32 v231, v196, v197, v231
	ds_read_b128 v[182:185], v224 offset:12288
	ds_read_b128 v[186:189], v224 offset:13312
	ds_read_b128 v[194:197], v240 offset:384
	s_waitcnt lgkmcnt(7)
	v_smfmac_f32_16x16x64_bf16 v[146:149], v[198:201], a[152:159], v223
	v_smfmac_f32_16x16x64_bf16 v[154:157], v[198:201], a[168:175], v223
	v_smfmac_f32_16x16x64_bf16 v[158:161], v[198:201], a[184:191], v223
	v_smfmac_f32_16x16x64_bf16 v[162:165], v[198:201], v[166:173], v223
	v_or3_b32 v231, v198, v199, v231
	v_or3_b32 v231, v200, v201, v231
	ds_read_b128 v[166:169], v224 offset:14336
	ds_read_b128 v[170:173], v224 offset:15360
	ds_read_b128 v[198:201], v241 offset:0
	s_waitcnt lgkmcnt(7)
	v_smfmac_f32_16x16x64_bf16 v[146:149], v[232:235], v[98:105], v223
	v_smfmac_f32_16x16x64_bf16 v[154:157], v[232:235], v[114:121], v223
	v_smfmac_f32_16x16x64_bf16 v[158:161], v[232:235], v[130:137], v223
	v_smfmac_f32_16x16x64_bf16 v[162:165], v[232:235], v[174:181], v223
	v_or3_b32 v231, v232, v233, v231
	v_or3_b32 v231, v234, v235, v231
	ds_read_b128 v[174:177], v224 offset:16384
	ds_read_b128 v[178:181], v224 offset:17408
	ds_read_b128 v[232:235], v241 offset:256
	s_waitcnt lgkmcnt(9)
	v_smfmac_f32_16x16x64_bf16 v[146:149], v[150:153], a[0:7], v223
	v_smfmac_f32_16x16x64_bf16 v[154:157], v[150:153], a[16:23], v223
	v_smfmac_f32_16x16x64_bf16 v[158:161], v[150:153], a[32:39], v223
	s_waitcnt lgkmcnt(7)
	v_smfmac_f32_16x16x64_bf16 v[162:165], v[150:153], v[182:189], v223
	v_or3_b32 v231, v150, v151, v231
	v_or3_b32 v231, v152, v153, v231
	ds_read_b128 v[182:185], v224 offset:20480
	ds_read_b128 v[186:189], v224 offset:21504
	ds_read_b128 v[150:153], v241 offset:384
	s_waitcnt lgkmcnt(9)
	v_smfmac_f32_16x16x64_bf16 v[146:149], v[194:197], a[8:15], v223
	v_smfmac_f32_16x16x64_bf16 v[154:157], v[194:197], a[24:31], v223
	v_smfmac_f32_16x16x64_bf16 v[158:161], v[194:197], a[40:47], v223
	s_waitcnt lgkmcnt(7)
	v_smfmac_f32_16x16x64_bf16 v[162:165], v[194:197], v[166:173], v223
	v_or3_b32 v231, v194, v195, v231
	v_or3_b32 v231, v196, v197, v231
	ds_read_b128 v[166:169], v224 offset:22528
	ds_read_b128 v[170:173], v224 offset:23552
	ds_read_b128 v[194:197], v242 offset:0
	s_waitcnt lgkmcnt(9)
	v_smfmac_f32_16x16x64_bf16 v[146:149], v[198:201], a[48:55], v223
	v_smfmac_f32_16x16x64_bf16 v[154:157], v[198:201], a[64:71], v223
	v_smfmac_f32_16x16x64_bf16 v[158:161], v[198:201], a[80:87], v223
	s_waitcnt lgkmcnt(7)
	v_smfmac_f32_16x16x64_bf16 v[162:165], v[198:201], v[174:181], v223
	v_or3_b32 v231, v198, v199, v231
	v_or3_b32 v231, v200, v201, v231
	ds_read_b128 v[174:177], v224 offset:24576
	ds_read_b128 v[178:181], v224 offset:25600
	ds_read_b128 v[198:201], v242 offset:256
	s_waitcnt lgkmcnt(9)
	v_smfmac_f32_16x16x64_bf16 v[146:149], v[232:235], a[96:103], v223
	v_smfmac_f32_16x16x64_bf16 v[154:157], v[232:235], a[112:119], v223
	v_smfmac_f32_16x16x64_bf16 v[158:161], v[232:235], a[128:135], v223
	s_waitcnt lgkmcnt(7)
	v_smfmac_f32_16x16x64_bf16 v[162:165], v[232:235], v[182:189], v223
	v_or3_b32 v231, v232, v233, v231
	v_or3_b32 v231, v234, v235, v231
	ds_read_b128 v[182:185], v224 offset:28672
	ds_read_b128 v[186:189], v224 offset:29696
	ds_read_b128 v[232:235], v242 offset:384
	s_waitcnt lgkmcnt(9)
	v_smfmac_f32_16x16x64_bf16 v[146:149], v[150:153], a[104:111], v223
	v_smfmac_f32_16x16x64_bf16 v[154:157], v[150:153], a[120:127], v223
	v_smfmac_f32_16x16x64_bf16 v[158:161], v[150:153], a[136:143], v223
	s_waitcnt lgkmcnt(7)
	v_smfmac_f32_16x16x64_bf16 v[162:165], v[150:153], v[166:173], v223
	v_or3_b32 v231, v150, v151, v231
	v_or3_b32 v231, v152, v153, v231
	ds_read_b128 v[166:169], v224 offset:30720
	ds_read_b128 v[170:173], v224 offset:31744
	s_waitcnt lgkmcnt(8)
	v_smfmac_f32_16x16x64_bf16 v[146:149], v[194:197], a[144:151], v223
	v_smfmac_f32_16x16x64_bf16 v[154:157], v[194:197], a[160:167], v223
	v_smfmac_f32_16x16x64_bf16 v[158:161], v[194:197], a[176:183], v223
	s_waitcnt lgkmcnt(6)
	v_smfmac_f32_16x16x64_bf16 v[162:165], v[194:197], v[174:181], v223
	v_or3_b32 v231, v194, v195, v231
	v_or3_b32 v231, v196, v197, v231
	ds_read_b128 v[174:177], v224 offset:2048
	ds_read_b128 v[178:181], v224 offset:3072
	s_waitcnt lgkmcnt(7)
	v_smfmac_f32_16x16x64_bf16 v[146:149], v[198:201], a[192:199], v223
	v_smfmac_f32_16x16x64_bf16 v[154:157], v[198:201], a[208:215], v223
	v_smfmac_f32_16x16x64_bf16 v[158:161], v[198:201], a[224:231], v223
	s_waitcnt lgkmcnt(5)
	v_smfmac_f32_16x16x64_bf16 v[162:165], v[198:201], v[182:189], v223
	v_or3_b32 v231, v198, v199, v231
	v_or3_b32 v231, v200, v201, v231
	ds_read_b128 v[182:185], v224 offset:4096
	ds_read_b128 v[186:189], v224 offset:5120
	s_waitcnt lgkmcnt(6)
	v_smfmac_f32_16x16x64_bf16 v[146:149], v[232:235], a[200:207], v223
	v_smfmac_f32_16x16x64_bf16 v[154:157], v[232:235], a[216:223], v223
	v_smfmac_f32_16x16x64_bf16 v[158:161], v[232:235], a[232:239], v223
	s_waitcnt lgkmcnt(4)
	v_smfmac_f32_16x16x64_bf16 v[162:165], v[232:235], v[166:173], v223
	v_or3_b32 v231, v232, v233, v231
	v_or3_b32 v231, v234, v235, v231
	ds_read_b128 v[166:169], v224 offset:0
	ds_read_b128 v[170:173], v224 offset:1024
	s_branch .Lj_Bend
.Lj_B2:
	ds_read_b128 v[150:153], v240 offset:256
	ds_read_b128 v[194:197], v241 offset:256
	ds_read_b128 v[198:201], v242 offset:256
	s_waitcnt lgkmcnt(2)
	v_smfmac_f32_16x16x64_bf16 v[146:149], v[150:153], a[0:7], v223
	v_smfmac_f32_16x16x64_bf16 v[154:157], v[150:153], a[16:23], v223
	v_smfmac_f32_16x16x64_bf16 v[158:161], v[150:153], a[32:39], v223
	v_smfmac_f32_16x16x64_bf16 v[162:165], v[150:153], v[174:181], v223
	v_or3_b32 v231, v150, v151, v231
	v_or3_b32 v231, v152, v153, v231
	ds_read_b128 v[174:177], v224 offset:8192
	ds_read_b128 v[178:181], v224 offset:9216
	s_barrier
	ds_read_b128 v[232:235], v240 offset:0
	ds_read_b128 v[150:153], v240 offset:128
	s_waitcnt lgkmcnt(5)
	v_smfmac_f32_16x16x64_bf16 v[146:149], v[194:197], a[96:103], v223
	v_smfmac_f32_16x16x64_bf16 v[154:157], v[194:197], a[112:119], v223
	v_smfmac_f32_16x16x64_bf16 v[158:161], v[194:197], a[128:135], v223
	v_smfmac_f32_16x16x64_bf16 v[162:165], v[194:197], v[182:189], v223
	v_or3_b32 v231, v194, v195, v231
	v_or3_b32 v231, v196, v197, v231
	ds_read_b128 v[182:185], v224 offset:10240
	ds_read_b128 v[186:189], v224 offset:11264
	ds_read_b128 v[194:197], v240 offset:384
	s_waitcnt lgkmcnt(7)
	v_smfmac_f32_16x16x64_bf16 v[146:149], v[198:201], a[192:199], v223
	v_smfmac_f32_16x16x64_bf16 v[154:157], v[198:201], a[208:215], v223
	v_smfmac_f32_16x16x64_bf16 v[158:161], v[198:201], a[224:231], v223
	v_smfmac_f32_16x16x64_bf16 v[162:165], v[198:201], v[166:173], v223
	v_or3_b32 v231, v198, v199, v231
	v_or3_b32 v231, v200, v201, v231
	ds_read_b128 v[166:169], v224 offset:14336
	ds_read_b128 v[170:173], v224 offset:15360
	ds_read_b128 v[198:201], v241 offset:0
	s_waitcnt lgkmcnt(7)
	v_smfmac_f32_16x16x64_bf16 v[146:149], v[232:235], v[98:105], v223
	v_smfmac_f32_16x16x64_bf16 v[154:157], v[232:235], v[114:121], v223
	v_smfmac_f32_16x16x64_bf16 v[158:161], v[232:235], v[130:137], v223
	v_smfmac_f32_16x16x64_bf16 v[162:165], v[232:235], v[174:181], v223
	v_or3_b32 v231, v232, v233, v231
	v_or3_b32 v231, v234, v235, v231
	ds_read_b128 v[174:177], v224 offset:16384
	ds_read_b128 v[178:181], v224 offset:17408
	ds_read_b128 v[232:235], v241 offset:128
	s_waitcnt lgkmcnt(9)
	v_smfmac_f32_16x16x64_bf16 v[146:149], v[150:153], v[106:113], v223
	v_smfmac_f32_16x16x64_bf16 v[154:157], v[150:153], v[122:129], v223
	v_smfmac_f32_16x16x64_bf16 v[158:161], v[150:153], v[138:145], v223
	s_waitcnt lgkmcnt(7)
	v_smfmac_f32_16x16x64_bf16 v[162:165], v[150:153], v[182:189], v223
	v_or3_b32 v231, v150, v151, v231
	v_or3_b32 v231, v152, v153, v231
	ds_read_b128 v[182:185], v224 offset:18432
	ds_read_b128 v[186:189], v224 offset:19456
	ds_read_b128 v[150:153], v241 offset:384
	s_waitcnt lgkmcnt(9)
	v_smfmac_f32_16x16x64_bf16 v[146:149], v[194:197], a[8:15], v223
	v_smfmac_f32_16x16x64_bf16 v[154:157], v[194:197], a[24:31], v223
	v_smfmac_f32_16x16x64_bf16 v[158:161], v[194:197], a[40:47], v223
	s_waitcnt lgkmcnt(7)
	v_smfmac_f32_16x16x64_bf16 v[162:165], v[194:197], v[166:173], v223
	v_or3_b32 v231, v194, v195, v231
	v_or3_b32 v231, v196, v197, v231
	ds_read_b128 v[166:169], v224 offset:22528
	ds_read_b128 v[170:173], v224 offset:23552
	ds_read_b128 v[194:197], v242 offset:0
	s_waitcnt lgkmcnt(9)
	v_smfmac_f32_16x16x64_bf16 v[146:149], v[198:201], a[48:55], v223
	v_smfmac_f32_16x16x64_bf16 v[154:157], v[198:201], a[64:71], v223
	v_smfmac_f32_16x16x64_bf16 v[158:161], v[198:201], a[80:87], v223
	s_waitcnt lgkmcnt(7)
	v_smfmac_f32_16x16x64_bf16 v[162:165], v[198:201], v[174:181], v223
	v_or3_b32 v231, v198, v199, v231
	v_or3_b32 v231, v200, v201, v231
	ds_read_b128 v[174:177], v224 offset:24576
	ds_read_b128 v[178:181], v224 offset:25600
	ds_read_b128 v[198:201], v242 offset:128
	s_waitcnt lgkmcnt(9)
	v_smfmac_f32_16x16x64_bf16 v[146:149], v[232:235], a[56:63], v223
	v_smfmac_f32_16x16x64_bf16 v[154:157], v[232:235], a[72:79], v223
	v_smfmac_f32_16x16x64_bf16 v[158:161], v[232:235], a[88:95], v223
	s_waitcnt lgkmcnt(7)
	v_smfmac_f32_16x16x64_bf16 v[162:165], v[232:235], v[182:189], v223
	v_or3_b32 v231, v232, v233, v231
	v_or3_b32 v231, v234, v235, v231
	ds_read_b128 v[182:185], v224 offset:26624
	ds_read_b128 v[186:189], v224 offset:27648
	ds_read_b128 v[232:235], v242 offset:384
	s_waitcnt lgkmcnt(9)
	v_smfmac_f32_16x16x64_bf16 v[146:149], v[150:153], a[104:111], v223
	v_smfmac_f32_16x16x64_bf16 v[154:157], v[150:153], a[120:127], v223
	v_smfmac_f32_16x16x64_bf16 v[158:161], v[150:153], a[136:143], v223
	s_waitcnt lgkmcnt(7)
	v_smfmac_f32_16x16x64_bf16 v[162:165], v[150:153], v[166:173], v223
	v_or3_b32 v231, v150, v151, v231
	v_or3_b32 v231, v152, v153, v231
	ds_read_b128 v[166:169], v224 offset:30720
	ds_read_b128 v[170:173], v224 offset:31744
	s_waitcnt lgkmcnt(8)
	v_smfmac_f32_16x16x64_bf16 v[146:149], v[194:197], a[144:151], v223
	v_smfmac_f32_16x16x64_bf16 v[154:157], v[194:197], a[160:167], v223
	v_smfmac_f32_16x16x64_bf16 v[158:161], v[194:197], a[176:183], v223
	s_waitcnt lgkmcnt(6)
	v_smfmac_f32_16x16x64_bf16 v[162:165], v[194:197], v[174:181], v223
	v_or3_b32 v231, v194, v195, v231
	v_or3_b32 v231, v196, v197, v231
	ds_read_b128 v[174:177], v224 offset:2048
	ds_read_b128 v[178:181], v224 offset:3072
	s_waitcnt lgkmcnt(7)
	v_smfmac_f32_16x16x64_bf16 v[146:149], v[198:201], a[152:159], v223
	v_smfmac_f32_16x16x64_bf16 v[154:157], v[198:201], a[168:175], v223
	v_smfmac_f32_16x16x64_bf16 v[158:161], v[198:201], a[184:191], v223
	s_waitcnt lgkmcnt(5)
	v_smfmac_f32_16x16x64_bf16 v[162:165], v[198:201], v[182:189], v223
	v_or3_b32 v231, v198, v199, v231
	v_or3_b32 v231, v200, v201, v231
	ds_read_b128 v[182:185], v224 offset:4096
	ds_read_b128 v[186:189], v224 offset:5120
	s_waitcnt lgkmcnt(6)
	v_smfmac_f32_16x16x64_bf16 v[146:149], v[232:235], a[200:207], v223
	v_smfmac_f32_16x16x64_bf16 v[154:157], v[232:235], a[216:223], v223
	v_smfmac_f32_16x16x64_bf16 v[158:161], v[232:235], a[232:239], v223
	s_waitcnt lgkmcnt(4)
	v_smfmac_f32_16x16x64_bf16 v[162:165], v[232:235], v[166:173], v223
	v_or3_b32 v231, v232, v233, v231
	v_or3_b32 v231, v234, v235, v231
	ds_read_b128 v[166:169], v224 offset:0
	ds_read_b128 v[170:173], v224 offset:1024
	s_branch .Lj_Bend
.Lj_B3:
	ds_read_b128 v[150:153], v240 offset:384
	ds_read_b128 v[194:197], v241 offset:384
	ds_read_b128 v[198:201], v242 offset:384
	s_waitcnt lgkmcnt(2)
	v_smfmac_f32_16x16x64_bf16 v[146:149], v[150:153], a[8:15], v223
	v_smfmac_f32_16x16x64_bf16 v[154:157], v[150:153], a[24:31], v223
	v_smfmac_f32_16x16x64_bf16 v[158:161], v[150:153], a[40:47], v223
	v_smfmac_f32_16x16x64_bf16 v[162:165], v[150:153], v[174:181], v223
	v_or3_b32 v231, v150, v151, v231
	v_or3_b32 v231, v152, v153, v231
	ds_read_b128 v[174:177], v224 offset:8192
	ds_read_b128 v[178:181], v224 offset:9216
	s_barrier
	ds_read_b128 v[232:235], v240 offset:0
	ds_read_b128 v[150:153], v240 offset:128
	s_waitcnt lgkmcnt(5)
	v_smfmac_f32_16x16x64_bf16 v[146:149], v[194:197], a[104:111], v223
	v_smfmac_f32_16x16x64_bf16 v[154:157], v[194:197], a[120:127], v223
	v_smfmac_f32_16x16x64_bf16 v[158:161], v[194:197], a[136:143], v223
	v_smfmac_f32_16x16x64_bf16 v[162:165], v[194:197], v[182:189], v223
	v_or3_b32 v231, v194, v195, v231
	v_or3_b32 v231, v196, v197, v231
	ds_read_b128 v[182:185], v224 offset:10240
	ds_read_b128 v[186:189], v224 offset:11264
	ds_read_b128 v[194:197], v240 offset:256
	s_waitcnt lgkmcnt(7)
	v_smfmac_f32_16x16x64_bf16 v[146:149], v[198:201], a[200:207], v223
	v_smfmac_f32_16x16x64_bf16 v[154:157], v[198:201], a[216:223], v223
	v_smfmac_f32_16x16x64_bf16 v[158:161], v[198:201], a[232:239], v223
	v_smfmac_f32_16x16x64_bf16 v[162:165], v[198:201], v[166:173], v223
	v_or3_b32 v231, v198, v199, v231
	v_or3_b32 v231, v200, v201, v231
	ds_read_b128 v[166:169], v224 offset:12288
	ds_read_b128 v[170:173], v224 offset:13312
	ds_read_b128 v[198:201], v241 offset:0
	s_waitcnt lgkmcnt(7)
	v_smfmac_f32_16x16x64_bf16 v[146:149], v[232:235], v[98:105], v223
	v_smfmac_f32_16x16x64_bf16 v[154:157], v[232:235], v[114:121], v223
	v_smfmac_f32_16x16x64_bf16 v[158:161], v[232:235], v[130:137], v223
	v_smfmac_f32_16x16x64_bf16 v[162:165], v[232:235], v[174:181], v223
	v_or3_b32 v231, v232, v233, v231
	v_or3_b32 v231, v234, v235, v231
	ds_read_b128 v[174:177], v224 offset:16384
	ds_read_b128 v[178:181], v224 offset:17408
	ds_read_b128 v[232:235], v241 offset:128
	s_waitcnt lgkmcnt(9)
	v_smfmac_f32_16x16x64_bf16 v[146:149], v[150:153], v[106:113], v223
	v_smfmac_f32_16x16x64_bf16 v[154:157], v[150:153], v[122:129], v223
	v_smfmac_f32_16x16x64_bf16 v[158:161], v[150:153], v[138:145], v223
	s_waitcnt lgkmcnt(7)
	v_smfmac_f32_16x16x64_bf16 v[162:165], v[150:153], v[182:189], v223
	v_or3_b32 v231, v150, v151, v231
	v_or3_b32 v231, v152, v153, v231
	ds_read_b128 v[182:185], v224 offset:18432
	ds_read_b128 v[186:189], v224 offset:19456
	ds_read_b128 v[150:153], v241 offset:256
	s_waitcnt lgkmcnt(9)
	v_smfmac_f32_16x16x64_bf16 v[146:149], v[194:197], a[0:7], v223
	v_smfmac_f32_16x16x64_bf16 v[154:157], v[194:197], a[16:23], v223
	v_smfmac_f32_16x16x64_bf16 v[158:161], v[194:197], a[32:39], v223
	s_waitcnt lgkmcnt(7)
	v_smfmac_f32_16x16x64_bf16 v[162:165], v[194:197], v[166:173], v223
	v_or3_b32 v231, v194, v195, v231
	v_or3_b32 v231, v196, v197, v231
	ds_read_b128 v[166:169], v224 offset:20480
	ds_read_b128 v[170:173], v224 offset:21504
	ds_read_b128 v[194:197], v242 offset:0
	s_waitcnt lgkmcnt(9)
	v_smfmac_f32_16x16x64_bf16 v[146:149], v[198:201], a[48:55], v223
	v_smfmac_f32_16x16x64_bf16 v[154:157], v[198:201], a[64:71], v223
	v_smfmac_f32_16x16x64_bf16 v[158:161], v[198:201], a[80:87], v223
	s_waitcnt lgkmcnt(7)
	v_smfmac_f32_16x16x64_bf16 v[162:165], v[198:201], v[174:181], v223
	v_or3_b32 v231, v198, v199, v231
	v_or3_b32 v231, v200, v201, v231
	ds_read_b128 v[174:177], v224 offset:24576
	ds_read_b128 v[178:181], v224 offset:25600
	ds_read_b128 v[198:201], v242 offset:128
	s_waitcnt lgkmcnt(9)
	v_smfmac_f32_16x16x64_bf16 v[146:149], v[232:235], a[56:63], v223
	v_smfmac_f32_16x16x64_bf16 v[154:157], v[232:235], a[72:79], v223
	v_smfmac_f32_16x16x64_bf16 v[158:161], v[232:235], a[88:95], v223
	s_waitcnt lgkmcnt(7)
	v_smfmac_f32_16x16x64_bf16 v[162:165], v[232:235], v[182:189], v223
	v_or3_b32 v231, v232, v233, v231
	v_or3_b32 v231, v234, v235, v231
	ds_read_b128 v[182:185], v224 offset:26624
	ds_read_b128 v[186:189], v224 offset:27648
	ds_read_b128 v[232:235], v242 offset:256
	s_waitcnt lgkmcnt(9)
	v_smfmac_f32_16x16x64_bf16 v[146:149], v[150:153], a[96:103], v223
	v_smfmac_f32_16x16x64_bf16 v[154:157], v[150:153], a[112:119], v223
	v_smfmac_f32_16x16x64_bf16 v[158:161], v[150:153], a[128:135], v223
	s_waitcnt lgkmcnt(7)
	v_smfmac_f32_16x16x64_bf16 v[162:165], v[150:153], v[166:173], v223
	v_or3_b32 v231, v150, v151, v231
	v_or3_b32 v231, v152, v153, v231
	ds_read_b128 v[166:169], v224 offset:28672
	ds_read_b128 v[170:173], v224 offset:29696
	s_waitcnt lgkmcnt(8)
	v_smfmac_f32_16x16x64_bf16 v[146:149], v[194:197], a[144:151], v223
	v_smfmac_f32_16x16x64_bf16 v[154:157], v[194:197], a[160:167], v223
	v_smfmac_f32_16x16x64_bf16 v[158:161], v[194:197], a[176:183], v223
	s_waitcnt lgkmcnt(6)
	v_smfmac_f32_16x16x64_bf16 v[162:165], v[194:197], v[174:181], v223
	v_or3_b32 v231, v194, v195, v231
	v_or3_b32 v231, v196, v197, v231
	ds_read_b128 v[174:177], v224 offset:2048
	ds_read_b128 v[178:181], v224 offset:3072
	s_waitcnt lgkmcnt(7)
	v_smfmac_f32_16x16x64_bf16 v[146:149], v[198:201], a[152:159], v223
	v_smfmac_f32_16x16x64_bf16 v[154:157], v[198:201], a[168:175], v223
	v_smfmac_f32_16x16x64_bf16 v[158:161], v[198:201], a[184:191], v223
	s_waitcnt lgkmcnt(5)
	v_smfmac_f32_16x16x64_bf16 v[162:165], v[198:201], v[182:189], v223
	v_or3_b32 v231, v198, v199, v231
	v_or3_b32 v231, v200, v201, v231
	ds_read_b128 v[182:185], v224 offset:4096
	ds_read_b128 v[186:189], v224 offset:5120
	s_waitcnt lgkmcnt(6)
	v_smfmac_f32_16x16x64_bf16 v[146:149], v[232:235], a[192:199], v223
	v_smfmac_f32_16x16x64_bf16 v[154:157], v[232:235], a[208:215], v223
	v_smfmac_f32_16x16x64_bf16 v[158:161], v[232:235], a[224:231], v223
	s_waitcnt lgkmcnt(4)
	v_smfmac_f32_16x16x64_bf16 v[162:165], v[232:235], v[166:173], v223
	v_or3_b32 v231, v232, v233, v231
	v_or3_b32 v231, v234, v235, v231
	ds_read_b128 v[166:169], v224 offset:0
	ds_read_b128 v[170:173], v224 offset:1024
.Lj_Bend:
	v_and_b32_e32 v231, 0x7fff7fff, v231
	v_cmp_ne_u32_e32 vcc, 0, v231
	s_nop 1
	v_pk_add_f32 v[236:237], v[146:147], v[148:149]
	v_pk_add_f32 v[238:239], v[154:155], v[156:157]
	v_pk_add_f32 v[240:241], v[158:159], v[160:161]
	v_pk_add_f32 v[146:147], v[162:163], v[164:165]
	s_cmp_eq_u64 vcc, 0
	s_cbranch_scc0 .Lj_nz
	s_cmp_lg_u32 s20, 0
	s_cbranch_scc1 .Lj_stop
